# E1 expert pre-activation item loop rewritten by hand: double-buffered software-pipelined gathers one token ahead, single f32 accumulator per expert (v_dot2 first term), saddr loads; E2 prefetch kept
# speedup vs baseline: 1.0163x; 1.0116x over previous
.LBB0_730:
	s_or_b64 exec, exec, s[24:25]
	v_mov_b32_e32 v2, s92
	s_waitcnt lgkmcnt(0)
	s_barrier
	ds_read_b32 v2, v2
	s_mov_b64 s[24:25], -1
	s_waitcnt lgkmcnt(0)
	v_readfirstlane_b32 s2, v2
	s_cmp_ge_i32 s2, s60
	s_cbranch_scc1 .LBB0_725
	s_lshl_b32 s4, s2, 6
	s_and_b32 s2, s2, 0xffffff00
	s_add_i32 s5, s2, 0x100
	s_and_b64 s[2:3], s[30:31], exec
	s_cselect_b32 s2, 0, s5
	s_add_i32 s2, s2, s4
	v_and_b32_e32 v233, 63, v0
	v_lshrrev_b32_e32 v234, 6, v0
	v_and_b32_e32 v235, 7, v0
	v_bfe_u32 v236, v0, 3, 3
	v_lshl_add_u32 v237, v234, 3, s2
	v_lshlrev_b32_e32 v218, 4, v235
	v_lshlrev_b32_e32 v219, 8, v237
	v_lshl_add_u32 v227, v233, 2, v219
	v_lshl_add_u32 v219, v236, 5, v219
	v_lshlrev_b32_e32 v226, 12, v237
	v_lshl_add_u32 v226, v235, 6, v226
	v_add_u32_e32 v226, s76, v226
	v_cmp_lt_u32_e64 s[38:39], 3, v235
	v_and_b32_e32 v238, 2, v0
	v_cmp_eq_u32_e64 s[40:41], 0, v238
	v_and_b32_e32 v238, 1, v0
	v_cmp_eq_u32_e64 s[42:43], 0, v238
	s_add_u32 s2, s96, 0x4c00000
	s_addc_u32 s3, s97, 0
	s_add_u32 s4, s96, 0x27600000
	s_addc_u32 s5, s97, 0
	s_add_u32 s4, s4, s80
	s_addc_u32 s5, s5, 0
	global_load_dwordx4 v[162:165], v219, s[22:23]
	global_load_dwordx4 v[166:169], v219, s[22:23] offset:16
	global_load_dwordx4 v[170:173], v219, s[22:23] offset:256
	global_load_dwordx4 v[174:177], v219, s[22:23] offset:272
	v_add_u32_e32 v219, 0x200, v219
	s_waitcnt vmcnt(2)
	v_and_b32_e32 v194, 0xffff, v162
	v_lshrrev_b32_e32 v195, 16, v162
	v_lshl_add_u32 v194, v194, 7, v218
	v_lshl_add_u32 v195, v195, 7, v218
	global_load_dwordx4 v[2:5], v194, s[10:11]
	global_load_dwordx4 v[6:9], v195, s[10:11]
	v_and_b32_e32 v194, 0xffff, v163
	v_lshrrev_b32_e32 v195, 16, v163
	v_lshl_add_u32 v194, v194, 7, v218
	v_lshl_add_u32 v195, v195, 7, v218
	global_load_dwordx4 v[10:13], v194, s[10:11]
	global_load_dwordx4 v[14:17], v195, s[10:11]
	v_and_b32_e32 v194, 0xffff, v164
	v_lshrrev_b32_e32 v195, 16, v164
	v_lshl_add_u32 v194, v194, 7, v218
	v_lshl_add_u32 v195, v195, 7, v218
	global_load_dwordx4 v[18:21], v194, s[10:11]
	global_load_dwordx4 v[22:25], v195, s[10:11]
	v_and_b32_e32 v194, 0xffff, v165
	v_lshrrev_b32_e32 v195, 16, v165
	v_lshl_add_u32 v194, v194, 7, v218
	v_lshl_add_u32 v195, v195, 7, v218
	global_load_dwordx4 v[26:29], v194, s[10:11]
	global_load_dwordx4 v[30:33], v195, s[10:11]
	v_and_b32_e32 v194, 0xffff, v166
	v_lshrrev_b32_e32 v195, 16, v166
	v_lshl_add_u32 v194, v194, 7, v218
	v_lshl_add_u32 v195, v195, 7, v218
	global_load_dwordx4 v[34:37], v194, s[10:11]
	global_load_dwordx4 v[38:41], v195, s[10:11]
	v_and_b32_e32 v194, 0xffff, v167
	v_lshrrev_b32_e32 v195, 16, v167
	v_lshl_add_u32 v194, v194, 7, v218
	v_lshl_add_u32 v195, v195, 7, v218
	global_load_dwordx4 v[42:45], v194, s[10:11]
	global_load_dwordx4 v[46:49], v195, s[10:11]
	v_and_b32_e32 v194, 0xffff, v168
	v_lshrrev_b32_e32 v195, 16, v168
	v_lshl_add_u32 v194, v194, 7, v218
	v_lshl_add_u32 v195, v195, 7, v218
	global_load_dwordx4 v[50:53], v194, s[10:11]
	global_load_dwordx4 v[54:57], v195, s[10:11]
	v_and_b32_e32 v194, 0xffff, v169
	v_lshrrev_b32_e32 v195, 16, v169
	v_lshl_add_u32 v194, v194, 7, v218
	v_lshl_add_u32 v195, v195, 7, v218
	global_load_dwordx4 v[58:61], v194, s[10:11]
	global_load_dwordx4 v[62:65], v195, s[10:11]
	global_load_dwordx4 v[130:133], v226, s[2:3]
	global_load_dwordx4 v[134:137], v226, s[2:3] offset:16
	global_load_dwordx4 v[138:141], v226, s[2:3] offset:32
	global_load_dwordx4 v[142:145], v226, s[2:3] offset:48
	s_mov_b32 s34, 0
	s_waitcnt vmcnt(0)
.Le1_loop:
	s_waitcnt vmcnt(1)
	v_and_b32_e32 v194, 0xffff, v170
	v_lshrrev_b32_e32 v195, 16, v170
	v_lshl_add_u32 v194, v194, 7, v218
	v_lshl_add_u32 v195, v195, 7, v218
	global_load_dwordx4 v[66:69], v194, s[10:11]
	global_load_dwordx4 v[70:73], v195, s[10:11]
	v_and_b32_e32 v194, 0xffff, v171
	v_lshrrev_b32_e32 v195, 16, v171
	v_lshl_add_u32 v194, v194, 7, v218
	v_lshl_add_u32 v195, v195, 7, v218
	global_load_dwordx4 v[74:77], v194, s[10:11]
	global_load_dwordx4 v[78:81], v195, s[10:11]
	v_and_b32_e32 v194, 0xffff, v172
	v_lshrrev_b32_e32 v195, 16, v172
	v_lshl_add_u32 v194, v194, 7, v218
	v_lshl_add_u32 v195, v195, 7, v218
	global_load_dwordx4 v[82:85], v194, s[10:11]
	global_load_dwordx4 v[86:89], v195, s[10:11]
	v_and_b32_e32 v194, 0xffff, v173
	v_lshrrev_b32_e32 v195, 16, v173
	v_lshl_add_u32 v194, v194, 7, v218
	v_lshl_add_u32 v195, v195, 7, v218
	global_load_dwordx4 v[90:93], v194, s[10:11]
	global_load_dwordx4 v[94:97], v195, s[10:11]
	v_and_b32_e32 v194, 0xffff, v174
	v_lshrrev_b32_e32 v195, 16, v174
	v_lshl_add_u32 v194, v194, 7, v218
	v_lshl_add_u32 v195, v195, 7, v218
	global_load_dwordx4 v[98:101], v194, s[10:11]
	global_load_dwordx4 v[102:105], v195, s[10:11]
	v_and_b32_e32 v194, 0xffff, v175
	v_lshrrev_b32_e32 v195, 16, v175
	v_lshl_add_u32 v194, v194, 7, v218
	v_lshl_add_u32 v195, v195, 7, v218
	global_load_dwordx4 v[106:109], v194, s[10:11]
	global_load_dwordx4 v[110:113], v195, s[10:11]
	v_and_b32_e32 v194, 0xffff, v176
	v_lshrrev_b32_e32 v195, 16, v176
	v_lshl_add_u32 v194, v194, 7, v218
	v_lshl_add_u32 v195, v195, 7, v218
	global_load_dwordx4 v[114:117], v194, s[10:11]
	global_load_dwordx4 v[118:121], v195, s[10:11]
	v_and_b32_e32 v194, 0xffff, v177
	v_lshrrev_b32_e32 v195, 16, v177
	v_lshl_add_u32 v194, v194, 7, v218
	v_lshl_add_u32 v195, v195, 7, v218
	global_load_dwordx4 v[122:125], v194, s[10:11]
	global_load_dwordx4 v[126:129], v195, s[10:11]
	v_add_u32_e32 v196, 0x1000, v226
	global_load_dwordx4 v[146:149], v196, s[2:3]
	global_load_dwordx4 v[150:153], v196, s[2:3] offset:16
	global_load_dwordx4 v[154:157], v196, s[2:3] offset:32
	global_load_dwordx4 v[158:161], v196, s[2:3] offset:48
	s_cmp_lt_u32 s34, 6
	s_cbranch_scc0 .Le1_skipA
	global_load_dwordx4 v[162:165], v219, s[22:23]
	global_load_dwordx4 v[166:169], v219, s[22:23] offset:16
.Le1_skipA:
	v_lshlrev_b32_e32 v194, 16, v130
	v_and_b32_e32 v195, 0xffff0000, v130
	v_cvt_pk_f16_f32 v130, v194, v195
	v_lshlrev_b32_e32 v194, 16, v131
	v_and_b32_e32 v195, 0xffff0000, v131
	v_cvt_pk_f16_f32 v131, v194, v195
	v_lshlrev_b32_e32 v194, 16, v132
	v_and_b32_e32 v195, 0xffff0000, v132
	v_cvt_pk_f16_f32 v132, v194, v195
	v_lshlrev_b32_e32 v194, 16, v133
	v_and_b32_e32 v195, 0xffff0000, v133
	v_cvt_pk_f16_f32 v133, v194, v195
	v_lshlrev_b32_e32 v194, 16, v134
	v_and_b32_e32 v195, 0xffff0000, v134
	v_cvt_pk_f16_f32 v134, v194, v195
	v_lshlrev_b32_e32 v194, 16, v135
	v_and_b32_e32 v195, 0xffff0000, v135
	v_cvt_pk_f16_f32 v135, v194, v195
	v_lshlrev_b32_e32 v194, 16, v136
	v_and_b32_e32 v195, 0xffff0000, v136
	v_cvt_pk_f16_f32 v136, v194, v195
	v_lshlrev_b32_e32 v194, 16, v137
	v_and_b32_e32 v195, 0xffff0000, v137
	v_cvt_pk_f16_f32 v137, v194, v195
	v_lshlrev_b32_e32 v194, 16, v138
	v_and_b32_e32 v195, 0xffff0000, v138
	v_cvt_pk_f16_f32 v138, v194, v195
	v_lshlrev_b32_e32 v194, 16, v139
	v_and_b32_e32 v195, 0xffff0000, v139
	v_cvt_pk_f16_f32 v139, v194, v195
	v_lshlrev_b32_e32 v194, 16, v140
	v_and_b32_e32 v195, 0xffff0000, v140
	v_cvt_pk_f16_f32 v140, v194, v195
	v_lshlrev_b32_e32 v194, 16, v141
	v_and_b32_e32 v195, 0xffff0000, v141
	v_cvt_pk_f16_f32 v141, v194, v195
	v_lshlrev_b32_e32 v194, 16, v142
	v_and_b32_e32 v195, 0xffff0000, v142
	v_cvt_pk_f16_f32 v142, v194, v195
	v_lshlrev_b32_e32 v194, 16, v143
	v_and_b32_e32 v195, 0xffff0000, v143
	v_cvt_pk_f16_f32 v143, v194, v195
	v_lshlrev_b32_e32 v194, 16, v144
	v_and_b32_e32 v195, 0xffff0000, v144
	v_cvt_pk_f16_f32 v144, v194, v195
	v_lshlrev_b32_e32 v194, 16, v145
	v_and_b32_e32 v195, 0xffff0000, v145
	v_cvt_pk_f16_f32 v145, v194, v195
	v_cvt_scalef32_pk_f16_fp4 v198, v2, 1.0
	v_cvt_scalef32_pk_f16_fp4 v199, v6, 1.0
	v_cvt_scalef32_pk_f16_fp4 v200, v10, 1.0
	v_cvt_scalef32_pk_f16_fp4 v201, v14, 1.0
	v_dot2_f32_f16 v178, v198, v130, 0
	v_dot2_f32_f16 v179, v199, v130, 0
	v_dot2_f32_f16 v180, v200, v130, 0
	v_dot2_f32_f16 v181, v201, v130, 0
	v_cvt_scalef32_pk_f16_fp4 v198, v2, 1.0 op_sel:[1,0,0]
	v_cvt_scalef32_pk_f16_fp4 v199, v6, 1.0 op_sel:[1,0,0]
	v_cvt_scalef32_pk_f16_fp4 v200, v10, 1.0 op_sel:[1,0,0]
	v_cvt_scalef32_pk_f16_fp4 v201, v14, 1.0 op_sel:[1,0,0]
	v_dot2c_f32_f16_e32 v178, v198, v131
	v_dot2c_f32_f16_e32 v179, v199, v131
	v_dot2c_f32_f16_e32 v180, v200, v131
	v_dot2c_f32_f16_e32 v181, v201, v131
	v_cvt_scalef32_pk_f16_fp4 v198, v2, 1.0 op_sel:[0,1,0]
	v_cvt_scalef32_pk_f16_fp4 v199, v6, 1.0 op_sel:[0,1,0]
	v_cvt_scalef32_pk_f16_fp4 v200, v10, 1.0 op_sel:[0,1,0]
	v_cvt_scalef32_pk_f16_fp4 v201, v14, 1.0 op_sel:[0,1,0]
	v_dot2c_f32_f16_e32 v178, v198, v132
	v_dot2c_f32_f16_e32 v179, v199, v132
	v_dot2c_f32_f16_e32 v180, v200, v132
	v_dot2c_f32_f16_e32 v181, v201, v132
	v_cvt_scalef32_pk_f16_fp4 v198, v2, 1.0 op_sel:[1,1,0]
	v_cvt_scalef32_pk_f16_fp4 v199, v6, 1.0 op_sel:[1,1,0]
	v_cvt_scalef32_pk_f16_fp4 v200, v10, 1.0 op_sel:[1,1,0]
	v_cvt_scalef32_pk_f16_fp4 v201, v14, 1.0 op_sel:[1,1,0]
	v_dot2c_f32_f16_e32 v178, v198, v133
	v_dot2c_f32_f16_e32 v179, v199, v133
	v_dot2c_f32_f16_e32 v180, v200, v133
	v_dot2c_f32_f16_e32 v181, v201, v133
	v_cvt_scalef32_pk_f16_fp4 v198, v3, 1.0
	v_cvt_scalef32_pk_f16_fp4 v199, v7, 1.0
	v_cvt_scalef32_pk_f16_fp4 v200, v11, 1.0
	v_cvt_scalef32_pk_f16_fp4 v201, v15, 1.0
	v_dot2c_f32_f16_e32 v178, v198, v134
	v_dot2c_f32_f16_e32 v179, v199, v134
	v_dot2c_f32_f16_e32 v180, v200, v134
	v_dot2c_f32_f16_e32 v181, v201, v134
	v_cvt_scalef32_pk_f16_fp4 v198, v3, 1.0 op_sel:[1,0,0]
	v_cvt_scalef32_pk_f16_fp4 v199, v7, 1.0 op_sel:[1,0,0]
	v_cvt_scalef32_pk_f16_fp4 v200, v11, 1.0 op_sel:[1,0,0]
	v_cvt_scalef32_pk_f16_fp4 v201, v15, 1.0 op_sel:[1,0,0]
	v_dot2c_f32_f16_e32 v178, v198, v135
	v_dot2c_f32_f16_e32 v179, v199, v135
	v_dot2c_f32_f16_e32 v180, v200, v135
	v_dot2c_f32_f16_e32 v181, v201, v135
	v_cvt_scalef32_pk_f16_fp4 v198, v3, 1.0 op_sel:[0,1,0]
	v_cvt_scalef32_pk_f16_fp4 v199, v7, 1.0 op_sel:[0,1,0]
	v_cvt_scalef32_pk_f16_fp4 v200, v11, 1.0 op_sel:[0,1,0]
	v_cvt_scalef32_pk_f16_fp4 v201, v15, 1.0 op_sel:[0,1,0]
	v_dot2c_f32_f16_e32 v178, v198, v136
	v_dot2c_f32_f16_e32 v179, v199, v136
	v_dot2c_f32_f16_e32 v180, v200, v136
	v_dot2c_f32_f16_e32 v181, v201, v136
	v_cvt_scalef32_pk_f16_fp4 v198, v3, 1.0 op_sel:[1,1,0]
	v_cvt_scalef32_pk_f16_fp4 v199, v7, 1.0 op_sel:[1,1,0]
	v_cvt_scalef32_pk_f16_fp4 v200, v11, 1.0 op_sel:[1,1,0]
	v_cvt_scalef32_pk_f16_fp4 v201, v15, 1.0 op_sel:[1,1,0]
	v_dot2c_f32_f16_e32 v178, v198, v137
	v_dot2c_f32_f16_e32 v179, v199, v137
	v_dot2c_f32_f16_e32 v180, v200, v137
	v_dot2c_f32_f16_e32 v181, v201, v137
	v_cvt_scalef32_pk_f16_fp4 v198, v4, 1.0
	v_cvt_scalef32_pk_f16_fp4 v199, v8, 1.0
	v_cvt_scalef32_pk_f16_fp4 v200, v12, 1.0
	v_cvt_scalef32_pk_f16_fp4 v201, v16, 1.0
	v_dot2c_f32_f16_e32 v178, v198, v138
	v_dot2c_f32_f16_e32 v179, v199, v138
	v_dot2c_f32_f16_e32 v180, v200, v138
	v_dot2c_f32_f16_e32 v181, v201, v138
	v_cvt_scalef32_pk_f16_fp4 v198, v4, 1.0 op_sel:[1,0,0]
	v_cvt_scalef32_pk_f16_fp4 v199, v8, 1.0 op_sel:[1,0,0]
	v_cvt_scalef32_pk_f16_fp4 v200, v12, 1.0 op_sel:[1,0,0]
	v_cvt_scalef32_pk_f16_fp4 v201, v16, 1.0 op_sel:[1,0,0]
	v_dot2c_f32_f16_e32 v178, v198, v139
	v_dot2c_f32_f16_e32 v179, v199, v139
	v_dot2c_f32_f16_e32 v180, v200, v139
	v_dot2c_f32_f16_e32 v181, v201, v139
	v_cvt_scalef32_pk_f16_fp4 v198, v4, 1.0 op_sel:[0,1,0]
	v_cvt_scalef32_pk_f16_fp4 v199, v8, 1.0 op_sel:[0,1,0]
	v_cvt_scalef32_pk_f16_fp4 v200, v12, 1.0 op_sel:[0,1,0]
	v_cvt_scalef32_pk_f16_fp4 v201, v16, 1.0 op_sel:[0,1,0]
	v_dot2c_f32_f16_e32 v178, v198, v140
	v_dot2c_f32_f16_e32 v179, v199, v140
	v_dot2c_f32_f16_e32 v180, v200, v140
	v_dot2c_f32_f16_e32 v181, v201, v140
	v_cvt_scalef32_pk_f16_fp4 v198, v4, 1.0 op_sel:[1,1,0]
	v_cvt_scalef32_pk_f16_fp4 v199, v8, 1.0 op_sel:[1,1,0]
	v_cvt_scalef32_pk_f16_fp4 v200, v12, 1.0 op_sel:[1,1,0]
	v_cvt_scalef32_pk_f16_fp4 v201, v16, 1.0 op_sel:[1,1,0]
	v_dot2c_f32_f16_e32 v178, v198, v141
	v_dot2c_f32_f16_e32 v179, v199, v141
	v_dot2c_f32_f16_e32 v180, v200, v141
	v_dot2c_f32_f16_e32 v181, v201, v141
	v_cvt_scalef32_pk_f16_fp4 v198, v5, 1.0
	v_cvt_scalef32_pk_f16_fp4 v199, v9, 1.0
	v_cvt_scalef32_pk_f16_fp4 v200, v13, 1.0
	v_cvt_scalef32_pk_f16_fp4 v201, v17, 1.0
	v_dot2c_f32_f16_e32 v178, v198, v142
	v_dot2c_f32_f16_e32 v179, v199, v142
	v_dot2c_f32_f16_e32 v180, v200, v142
	v_dot2c_f32_f16_e32 v181, v201, v142
	v_cvt_scalef32_pk_f16_fp4 v198, v5, 1.0 op_sel:[1,0,0]
	v_cvt_scalef32_pk_f16_fp4 v199, v9, 1.0 op_sel:[1,0,0]
	v_cvt_scalef32_pk_f16_fp4 v200, v13, 1.0 op_sel:[1,0,0]
	v_cvt_scalef32_pk_f16_fp4 v201, v17, 1.0 op_sel:[1,0,0]
	v_dot2c_f32_f16_e32 v178, v198, v143
	v_dot2c_f32_f16_e32 v179, v199, v143
	v_dot2c_f32_f16_e32 v180, v200, v143
	v_dot2c_f32_f16_e32 v181, v201, v143
	v_cvt_scalef32_pk_f16_fp4 v198, v5, 1.0 op_sel:[0,1,0]
	v_cvt_scalef32_pk_f16_fp4 v199, v9, 1.0 op_sel:[0,1,0]
	v_cvt_scalef32_pk_f16_fp4 v200, v13, 1.0 op_sel:[0,1,0]
	v_cvt_scalef32_pk_f16_fp4 v201, v17, 1.0 op_sel:[0,1,0]
	v_dot2c_f32_f16_e32 v178, v198, v144
	v_dot2c_f32_f16_e32 v179, v199, v144
	v_dot2c_f32_f16_e32 v180, v200, v144
	v_dot2c_f32_f16_e32 v181, v201, v144
	v_cvt_scalef32_pk_f16_fp4 v198, v5, 1.0 op_sel:[1,1,0]
	v_cvt_scalef32_pk_f16_fp4 v199, v9, 1.0 op_sel:[1,1,0]
	v_cvt_scalef32_pk_f16_fp4 v200, v13, 1.0 op_sel:[1,1,0]
	v_cvt_scalef32_pk_f16_fp4 v201, v17, 1.0 op_sel:[1,1,0]
	v_dot2c_f32_f16_e32 v178, v198, v145
	v_dot2c_f32_f16_e32 v179, v199, v145
	v_dot2c_f32_f16_e32 v180, v200, v145
	v_dot2c_f32_f16_e32 v181, v201, v145
	v_cvt_scalef32_pk_f16_fp4 v198, v18, 1.0
	v_cvt_scalef32_pk_f16_fp4 v199, v22, 1.0
	v_cvt_scalef32_pk_f16_fp4 v200, v26, 1.0
	v_cvt_scalef32_pk_f16_fp4 v201, v30, 1.0
	v_dot2_f32_f16 v182, v198, v130, 0
	v_dot2_f32_f16 v183, v199, v130, 0
	v_dot2_f32_f16 v184, v200, v130, 0
	v_dot2_f32_f16 v185, v201, v130, 0
	v_cvt_scalef32_pk_f16_fp4 v198, v18, 1.0 op_sel:[1,0,0]
	v_cvt_scalef32_pk_f16_fp4 v199, v22, 1.0 op_sel:[1,0,0]
	v_cvt_scalef32_pk_f16_fp4 v200, v26, 1.0 op_sel:[1,0,0]
	v_cvt_scalef32_pk_f16_fp4 v201, v30, 1.0 op_sel:[1,0,0]
	v_dot2c_f32_f16_e32 v182, v198, v131
	v_dot2c_f32_f16_e32 v183, v199, v131
	v_dot2c_f32_f16_e32 v184, v200, v131
	v_dot2c_f32_f16_e32 v185, v201, v131
	v_cvt_scalef32_pk_f16_fp4 v198, v18, 1.0 op_sel:[0,1,0]
	v_cvt_scalef32_pk_f16_fp4 v199, v22, 1.0 op_sel:[0,1,0]
	v_cvt_scalef32_pk_f16_fp4 v200, v26, 1.0 op_sel:[0,1,0]
	v_cvt_scalef32_pk_f16_fp4 v201, v30, 1.0 op_sel:[0,1,0]
	v_dot2c_f32_f16_e32 v182, v198, v132
	v_dot2c_f32_f16_e32 v183, v199, v132
	v_dot2c_f32_f16_e32 v184, v200, v132
	v_dot2c_f32_f16_e32 v185, v201, v132
	v_cvt_scalef32_pk_f16_fp4 v198, v18, 1.0 op_sel:[1,1,0]
	v_cvt_scalef32_pk_f16_fp4 v199, v22, 1.0 op_sel:[1,1,0]
	v_cvt_scalef32_pk_f16_fp4 v200, v26, 1.0 op_sel:[1,1,0]
	v_cvt_scalef32_pk_f16_fp4 v201, v30, 1.0 op_sel:[1,1,0]
	v_dot2c_f32_f16_e32 v182, v198, v133
	v_dot2c_f32_f16_e32 v183, v199, v133
	v_dot2c_f32_f16_e32 v184, v200, v133
	v_dot2c_f32_f16_e32 v185, v201, v133
	v_cvt_scalef32_pk_f16_fp4 v198, v19, 1.0
	v_cvt_scalef32_pk_f16_fp4 v199, v23, 1.0
	v_cvt_scalef32_pk_f16_fp4 v200, v27, 1.0
	v_cvt_scalef32_pk_f16_fp4 v201, v31, 1.0
	v_dot2c_f32_f16_e32 v182, v198, v134
	v_dot2c_f32_f16_e32 v183, v199, v134
	v_dot2c_f32_f16_e32 v184, v200, v134
	v_dot2c_f32_f16_e32 v185, v201, v134
	v_cvt_scalef32_pk_f16_fp4 v198, v19, 1.0 op_sel:[1,0,0]
	v_cvt_scalef32_pk_f16_fp4 v199, v23, 1.0 op_sel:[1,0,0]
	v_cvt_scalef32_pk_f16_fp4 v200, v27, 1.0 op_sel:[1,0,0]
	v_cvt_scalef32_pk_f16_fp4 v201, v31, 1.0 op_sel:[1,0,0]
	v_dot2c_f32_f16_e32 v182, v198, v135
	v_dot2c_f32_f16_e32 v183, v199, v135
	v_dot2c_f32_f16_e32 v184, v200, v135
	v_dot2c_f32_f16_e32 v185, v201, v135
	v_cvt_scalef32_pk_f16_fp4 v198, v19, 1.0 op_sel:[0,1,0]
	v_cvt_scalef32_pk_f16_fp4 v199, v23, 1.0 op_sel:[0,1,0]
	v_cvt_scalef32_pk_f16_fp4 v200, v27, 1.0 op_sel:[0,1,0]
	v_cvt_scalef32_pk_f16_fp4 v201, v31, 1.0 op_sel:[0,1,0]
	v_dot2c_f32_f16_e32 v182, v198, v136
	v_dot2c_f32_f16_e32 v183, v199, v136
	v_dot2c_f32_f16_e32 v184, v200, v136
	v_dot2c_f32_f16_e32 v185, v201, v136
	v_cvt_scalef32_pk_f16_fp4 v198, v19, 1.0 op_sel:[1,1,0]
	v_cvt_scalef32_pk_f16_fp4 v199, v23, 1.0 op_sel:[1,1,0]
	v_cvt_scalef32_pk_f16_fp4 v200, v27, 1.0 op_sel:[1,1,0]
	v_cvt_scalef32_pk_f16_fp4 v201, v31, 1.0 op_sel:[1,1,0]
	v_dot2c_f32_f16_e32 v182, v198, v137
	v_dot2c_f32_f16_e32 v183, v199, v137
	v_dot2c_f32_f16_e32 v184, v200, v137
	v_dot2c_f32_f16_e32 v185, v201, v137
	v_cvt_scalef32_pk_f16_fp4 v198, v20, 1.0
	v_cvt_scalef32_pk_f16_fp4 v199, v24, 1.0
	v_cvt_scalef32_pk_f16_fp4 v200, v28, 1.0
	v_cvt_scalef32_pk_f16_fp4 v201, v32, 1.0
	v_dot2c_f32_f16_e32 v182, v198, v138
	v_dot2c_f32_f16_e32 v183, v199, v138
	v_dot2c_f32_f16_e32 v184, v200, v138
	v_dot2c_f32_f16_e32 v185, v201, v138
	v_cvt_scalef32_pk_f16_fp4 v198, v20, 1.0 op_sel:[1,0,0]
	v_cvt_scalef32_pk_f16_fp4 v199, v24, 1.0 op_sel:[1,0,0]
	v_cvt_scalef32_pk_f16_fp4 v200, v28, 1.0 op_sel:[1,0,0]
	v_cvt_scalef32_pk_f16_fp4 v201, v32, 1.0 op_sel:[1,0,0]
	v_dot2c_f32_f16_e32 v182, v198, v139
	v_dot2c_f32_f16_e32 v183, v199, v139
	v_dot2c_f32_f16_e32 v184, v200, v139
	v_dot2c_f32_f16_e32 v185, v201, v139
	v_cvt_scalef32_pk_f16_fp4 v198, v20, 1.0 op_sel:[0,1,0]
	v_cvt_scalef32_pk_f16_fp4 v199, v24, 1.0 op_sel:[0,1,0]
	v_cvt_scalef32_pk_f16_fp4 v200, v28, 1.0 op_sel:[0,1,0]
	v_cvt_scalef32_pk_f16_fp4 v201, v32, 1.0 op_sel:[0,1,0]
	v_dot2c_f32_f16_e32 v182, v198, v140
	v_dot2c_f32_f16_e32 v183, v199, v140
	v_dot2c_f32_f16_e32 v184, v200, v140
	v_dot2c_f32_f16_e32 v185, v201, v140
	v_cvt_scalef32_pk_f16_fp4 v198, v20, 1.0 op_sel:[1,1,0]
	v_cvt_scalef32_pk_f16_fp4 v199, v24, 1.0 op_sel:[1,1,0]
	v_cvt_scalef32_pk_f16_fp4 v200, v28, 1.0 op_sel:[1,1,0]
	v_cvt_scalef32_pk_f16_fp4 v201, v32, 1.0 op_sel:[1,1,0]
	v_dot2c_f32_f16_e32 v182, v198, v141
	v_dot2c_f32_f16_e32 v183, v199, v141
	v_dot2c_f32_f16_e32 v184, v200, v141
	v_dot2c_f32_f16_e32 v185, v201, v141
	v_cvt_scalef32_pk_f16_fp4 v198, v21, 1.0
	v_cvt_scalef32_pk_f16_fp4 v199, v25, 1.0
	v_cvt_scalef32_pk_f16_fp4 v200, v29, 1.0
	v_cvt_scalef32_pk_f16_fp4 v201, v33, 1.0
	v_dot2c_f32_f16_e32 v182, v198, v142
	v_dot2c_f32_f16_e32 v183, v199, v142
	v_dot2c_f32_f16_e32 v184, v200, v142
	v_dot2c_f32_f16_e32 v185, v201, v142
	v_cvt_scalef32_pk_f16_fp4 v198, v21, 1.0 op_sel:[1,0,0]
	v_cvt_scalef32_pk_f16_fp4 v199, v25, 1.0 op_sel:[1,0,0]
	v_cvt_scalef32_pk_f16_fp4 v200, v29, 1.0 op_sel:[1,0,0]
	v_cvt_scalef32_pk_f16_fp4 v201, v33, 1.0 op_sel:[1,0,0]
	v_dot2c_f32_f16_e32 v182, v198, v143
	v_dot2c_f32_f16_e32 v183, v199, v143
	v_dot2c_f32_f16_e32 v184, v200, v143
	v_dot2c_f32_f16_e32 v185, v201, v143
	v_cvt_scalef32_pk_f16_fp4 v198, v21, 1.0 op_sel:[0,1,0]
	v_cvt_scalef32_pk_f16_fp4 v199, v25, 1.0 op_sel:[0,1,0]
	v_cvt_scalef32_pk_f16_fp4 v200, v29, 1.0 op_sel:[0,1,0]
	v_cvt_scalef32_pk_f16_fp4 v201, v33, 1.0 op_sel:[0,1,0]
	v_dot2c_f32_f16_e32 v182, v198, v144
	v_dot2c_f32_f16_e32 v183, v199, v144
	v_dot2c_f32_f16_e32 v184, v200, v144
	v_dot2c_f32_f16_e32 v185, v201, v144
	v_cvt_scalef32_pk_f16_fp4 v198, v21, 1.0 op_sel:[1,1,0]
	v_cvt_scalef32_pk_f16_fp4 v199, v25, 1.0 op_sel:[1,1,0]
	v_cvt_scalef32_pk_f16_fp4 v200, v29, 1.0 op_sel:[1,1,0]
	v_cvt_scalef32_pk_f16_fp4 v201, v33, 1.0 op_sel:[1,1,0]
	v_dot2c_f32_f16_e32 v182, v198, v145
	v_dot2c_f32_f16_e32 v183, v199, v145
	v_dot2c_f32_f16_e32 v184, v200, v145
	v_dot2c_f32_f16_e32 v185, v201, v145
	v_cvt_scalef32_pk_f16_fp4 v198, v34, 1.0
	v_cvt_scalef32_pk_f16_fp4 v199, v38, 1.0
	v_cvt_scalef32_pk_f16_fp4 v200, v42, 1.0
	v_cvt_scalef32_pk_f16_fp4 v201, v46, 1.0
	v_dot2_f32_f16 v186, v198, v130, 0
	v_dot2_f32_f16 v187, v199, v130, 0
	v_dot2_f32_f16 v188, v200, v130, 0
	v_dot2_f32_f16 v189, v201, v130, 0
	v_cvt_scalef32_pk_f16_fp4 v198, v34, 1.0 op_sel:[1,0,0]
	v_cvt_scalef32_pk_f16_fp4 v199, v38, 1.0 op_sel:[1,0,0]
	v_cvt_scalef32_pk_f16_fp4 v200, v42, 1.0 op_sel:[1,0,0]
	v_cvt_scalef32_pk_f16_fp4 v201, v46, 1.0 op_sel:[1,0,0]
	v_dot2c_f32_f16_e32 v186, v198, v131
	v_dot2c_f32_f16_e32 v187, v199, v131
	v_dot2c_f32_f16_e32 v188, v200, v131
	v_dot2c_f32_f16_e32 v189, v201, v131
	v_cvt_scalef32_pk_f16_fp4 v198, v34, 1.0 op_sel:[0,1,0]
	v_cvt_scalef32_pk_f16_fp4 v199, v38, 1.0 op_sel:[0,1,0]
	v_cvt_scalef32_pk_f16_fp4 v200, v42, 1.0 op_sel:[0,1,0]
	v_cvt_scalef32_pk_f16_fp4 v201, v46, 1.0 op_sel:[0,1,0]
	v_dot2c_f32_f16_e32 v186, v198, v132
	v_dot2c_f32_f16_e32 v187, v199, v132
	v_dot2c_f32_f16_e32 v188, v200, v132
	v_dot2c_f32_f16_e32 v189, v201, v132
	v_cvt_scalef32_pk_f16_fp4 v198, v34, 1.0 op_sel:[1,1,0]
	v_cvt_scalef32_pk_f16_fp4 v199, v38, 1.0 op_sel:[1,1,0]
	v_cvt_scalef32_pk_f16_fp4 v200, v42, 1.0 op_sel:[1,1,0]
	v_cvt_scalef32_pk_f16_fp4 v201, v46, 1.0 op_sel:[1,1,0]
	v_dot2c_f32_f16_e32 v186, v198, v133
	v_dot2c_f32_f16_e32 v187, v199, v133
	v_dot2c_f32_f16_e32 v188, v200, v133
	v_dot2c_f32_f16_e32 v189, v201, v133
	v_cvt_scalef32_pk_f16_fp4 v198, v35, 1.0
	v_cvt_scalef32_pk_f16_fp4 v199, v39, 1.0
	v_cvt_scalef32_pk_f16_fp4 v200, v43, 1.0
	v_cvt_scalef32_pk_f16_fp4 v201, v47, 1.0
	v_dot2c_f32_f16_e32 v186, v198, v134
	v_dot2c_f32_f16_e32 v187, v199, v134
	v_dot2c_f32_f16_e32 v188, v200, v134
	v_dot2c_f32_f16_e32 v189, v201, v134
	v_cvt_scalef32_pk_f16_fp4 v198, v35, 1.0 op_sel:[1,0,0]
	v_cvt_scalef32_pk_f16_fp4 v199, v39, 1.0 op_sel:[1,0,0]
	v_cvt_scalef32_pk_f16_fp4 v200, v43, 1.0 op_sel:[1,0,0]
	v_cvt_scalef32_pk_f16_fp4 v201, v47, 1.0 op_sel:[1,0,0]
	v_dot2c_f32_f16_e32 v186, v198, v135
	v_dot2c_f32_f16_e32 v187, v199, v135
	v_dot2c_f32_f16_e32 v188, v200, v135
	v_dot2c_f32_f16_e32 v189, v201, v135
	v_cvt_scalef32_pk_f16_fp4 v198, v35, 1.0 op_sel:[0,1,0]
	v_cvt_scalef32_pk_f16_fp4 v199, v39, 1.0 op_sel:[0,1,0]
	v_cvt_scalef32_pk_f16_fp4 v200, v43, 1.0 op_sel:[0,1,0]
	v_cvt_scalef32_pk_f16_fp4 v201, v47, 1.0 op_sel:[0,1,0]
	v_dot2c_f32_f16_e32 v186, v198, v136
	v_dot2c_f32_f16_e32 v187, v199, v136
	v_dot2c_f32_f16_e32 v188, v200, v136
	v_dot2c_f32_f16_e32 v189, v201, v136
	v_cvt_scalef32_pk_f16_fp4 v198, v35, 1.0 op_sel:[1,1,0]
	v_cvt_scalef32_pk_f16_fp4 v199, v39, 1.0 op_sel:[1,1,0]
	v_cvt_scalef32_pk_f16_fp4 v200, v43, 1.0 op_sel:[1,1,0]
	v_cvt_scalef32_pk_f16_fp4 v201, v47, 1.0 op_sel:[1,1,0]
	v_dot2c_f32_f16_e32 v186, v198, v137
	v_dot2c_f32_f16_e32 v187, v199, v137
	v_dot2c_f32_f16_e32 v188, v200, v137
	v_dot2c_f32_f16_e32 v189, v201, v137
	v_cvt_scalef32_pk_f16_fp4 v198, v36, 1.0
	v_cvt_scalef32_pk_f16_fp4 v199, v40, 1.0
	v_cvt_scalef32_pk_f16_fp4 v200, v44, 1.0
	v_cvt_scalef32_pk_f16_fp4 v201, v48, 1.0
	v_dot2c_f32_f16_e32 v186, v198, v138
	v_dot2c_f32_f16_e32 v187, v199, v138
	v_dot2c_f32_f16_e32 v188, v200, v138
	v_dot2c_f32_f16_e32 v189, v201, v138
	v_cvt_scalef32_pk_f16_fp4 v198, v36, 1.0 op_sel:[1,0,0]
	v_cvt_scalef32_pk_f16_fp4 v199, v40, 1.0 op_sel:[1,0,0]
	v_cvt_scalef32_pk_f16_fp4 v200, v44, 1.0 op_sel:[1,0,0]
	v_cvt_scalef32_pk_f16_fp4 v201, v48, 1.0 op_sel:[1,0,0]
	v_dot2c_f32_f16_e32 v186, v198, v139
	v_dot2c_f32_f16_e32 v187, v199, v139
	v_dot2c_f32_f16_e32 v188, v200, v139
	v_dot2c_f32_f16_e32 v189, v201, v139
	v_cvt_scalef32_pk_f16_fp4 v198, v36, 1.0 op_sel:[0,1,0]
	v_cvt_scalef32_pk_f16_fp4 v199, v40, 1.0 op_sel:[0,1,0]
	v_cvt_scalef32_pk_f16_fp4 v200, v44, 1.0 op_sel:[0,1,0]
	v_cvt_scalef32_pk_f16_fp4 v201, v48, 1.0 op_sel:[0,1,0]
	v_dot2c_f32_f16_e32 v186, v198, v140
	v_dot2c_f32_f16_e32 v187, v199, v140
	v_dot2c_f32_f16_e32 v188, v200, v140
	v_dot2c_f32_f16_e32 v189, v201, v140
	v_cvt_scalef32_pk_f16_fp4 v198, v36, 1.0 op_sel:[1,1,0]
	v_cvt_scalef32_pk_f16_fp4 v199, v40, 1.0 op_sel:[1,1,0]
	v_cvt_scalef32_pk_f16_fp4 v200, v44, 1.0 op_sel:[1,1,0]
	v_cvt_scalef32_pk_f16_fp4 v201, v48, 1.0 op_sel:[1,1,0]
	v_dot2c_f32_f16_e32 v186, v198, v141
	v_dot2c_f32_f16_e32 v187, v199, v141
	v_dot2c_f32_f16_e32 v188, v200, v141
	v_dot2c_f32_f16_e32 v189, v201, v141
	v_cvt_scalef32_pk_f16_fp4 v198, v37, 1.0
	v_cvt_scalef32_pk_f16_fp4 v199, v41, 1.0
	v_cvt_scalef32_pk_f16_fp4 v200, v45, 1.0
	v_cvt_scalef32_pk_f16_fp4 v201, v49, 1.0
	v_dot2c_f32_f16_e32 v186, v198, v142
	v_dot2c_f32_f16_e32 v187, v199, v142
	v_dot2c_f32_f16_e32 v188, v200, v142
	v_dot2c_f32_f16_e32 v189, v201, v142
	v_cvt_scalef32_pk_f16_fp4 v198, v37, 1.0 op_sel:[1,0,0]
	v_cvt_scalef32_pk_f16_fp4 v199, v41, 1.0 op_sel:[1,0,0]
	v_cvt_scalef32_pk_f16_fp4 v200, v45, 1.0 op_sel:[1,0,0]
	v_cvt_scalef32_pk_f16_fp4 v201, v49, 1.0 op_sel:[1,0,0]
	v_dot2c_f32_f16_e32 v186, v198, v143
	v_dot2c_f32_f16_e32 v187, v199, v143
	v_dot2c_f32_f16_e32 v188, v200, v143
	v_dot2c_f32_f16_e32 v189, v201, v143
	v_cvt_scalef32_pk_f16_fp4 v198, v37, 1.0 op_sel:[0,1,0]
	v_cvt_scalef32_pk_f16_fp4 v199, v41, 1.0 op_sel:[0,1,0]
	v_cvt_scalef32_pk_f16_fp4 v200, v45, 1.0 op_sel:[0,1,0]
	v_cvt_scalef32_pk_f16_fp4 v201, v49, 1.0 op_sel:[0,1,0]
	v_dot2c_f32_f16_e32 v186, v198, v144
	v_dot2c_f32_f16_e32 v187, v199, v144
	v_dot2c_f32_f16_e32 v188, v200, v144
	v_dot2c_f32_f16_e32 v189, v201, v144
	v_cvt_scalef32_pk_f16_fp4 v198, v37, 1.0 op_sel:[1,1,0]
	v_cvt_scalef32_pk_f16_fp4 v199, v41, 1.0 op_sel:[1,1,0]
	v_cvt_scalef32_pk_f16_fp4 v200, v45, 1.0 op_sel:[1,1,0]
	v_cvt_scalef32_pk_f16_fp4 v201, v49, 1.0 op_sel:[1,1,0]
	v_dot2c_f32_f16_e32 v186, v198, v145
	v_dot2c_f32_f16_e32 v187, v199, v145
	v_dot2c_f32_f16_e32 v188, v200, v145
	v_dot2c_f32_f16_e32 v189, v201, v145
	v_cvt_scalef32_pk_f16_fp4 v198, v50, 1.0
	v_cvt_scalef32_pk_f16_fp4 v199, v54, 1.0
	v_cvt_scalef32_pk_f16_fp4 v200, v58, 1.0
	v_cvt_scalef32_pk_f16_fp4 v201, v62, 1.0
	v_dot2_f32_f16 v190, v198, v130, 0
	v_dot2_f32_f16 v191, v199, v130, 0
	v_dot2_f32_f16 v192, v200, v130, 0
	v_dot2_f32_f16 v193, v201, v130, 0
	v_cvt_scalef32_pk_f16_fp4 v198, v50, 1.0 op_sel:[1,0,0]
	v_cvt_scalef32_pk_f16_fp4 v199, v54, 1.0 op_sel:[1,0,0]
	v_cvt_scalef32_pk_f16_fp4 v200, v58, 1.0 op_sel:[1,0,0]
	v_cvt_scalef32_pk_f16_fp4 v201, v62, 1.0 op_sel:[1,0,0]
	v_dot2c_f32_f16_e32 v190, v198, v131
	v_dot2c_f32_f16_e32 v191, v199, v131
	v_dot2c_f32_f16_e32 v192, v200, v131
	v_dot2c_f32_f16_e32 v193, v201, v131
	v_cvt_scalef32_pk_f16_fp4 v198, v50, 1.0 op_sel:[0,1,0]
	v_cvt_scalef32_pk_f16_fp4 v199, v54, 1.0 op_sel:[0,1,0]
	v_cvt_scalef32_pk_f16_fp4 v200, v58, 1.0 op_sel:[0,1,0]
	v_cvt_scalef32_pk_f16_fp4 v201, v62, 1.0 op_sel:[0,1,0]
	v_dot2c_f32_f16_e32 v190, v198, v132
	v_dot2c_f32_f16_e32 v191, v199, v132
	v_dot2c_f32_f16_e32 v192, v200, v132
	v_dot2c_f32_f16_e32 v193, v201, v132
	v_cvt_scalef32_pk_f16_fp4 v198, v50, 1.0 op_sel:[1,1,0]
	v_cvt_scalef32_pk_f16_fp4 v199, v54, 1.0 op_sel:[1,1,0]
	v_cvt_scalef32_pk_f16_fp4 v200, v58, 1.0 op_sel:[1,1,0]
	v_cvt_scalef32_pk_f16_fp4 v201, v62, 1.0 op_sel:[1,1,0]
	v_dot2c_f32_f16_e32 v190, v198, v133
	v_dot2c_f32_f16_e32 v191, v199, v133
	v_dot2c_f32_f16_e32 v192, v200, v133
	v_dot2c_f32_f16_e32 v193, v201, v133
	v_cvt_scalef32_pk_f16_fp4 v198, v51, 1.0
	v_cvt_scalef32_pk_f16_fp4 v199, v55, 1.0
	v_cvt_scalef32_pk_f16_fp4 v200, v59, 1.0
	v_cvt_scalef32_pk_f16_fp4 v201, v63, 1.0
	v_dot2c_f32_f16_e32 v190, v198, v134
	v_dot2c_f32_f16_e32 v191, v199, v134
	v_dot2c_f32_f16_e32 v192, v200, v134
	v_dot2c_f32_f16_e32 v193, v201, v134
	v_cvt_scalef32_pk_f16_fp4 v198, v51, 1.0 op_sel:[1,0,0]
	v_cvt_scalef32_pk_f16_fp4 v199, v55, 1.0 op_sel:[1,0,0]
	v_cvt_scalef32_pk_f16_fp4 v200, v59, 1.0 op_sel:[1,0,0]
	v_cvt_scalef32_pk_f16_fp4 v201, v63, 1.0 op_sel:[1,0,0]
	v_dot2c_f32_f16_e32 v190, v198, v135
	v_dot2c_f32_f16_e32 v191, v199, v135
	v_dot2c_f32_f16_e32 v192, v200, v135
	v_dot2c_f32_f16_e32 v193, v201, v135
	v_cvt_scalef32_pk_f16_fp4 v198, v51, 1.0 op_sel:[0,1,0]
	v_cvt_scalef32_pk_f16_fp4 v199, v55, 1.0 op_sel:[0,1,0]
	v_cvt_scalef32_pk_f16_fp4 v200, v59, 1.0 op_sel:[0,1,0]
	v_cvt_scalef32_pk_f16_fp4 v201, v63, 1.0 op_sel:[0,1,0]
	v_dot2c_f32_f16_e32 v190, v198, v136
	v_dot2c_f32_f16_e32 v191, v199, v136
	v_dot2c_f32_f16_e32 v192, v200, v136
	v_dot2c_f32_f16_e32 v193, v201, v136
	v_cvt_scalef32_pk_f16_fp4 v198, v51, 1.0 op_sel:[1,1,0]
	v_cvt_scalef32_pk_f16_fp4 v199, v55, 1.0 op_sel:[1,1,0]
	v_cvt_scalef32_pk_f16_fp4 v200, v59, 1.0 op_sel:[1,1,0]
	v_cvt_scalef32_pk_f16_fp4 v201, v63, 1.0 op_sel:[1,1,0]
	v_dot2c_f32_f16_e32 v190, v198, v137
	v_dot2c_f32_f16_e32 v191, v199, v137
	v_dot2c_f32_f16_e32 v192, v200, v137
	v_dot2c_f32_f16_e32 v193, v201, v137
	v_cvt_scalef32_pk_f16_fp4 v198, v52, 1.0
	v_cvt_scalef32_pk_f16_fp4 v199, v56, 1.0
	v_cvt_scalef32_pk_f16_fp4 v200, v60, 1.0
	v_cvt_scalef32_pk_f16_fp4 v201, v64, 1.0
	v_dot2c_f32_f16_e32 v190, v198, v138
	v_dot2c_f32_f16_e32 v191, v199, v138
	v_dot2c_f32_f16_e32 v192, v200, v138
	v_dot2c_f32_f16_e32 v193, v201, v138
	v_cvt_scalef32_pk_f16_fp4 v198, v52, 1.0 op_sel:[1,0,0]
	v_cvt_scalef32_pk_f16_fp4 v199, v56, 1.0 op_sel:[1,0,0]
	v_cvt_scalef32_pk_f16_fp4 v200, v60, 1.0 op_sel:[1,0,0]
	v_cvt_scalef32_pk_f16_fp4 v201, v64, 1.0 op_sel:[1,0,0]
	v_dot2c_f32_f16_e32 v190, v198, v139
	v_dot2c_f32_f16_e32 v191, v199, v139
	v_dot2c_f32_f16_e32 v192, v200, v139
	v_dot2c_f32_f16_e32 v193, v201, v139
	v_cvt_scalef32_pk_f16_fp4 v198, v52, 1.0 op_sel:[0,1,0]
	v_cvt_scalef32_pk_f16_fp4 v199, v56, 1.0 op_sel:[0,1,0]
	v_cvt_scalef32_pk_f16_fp4 v200, v60, 1.0 op_sel:[0,1,0]
	v_cvt_scalef32_pk_f16_fp4 v201, v64, 1.0 op_sel:[0,1,0]
	v_dot2c_f32_f16_e32 v190, v198, v140
	v_dot2c_f32_f16_e32 v191, v199, v140
	v_dot2c_f32_f16_e32 v192, v200, v140
	v_dot2c_f32_f16_e32 v193, v201, v140
	v_cvt_scalef32_pk_f16_fp4 v198, v52, 1.0 op_sel:[1,1,0]
	v_cvt_scalef32_pk_f16_fp4 v199, v56, 1.0 op_sel:[1,1,0]
	v_cvt_scalef32_pk_f16_fp4 v200, v60, 1.0 op_sel:[1,1,0]
	v_cvt_scalef32_pk_f16_fp4 v201, v64, 1.0 op_sel:[1,1,0]
	v_dot2c_f32_f16_e32 v190, v198, v141
	v_dot2c_f32_f16_e32 v191, v199, v141
	v_dot2c_f32_f16_e32 v192, v200, v141
	v_dot2c_f32_f16_e32 v193, v201, v141
	v_cvt_scalef32_pk_f16_fp4 v198, v53, 1.0
	v_cvt_scalef32_pk_f16_fp4 v199, v57, 1.0
	v_cvt_scalef32_pk_f16_fp4 v200, v61, 1.0
	v_cvt_scalef32_pk_f16_fp4 v201, v65, 1.0
	v_dot2c_f32_f16_e32 v190, v198, v142
	v_dot2c_f32_f16_e32 v191, v199, v142
	v_dot2c_f32_f16_e32 v192, v200, v142
	v_dot2c_f32_f16_e32 v193, v201, v142
	v_cvt_scalef32_pk_f16_fp4 v198, v53, 1.0 op_sel:[1,0,0]
	v_cvt_scalef32_pk_f16_fp4 v199, v57, 1.0 op_sel:[1,0,0]
	v_cvt_scalef32_pk_f16_fp4 v200, v61, 1.0 op_sel:[1,0,0]
	v_cvt_scalef32_pk_f16_fp4 v201, v65, 1.0 op_sel:[1,0,0]
	v_dot2c_f32_f16_e32 v190, v198, v143
	v_dot2c_f32_f16_e32 v191, v199, v143
	v_dot2c_f32_f16_e32 v192, v200, v143
	v_dot2c_f32_f16_e32 v193, v201, v143
	v_cvt_scalef32_pk_f16_fp4 v198, v53, 1.0 op_sel:[0,1,0]
	v_cvt_scalef32_pk_f16_fp4 v199, v57, 1.0 op_sel:[0,1,0]
	v_cvt_scalef32_pk_f16_fp4 v200, v61, 1.0 op_sel:[0,1,0]
	v_cvt_scalef32_pk_f16_fp4 v201, v65, 1.0 op_sel:[0,1,0]
	v_dot2c_f32_f16_e32 v190, v198, v144
	v_dot2c_f32_f16_e32 v191, v199, v144
	v_dot2c_f32_f16_e32 v192, v200, v144
	v_dot2c_f32_f16_e32 v193, v201, v144
	v_cvt_scalef32_pk_f16_fp4 v198, v53, 1.0 op_sel:[1,1,0]
	v_cvt_scalef32_pk_f16_fp4 v199, v57, 1.0 op_sel:[1,1,0]
	v_cvt_scalef32_pk_f16_fp4 v200, v61, 1.0 op_sel:[1,1,0]
	v_cvt_scalef32_pk_f16_fp4 v201, v65, 1.0 op_sel:[1,1,0]
	v_dot2c_f32_f16_e32 v190, v198, v145
	v_dot2c_f32_f16_e32 v191, v199, v145
	v_dot2c_f32_f16_e32 v192, v200, v145
	v_dot2c_f32_f16_e32 v193, v201, v145
	s_nop 3
	v_cndmask_b32_e64 v194, v178, v186, s[38:39]
	v_cndmask_b32_e64 v233, v186, v178, s[38:39]
	v_cndmask_b32_e64 v195, v179, v187, s[38:39]
	v_cndmask_b32_e64 v234, v187, v179, s[38:39]
	v_cndmask_b32_e64 v196, v180, v188, s[38:39]
	v_cndmask_b32_e64 v235, v188, v180, s[38:39]
	v_cndmask_b32_e64 v197, v181, v189, s[38:39]
	v_cndmask_b32_e64 v236, v189, v181, s[38:39]
	v_cndmask_b32_e64 v198, v182, v190, s[38:39]
	v_cndmask_b32_e64 v237, v190, v182, s[38:39]
	v_cndmask_b32_e64 v199, v183, v191, s[38:39]
	v_cndmask_b32_e64 v238, v191, v183, s[38:39]
	v_cndmask_b32_e64 v200, v184, v192, s[38:39]
	v_cndmask_b32_e64 v239, v192, v184, s[38:39]
	v_cndmask_b32_e64 v201, v185, v193, s[38:39]
	v_cndmask_b32_e64 v240, v193, v185, s[38:39]
	v_add_f32_dpp v241, v233, v194 row_half_mirror row_mask:0xf bank_mask:0xf bound_ctrl:1
	v_add_f32_dpp v242, v234, v195 row_half_mirror row_mask:0xf bank_mask:0xf bound_ctrl:1
	v_add_f32_dpp v243, v235, v196 row_half_mirror row_mask:0xf bank_mask:0xf bound_ctrl:1
	v_add_f32_dpp v244, v236, v197 row_half_mirror row_mask:0xf bank_mask:0xf bound_ctrl:1
	v_add_f32_dpp v245, v237, v198 row_half_mirror row_mask:0xf bank_mask:0xf bound_ctrl:1
	v_add_f32_dpp v246, v238, v199 row_half_mirror row_mask:0xf bank_mask:0xf bound_ctrl:1
	v_add_f32_dpp v247, v239, v200 row_half_mirror row_mask:0xf bank_mask:0xf bound_ctrl:1
	v_add_f32_dpp v248, v240, v201 row_half_mirror row_mask:0xf bank_mask:0xf bound_ctrl:1
	v_cndmask_b32_e64 v194, v245, v241, s[40:41]
	v_cndmask_b32_e64 v233, v241, v245, s[40:41]
	v_cndmask_b32_e64 v195, v246, v242, s[40:41]
	v_cndmask_b32_e64 v234, v242, v246, s[40:41]
	v_cndmask_b32_e64 v196, v247, v243, s[40:41]
	v_cndmask_b32_e64 v235, v243, v247, s[40:41]
	v_cndmask_b32_e64 v197, v248, v244, s[40:41]
	v_cndmask_b32_e64 v236, v244, v248, s[40:41]
	v_add_f32_dpp v178, v233, v194 quad_perm:[2,3,0,1] row_mask:0xf bank_mask:0xf bound_ctrl:1
	v_add_f32_dpp v179, v234, v195 quad_perm:[2,3,0,1] row_mask:0xf bank_mask:0xf bound_ctrl:1
	v_add_f32_dpp v180, v235, v196 quad_perm:[2,3,0,1] row_mask:0xf bank_mask:0xf bound_ctrl:1
	v_add_f32_dpp v181, v236, v197 quad_perm:[2,3,0,1] row_mask:0xf bank_mask:0xf bound_ctrl:1
	v_cndmask_b32_e64 v194, v180, v178, s[42:43]
	v_cndmask_b32_e64 v233, v178, v180, s[42:43]
	v_cndmask_b32_e64 v195, v181, v179, s[42:43]
	v_cndmask_b32_e64 v234, v179, v181, s[42:43]
	s_nop 1
	v_add_f32_dpp v196, v233, v194 quad_perm:[1,0,3,2] row_mask:0xf bank_mask:0xf bound_ctrl:1
	v_add_f32_dpp v197, v234, v195 quad_perm:[1,0,3,2] row_mask:0xf bank_mask:0xf bound_ctrl:1
	v_cvt_pk_bf16_f32 v198, v196, v197
	global_store_dword v227, v198, s[4:5]
	s_waitcnt vmcnt(1)
	s_cmp_lt_u32 s34, 6
	s_cbranch_scc0 .Le1_skipB
	v_and_b32_e32 v194, 0xffff, v162
	v_lshrrev_b32_e32 v195, 16, v162
	v_lshl_add_u32 v194, v194, 7, v218
	v_lshl_add_u32 v195, v195, 7, v218
	global_load_dwordx4 v[2:5], v194, s[10:11]
	global_load_dwordx4 v[6:9], v195, s[10:11]
	v_and_b32_e32 v194, 0xffff, v163
	v_lshrrev_b32_e32 v195, 16, v163
	v_lshl_add_u32 v194, v194, 7, v218
	v_lshl_add_u32 v195, v195, 7, v218
	global_load_dwordx4 v[10:13], v194, s[10:11]
	global_load_dwordx4 v[14:17], v195, s[10:11]
	v_and_b32_e32 v194, 0xffff, v164
	v_lshrrev_b32_e32 v195, 16, v164
	v_lshl_add_u32 v194, v194, 7, v218
	v_lshl_add_u32 v195, v195, 7, v218
	global_load_dwordx4 v[18:21], v194, s[10:11]
	global_load_dwordx4 v[22:25], v195, s[10:11]
	v_and_b32_e32 v194, 0xffff, v165
	v_lshrrev_b32_e32 v195, 16, v165
	v_lshl_add_u32 v194, v194, 7, v218
	v_lshl_add_u32 v195, v195, 7, v218
	global_load_dwordx4 v[26:29], v194, s[10:11]
	global_load_dwordx4 v[30:33], v195, s[10:11]
	v_and_b32_e32 v194, 0xffff, v166
	v_lshrrev_b32_e32 v195, 16, v166
	v_lshl_add_u32 v194, v194, 7, v218
	v_lshl_add_u32 v195, v195, 7, v218
	global_load_dwordx4 v[34:37], v194, s[10:11]
	global_load_dwordx4 v[38:41], v195, s[10:11]
	v_and_b32_e32 v194, 0xffff, v167
	v_lshrrev_b32_e32 v195, 16, v167
	v_lshl_add_u32 v194, v194, 7, v218
	v_lshl_add_u32 v195, v195, 7, v218
	global_load_dwordx4 v[42:45], v194, s[10:11]
	global_load_dwordx4 v[46:49], v195, s[10:11]
	v_and_b32_e32 v194, 0xffff, v168
	v_lshrrev_b32_e32 v195, 16, v168
	v_lshl_add_u32 v194, v194, 7, v218
	v_lshl_add_u32 v195, v195, 7, v218
	global_load_dwordx4 v[50:53], v194, s[10:11]
	global_load_dwordx4 v[54:57], v195, s[10:11]
	v_and_b32_e32 v194, 0xffff, v169
	v_lshrrev_b32_e32 v195, 16, v169
	v_lshl_add_u32 v194, v194, 7, v218
	v_lshl_add_u32 v195, v195, 7, v218
	global_load_dwordx4 v[58:61], v194, s[10:11]
	global_load_dwordx4 v[62:65], v195, s[10:11]
	v_add_u32_e32 v196, 0x2000, v226
	global_load_dwordx4 v[130:133], v196, s[2:3]
	global_load_dwordx4 v[134:137], v196, s[2:3] offset:16
	global_load_dwordx4 v[138:141], v196, s[2:3] offset:32
	global_load_dwordx4 v[142:145], v196, s[2:3] offset:48
	global_load_dwordx4 v[170:173], v219, s[22:23] offset:256
	global_load_dwordx4 v[174:177], v219, s[22:23] offset:272
	v_add_u32_e32 v219, 0x200, v219
.Le1_skipB:
	v_lshlrev_b32_e32 v194, 16, v146
	v_and_b32_e32 v195, 0xffff0000, v146
	v_cvt_pk_f16_f32 v146, v194, v195
	v_lshlrev_b32_e32 v194, 16, v147
	v_and_b32_e32 v195, 0xffff0000, v147
	v_cvt_pk_f16_f32 v147, v194, v195
	v_lshlrev_b32_e32 v194, 16, v148
	v_and_b32_e32 v195, 0xffff0000, v148
	v_cvt_pk_f16_f32 v148, v194, v195
	v_lshlrev_b32_e32 v194, 16, v149
	v_and_b32_e32 v195, 0xffff0000, v149
	v_cvt_pk_f16_f32 v149, v194, v195
	v_lshlrev_b32_e32 v194, 16, v150
	v_and_b32_e32 v195, 0xffff0000, v150
	v_cvt_pk_f16_f32 v150, v194, v195
	v_lshlrev_b32_e32 v194, 16, v151
	v_and_b32_e32 v195, 0xffff0000, v151
	v_cvt_pk_f16_f32 v151, v194, v195
	v_lshlrev_b32_e32 v194, 16, v152
	v_and_b32_e32 v195, 0xffff0000, v152
	v_cvt_pk_f16_f32 v152, v194, v195
	v_lshlrev_b32_e32 v194, 16, v153
	v_and_b32_e32 v195, 0xffff0000, v153
	v_cvt_pk_f16_f32 v153, v194, v195
	v_lshlrev_b32_e32 v194, 16, v154
	v_and_b32_e32 v195, 0xffff0000, v154
	v_cvt_pk_f16_f32 v154, v194, v195
	v_lshlrev_b32_e32 v194, 16, v155
	v_and_b32_e32 v195, 0xffff0000, v155
	v_cvt_pk_f16_f32 v155, v194, v195
	v_lshlrev_b32_e32 v194, 16, v156
	v_and_b32_e32 v195, 0xffff0000, v156
	v_cvt_pk_f16_f32 v156, v194, v195
	v_lshlrev_b32_e32 v194, 16, v157
	v_and_b32_e32 v195, 0xffff0000, v157
	v_cvt_pk_f16_f32 v157, v194, v195
	v_lshlrev_b32_e32 v194, 16, v158
	v_and_b32_e32 v195, 0xffff0000, v158
	v_cvt_pk_f16_f32 v158, v194, v195
	v_lshlrev_b32_e32 v194, 16, v159
	v_and_b32_e32 v195, 0xffff0000, v159
	v_cvt_pk_f16_f32 v159, v194, v195
	v_lshlrev_b32_e32 v194, 16, v160
	v_and_b32_e32 v195, 0xffff0000, v160
	v_cvt_pk_f16_f32 v160, v194, v195
	v_lshlrev_b32_e32 v194, 16, v161
	v_and_b32_e32 v195, 0xffff0000, v161
	v_cvt_pk_f16_f32 v161, v194, v195
	v_cvt_scalef32_pk_f16_fp4 v198, v66, 1.0
	v_cvt_scalef32_pk_f16_fp4 v199, v70, 1.0
	v_cvt_scalef32_pk_f16_fp4 v200, v74, 1.0
	v_cvt_scalef32_pk_f16_fp4 v201, v78, 1.0
	v_dot2_f32_f16 v178, v198, v146, 0
	v_dot2_f32_f16 v179, v199, v146, 0
	v_dot2_f32_f16 v180, v200, v146, 0
	v_dot2_f32_f16 v181, v201, v146, 0
	v_cvt_scalef32_pk_f16_fp4 v198, v66, 1.0 op_sel:[1,0,0]
	v_cvt_scalef32_pk_f16_fp4 v199, v70, 1.0 op_sel:[1,0,0]
	v_cvt_scalef32_pk_f16_fp4 v200, v74, 1.0 op_sel:[1,0,0]
	v_cvt_scalef32_pk_f16_fp4 v201, v78, 1.0 op_sel:[1,0,0]
	v_dot2c_f32_f16_e32 v178, v198, v147
	v_dot2c_f32_f16_e32 v179, v199, v147
	v_dot2c_f32_f16_e32 v180, v200, v147
	v_dot2c_f32_f16_e32 v181, v201, v147
	v_cvt_scalef32_pk_f16_fp4 v198, v66, 1.0 op_sel:[0,1,0]
	v_cvt_scalef32_pk_f16_fp4 v199, v70, 1.0 op_sel:[0,1,0]
	v_cvt_scalef32_pk_f16_fp4 v200, v74, 1.0 op_sel:[0,1,0]
	v_cvt_scalef32_pk_f16_fp4 v201, v78, 1.0 op_sel:[0,1,0]
	v_dot2c_f32_f16_e32 v178, v198, v148
	v_dot2c_f32_f16_e32 v179, v199, v148
	v_dot2c_f32_f16_e32 v180, v200, v148
	v_dot2c_f32_f16_e32 v181, v201, v148
	v_cvt_scalef32_pk_f16_fp4 v198, v66, 1.0 op_sel:[1,1,0]
	v_cvt_scalef32_pk_f16_fp4 v199, v70, 1.0 op_sel:[1,1,0]
	v_cvt_scalef32_pk_f16_fp4 v200, v74, 1.0 op_sel:[1,1,0]
	v_cvt_scalef32_pk_f16_fp4 v201, v78, 1.0 op_sel:[1,1,0]
	v_dot2c_f32_f16_e32 v178, v198, v149
	v_dot2c_f32_f16_e32 v179, v199, v149
	v_dot2c_f32_f16_e32 v180, v200, v149
	v_dot2c_f32_f16_e32 v181, v201, v149
	v_cvt_scalef32_pk_f16_fp4 v198, v67, 1.0
	v_cvt_scalef32_pk_f16_fp4 v199, v71, 1.0
	v_cvt_scalef32_pk_f16_fp4 v200, v75, 1.0
	v_cvt_scalef32_pk_f16_fp4 v201, v79, 1.0
	v_dot2c_f32_f16_e32 v178, v198, v150
	v_dot2c_f32_f16_e32 v179, v199, v150
	v_dot2c_f32_f16_e32 v180, v200, v150
	v_dot2c_f32_f16_e32 v181, v201, v150
	v_cvt_scalef32_pk_f16_fp4 v198, v67, 1.0 op_sel:[1,0,0]
	v_cvt_scalef32_pk_f16_fp4 v199, v71, 1.0 op_sel:[1,0,0]
	v_cvt_scalef32_pk_f16_fp4 v200, v75, 1.0 op_sel:[1,0,0]
	v_cvt_scalef32_pk_f16_fp4 v201, v79, 1.0 op_sel:[1,0,0]
	v_dot2c_f32_f16_e32 v178, v198, v151
	v_dot2c_f32_f16_e32 v179, v199, v151
	v_dot2c_f32_f16_e32 v180, v200, v151
	v_dot2c_f32_f16_e32 v181, v201, v151
	v_cvt_scalef32_pk_f16_fp4 v198, v67, 1.0 op_sel:[0,1,0]
	v_cvt_scalef32_pk_f16_fp4 v199, v71, 1.0 op_sel:[0,1,0]
	v_cvt_scalef32_pk_f16_fp4 v200, v75, 1.0 op_sel:[0,1,0]
	v_cvt_scalef32_pk_f16_fp4 v201, v79, 1.0 op_sel:[0,1,0]
	v_dot2c_f32_f16_e32 v178, v198, v152
	v_dot2c_f32_f16_e32 v179, v199, v152
	v_dot2c_f32_f16_e32 v180, v200, v152
	v_dot2c_f32_f16_e32 v181, v201, v152
	v_cvt_scalef32_pk_f16_fp4 v198, v67, 1.0 op_sel:[1,1,0]
	v_cvt_scalef32_pk_f16_fp4 v199, v71, 1.0 op_sel:[1,1,0]
	v_cvt_scalef32_pk_f16_fp4 v200, v75, 1.0 op_sel:[1,1,0]
	v_cvt_scalef32_pk_f16_fp4 v201, v79, 1.0 op_sel:[1,1,0]
	v_dot2c_f32_f16_e32 v178, v198, v153
	v_dot2c_f32_f16_e32 v179, v199, v153
	v_dot2c_f32_f16_e32 v180, v200, v153
	v_dot2c_f32_f16_e32 v181, v201, v153
	v_cvt_scalef32_pk_f16_fp4 v198, v68, 1.0
	v_cvt_scalef32_pk_f16_fp4 v199, v72, 1.0
	v_cvt_scalef32_pk_f16_fp4 v200, v76, 1.0
	v_cvt_scalef32_pk_f16_fp4 v201, v80, 1.0
	v_dot2c_f32_f16_e32 v178, v198, v154
	v_dot2c_f32_f16_e32 v179, v199, v154
	v_dot2c_f32_f16_e32 v180, v200, v154
	v_dot2c_f32_f16_e32 v181, v201, v154
	v_cvt_scalef32_pk_f16_fp4 v198, v68, 1.0 op_sel:[1,0,0]
	v_cvt_scalef32_pk_f16_fp4 v199, v72, 1.0 op_sel:[1,0,0]
	v_cvt_scalef32_pk_f16_fp4 v200, v76, 1.0 op_sel:[1,0,0]
	v_cvt_scalef32_pk_f16_fp4 v201, v80, 1.0 op_sel:[1,0,0]
	v_dot2c_f32_f16_e32 v178, v198, v155
	v_dot2c_f32_f16_e32 v179, v199, v155
	v_dot2c_f32_f16_e32 v180, v200, v155
	v_dot2c_f32_f16_e32 v181, v201, v155
	v_cvt_scalef32_pk_f16_fp4 v198, v68, 1.0 op_sel:[0,1,0]
	v_cvt_scalef32_pk_f16_fp4 v199, v72, 1.0 op_sel:[0,1,0]
	v_cvt_scalef32_pk_f16_fp4 v200, v76, 1.0 op_sel:[0,1,0]
	v_cvt_scalef32_pk_f16_fp4 v201, v80, 1.0 op_sel:[0,1,0]
	v_dot2c_f32_f16_e32 v178, v198, v156
	v_dot2c_f32_f16_e32 v179, v199, v156
	v_dot2c_f32_f16_e32 v180, v200, v156
	v_dot2c_f32_f16_e32 v181, v201, v156
	v_cvt_scalef32_pk_f16_fp4 v198, v68, 1.0 op_sel:[1,1,0]
	v_cvt_scalef32_pk_f16_fp4 v199, v72, 1.0 op_sel:[1,1,0]
	v_cvt_scalef32_pk_f16_fp4 v200, v76, 1.0 op_sel:[1,1,0]
	v_cvt_scalef32_pk_f16_fp4 v201, v80, 1.0 op_sel:[1,1,0]
	v_dot2c_f32_f16_e32 v178, v198, v157
	v_dot2c_f32_f16_e32 v179, v199, v157
	v_dot2c_f32_f16_e32 v180, v200, v157
	v_dot2c_f32_f16_e32 v181, v201, v157
	v_cvt_scalef32_pk_f16_fp4 v198, v69, 1.0
	v_cvt_scalef32_pk_f16_fp4 v199, v73, 1.0
	v_cvt_scalef32_pk_f16_fp4 v200, v77, 1.0
	v_cvt_scalef32_pk_f16_fp4 v201, v81, 1.0
	v_dot2c_f32_f16_e32 v178, v198, v158
	v_dot2c_f32_f16_e32 v179, v199, v158
	v_dot2c_f32_f16_e32 v180, v200, v158
	v_dot2c_f32_f16_e32 v181, v201, v158
	v_cvt_scalef32_pk_f16_fp4 v198, v69, 1.0 op_sel:[1,0,0]
	v_cvt_scalef32_pk_f16_fp4 v199, v73, 1.0 op_sel:[1,0,0]
	v_cvt_scalef32_pk_f16_fp4 v200, v77, 1.0 op_sel:[1,0,0]
	v_cvt_scalef32_pk_f16_fp4 v201, v81, 1.0 op_sel:[1,0,0]
	v_dot2c_f32_f16_e32 v178, v198, v159
	v_dot2c_f32_f16_e32 v179, v199, v159
	v_dot2c_f32_f16_e32 v180, v200, v159
	v_dot2c_f32_f16_e32 v181, v201, v159
	v_cvt_scalef32_pk_f16_fp4 v198, v69, 1.0 op_sel:[0,1,0]
	v_cvt_scalef32_pk_f16_fp4 v199, v73, 1.0 op_sel:[0,1,0]
	v_cvt_scalef32_pk_f16_fp4 v200, v77, 1.0 op_sel:[0,1,0]
	v_cvt_scalef32_pk_f16_fp4 v201, v81, 1.0 op_sel:[0,1,0]
	v_dot2c_f32_f16_e32 v178, v198, v160
	v_dot2c_f32_f16_e32 v179, v199, v160
	v_dot2c_f32_f16_e32 v180, v200, v160
	v_dot2c_f32_f16_e32 v181, v201, v160
	v_cvt_scalef32_pk_f16_fp4 v198, v69, 1.0 op_sel:[1,1,0]
	v_cvt_scalef32_pk_f16_fp4 v199, v73, 1.0 op_sel:[1,1,0]
	v_cvt_scalef32_pk_f16_fp4 v200, v77, 1.0 op_sel:[1,1,0]
	v_cvt_scalef32_pk_f16_fp4 v201, v81, 1.0 op_sel:[1,1,0]
	v_dot2c_f32_f16_e32 v178, v198, v161
	v_dot2c_f32_f16_e32 v179, v199, v161
	v_dot2c_f32_f16_e32 v180, v200, v161
	v_dot2c_f32_f16_e32 v181, v201, v161
	v_cvt_scalef32_pk_f16_fp4 v198, v82, 1.0
	v_cvt_scalef32_pk_f16_fp4 v199, v86, 1.0
	v_cvt_scalef32_pk_f16_fp4 v200, v90, 1.0
	v_cvt_scalef32_pk_f16_fp4 v201, v94, 1.0
	v_dot2_f32_f16 v182, v198, v146, 0
	v_dot2_f32_f16 v183, v199, v146, 0
	v_dot2_f32_f16 v184, v200, v146, 0
	v_dot2_f32_f16 v185, v201, v146, 0
	v_cvt_scalef32_pk_f16_fp4 v198, v82, 1.0 op_sel:[1,0,0]
	v_cvt_scalef32_pk_f16_fp4 v199, v86, 1.0 op_sel:[1,0,0]
	v_cvt_scalef32_pk_f16_fp4 v200, v90, 1.0 op_sel:[1,0,0]
	v_cvt_scalef32_pk_f16_fp4 v201, v94, 1.0 op_sel:[1,0,0]
	v_dot2c_f32_f16_e32 v182, v198, v147
	v_dot2c_f32_f16_e32 v183, v199, v147
	v_dot2c_f32_f16_e32 v184, v200, v147
	v_dot2c_f32_f16_e32 v185, v201, v147
	v_cvt_scalef32_pk_f16_fp4 v198, v82, 1.0 op_sel:[0,1,0]
	v_cvt_scalef32_pk_f16_fp4 v199, v86, 1.0 op_sel:[0,1,0]
	v_cvt_scalef32_pk_f16_fp4 v200, v90, 1.0 op_sel:[0,1,0]
	v_cvt_scalef32_pk_f16_fp4 v201, v94, 1.0 op_sel:[0,1,0]
	v_dot2c_f32_f16_e32 v182, v198, v148
	v_dot2c_f32_f16_e32 v183, v199, v148
	v_dot2c_f32_f16_e32 v184, v200, v148
	v_dot2c_f32_f16_e32 v185, v201, v148
	v_cvt_scalef32_pk_f16_fp4 v198, v82, 1.0 op_sel:[1,1,0]
	v_cvt_scalef32_pk_f16_fp4 v199, v86, 1.0 op_sel:[1,1,0]
	v_cvt_scalef32_pk_f16_fp4 v200, v90, 1.0 op_sel:[1,1,0]
	v_cvt_scalef32_pk_f16_fp4 v201, v94, 1.0 op_sel:[1,1,0]
	v_dot2c_f32_f16_e32 v182, v198, v149
	v_dot2c_f32_f16_e32 v183, v199, v149
	v_dot2c_f32_f16_e32 v184, v200, v149
	v_dot2c_f32_f16_e32 v185, v201, v149
	v_cvt_scalef32_pk_f16_fp4 v198, v83, 1.0
	v_cvt_scalef32_pk_f16_fp4 v199, v87, 1.0
	v_cvt_scalef32_pk_f16_fp4 v200, v91, 1.0
	v_cvt_scalef32_pk_f16_fp4 v201, v95, 1.0
	v_dot2c_f32_f16_e32 v182, v198, v150
	v_dot2c_f32_f16_e32 v183, v199, v150
	v_dot2c_f32_f16_e32 v184, v200, v150
	v_dot2c_f32_f16_e32 v185, v201, v150
	v_cvt_scalef32_pk_f16_fp4 v198, v83, 1.0 op_sel:[1,0,0]
	v_cvt_scalef32_pk_f16_fp4 v199, v87, 1.0 op_sel:[1,0,0]
	v_cvt_scalef32_pk_f16_fp4 v200, v91, 1.0 op_sel:[1,0,0]
	v_cvt_scalef32_pk_f16_fp4 v201, v95, 1.0 op_sel:[1,0,0]
	v_dot2c_f32_f16_e32 v182, v198, v151
	v_dot2c_f32_f16_e32 v183, v199, v151
	v_dot2c_f32_f16_e32 v184, v200, v151
	v_dot2c_f32_f16_e32 v185, v201, v151
	v_cvt_scalef32_pk_f16_fp4 v198, v83, 1.0 op_sel:[0,1,0]
	v_cvt_scalef32_pk_f16_fp4 v199, v87, 1.0 op_sel:[0,1,0]
	v_cvt_scalef32_pk_f16_fp4 v200, v91, 1.0 op_sel:[0,1,0]
	v_cvt_scalef32_pk_f16_fp4 v201, v95, 1.0 op_sel:[0,1,0]
	v_dot2c_f32_f16_e32 v182, v198, v152
	v_dot2c_f32_f16_e32 v183, v199, v152
	v_dot2c_f32_f16_e32 v184, v200, v152
	v_dot2c_f32_f16_e32 v185, v201, v152
	v_cvt_scalef32_pk_f16_fp4 v198, v83, 1.0 op_sel:[1,1,0]
	v_cvt_scalef32_pk_f16_fp4 v199, v87, 1.0 op_sel:[1,1,0]
	v_cvt_scalef32_pk_f16_fp4 v200, v91, 1.0 op_sel:[1,1,0]
	v_cvt_scalef32_pk_f16_fp4 v201, v95, 1.0 op_sel:[1,1,0]
	v_dot2c_f32_f16_e32 v182, v198, v153
	v_dot2c_f32_f16_e32 v183, v199, v153
	v_dot2c_f32_f16_e32 v184, v200, v153
	v_dot2c_f32_f16_e32 v185, v201, v153
	v_cvt_scalef32_pk_f16_fp4 v198, v84, 1.0
	v_cvt_scalef32_pk_f16_fp4 v199, v88, 1.0
	v_cvt_scalef32_pk_f16_fp4 v200, v92, 1.0
	v_cvt_scalef32_pk_f16_fp4 v201, v96, 1.0
	v_dot2c_f32_f16_e32 v182, v198, v154
	v_dot2c_f32_f16_e32 v183, v199, v154
	v_dot2c_f32_f16_e32 v184, v200, v154
	v_dot2c_f32_f16_e32 v185, v201, v154
	v_cvt_scalef32_pk_f16_fp4 v198, v84, 1.0 op_sel:[1,0,0]
	v_cvt_scalef32_pk_f16_fp4 v199, v88, 1.0 op_sel:[1,0,0]
	v_cvt_scalef32_pk_f16_fp4 v200, v92, 1.0 op_sel:[1,0,0]
	v_cvt_scalef32_pk_f16_fp4 v201, v96, 1.0 op_sel:[1,0,0]
	v_dot2c_f32_f16_e32 v182, v198, v155
	v_dot2c_f32_f16_e32 v183, v199, v155
	v_dot2c_f32_f16_e32 v184, v200, v155
	v_dot2c_f32_f16_e32 v185, v201, v155
	v_cvt_scalef32_pk_f16_fp4 v198, v84, 1.0 op_sel:[0,1,0]
	v_cvt_scalef32_pk_f16_fp4 v199, v88, 1.0 op_sel:[0,1,0]
	v_cvt_scalef32_pk_f16_fp4 v200, v92, 1.0 op_sel:[0,1,0]
	v_cvt_scalef32_pk_f16_fp4 v201, v96, 1.0 op_sel:[0,1,0]
	v_dot2c_f32_f16_e32 v182, v198, v156
	v_dot2c_f32_f16_e32 v183, v199, v156
	v_dot2c_f32_f16_e32 v184, v200, v156
	v_dot2c_f32_f16_e32 v185, v201, v156
	v_cvt_scalef32_pk_f16_fp4 v198, v84, 1.0 op_sel:[1,1,0]
	v_cvt_scalef32_pk_f16_fp4 v199, v88, 1.0 op_sel:[1,1,0]
	v_cvt_scalef32_pk_f16_fp4 v200, v92, 1.0 op_sel:[1,1,0]
	v_cvt_scalef32_pk_f16_fp4 v201, v96, 1.0 op_sel:[1,1,0]
	v_dot2c_f32_f16_e32 v182, v198, v157
	v_dot2c_f32_f16_e32 v183, v199, v157
	v_dot2c_f32_f16_e32 v184, v200, v157
	v_dot2c_f32_f16_e32 v185, v201, v157
	v_cvt_scalef32_pk_f16_fp4 v198, v85, 1.0
	v_cvt_scalef32_pk_f16_fp4 v199, v89, 1.0
	v_cvt_scalef32_pk_f16_fp4 v200, v93, 1.0
	v_cvt_scalef32_pk_f16_fp4 v201, v97, 1.0
	v_dot2c_f32_f16_e32 v182, v198, v158
	v_dot2c_f32_f16_e32 v183, v199, v158
	v_dot2c_f32_f16_e32 v184, v200, v158
	v_dot2c_f32_f16_e32 v185, v201, v158
	v_cvt_scalef32_pk_f16_fp4 v198, v85, 1.0 op_sel:[1,0,0]
	v_cvt_scalef32_pk_f16_fp4 v199, v89, 1.0 op_sel:[1,0,0]
	v_cvt_scalef32_pk_f16_fp4 v200, v93, 1.0 op_sel:[1,0,0]
	v_cvt_scalef32_pk_f16_fp4 v201, v97, 1.0 op_sel:[1,0,0]
	v_dot2c_f32_f16_e32 v182, v198, v159
	v_dot2c_f32_f16_e32 v183, v199, v159
	v_dot2c_f32_f16_e32 v184, v200, v159
	v_dot2c_f32_f16_e32 v185, v201, v159
	v_cvt_scalef32_pk_f16_fp4 v198, v85, 1.0 op_sel:[0,1,0]
	v_cvt_scalef32_pk_f16_fp4 v199, v89, 1.0 op_sel:[0,1,0]
	v_cvt_scalef32_pk_f16_fp4 v200, v93, 1.0 op_sel:[0,1,0]
	v_cvt_scalef32_pk_f16_fp4 v201, v97, 1.0 op_sel:[0,1,0]
	v_dot2c_f32_f16_e32 v182, v198, v160
	v_dot2c_f32_f16_e32 v183, v199, v160
	v_dot2c_f32_f16_e32 v184, v200, v160
	v_dot2c_f32_f16_e32 v185, v201, v160
	v_cvt_scalef32_pk_f16_fp4 v198, v85, 1.0 op_sel:[1,1,0]
	v_cvt_scalef32_pk_f16_fp4 v199, v89, 1.0 op_sel:[1,1,0]
	v_cvt_scalef32_pk_f16_fp4 v200, v93, 1.0 op_sel:[1,1,0]
	v_cvt_scalef32_pk_f16_fp4 v201, v97, 1.0 op_sel:[1,1,0]
	v_dot2c_f32_f16_e32 v182, v198, v161
	v_dot2c_f32_f16_e32 v183, v199, v161
	v_dot2c_f32_f16_e32 v184, v200, v161
	v_dot2c_f32_f16_e32 v185, v201, v161
	v_cvt_scalef32_pk_f16_fp4 v198, v98, 1.0
	v_cvt_scalef32_pk_f16_fp4 v199, v102, 1.0
	v_cvt_scalef32_pk_f16_fp4 v200, v106, 1.0
	v_cvt_scalef32_pk_f16_fp4 v201, v110, 1.0
	v_dot2_f32_f16 v186, v198, v146, 0
	v_dot2_f32_f16 v187, v199, v146, 0
	v_dot2_f32_f16 v188, v200, v146, 0
	v_dot2_f32_f16 v189, v201, v146, 0
	v_cvt_scalef32_pk_f16_fp4 v198, v98, 1.0 op_sel:[1,0,0]
	v_cvt_scalef32_pk_f16_fp4 v199, v102, 1.0 op_sel:[1,0,0]
	v_cvt_scalef32_pk_f16_fp4 v200, v106, 1.0 op_sel:[1,0,0]
	v_cvt_scalef32_pk_f16_fp4 v201, v110, 1.0 op_sel:[1,0,0]
	v_dot2c_f32_f16_e32 v186, v198, v147
	v_dot2c_f32_f16_e32 v187, v199, v147
	v_dot2c_f32_f16_e32 v188, v200, v147
	v_dot2c_f32_f16_e32 v189, v201, v147
	v_cvt_scalef32_pk_f16_fp4 v198, v98, 1.0 op_sel:[0,1,0]
	v_cvt_scalef32_pk_f16_fp4 v199, v102, 1.0 op_sel:[0,1,0]
	v_cvt_scalef32_pk_f16_fp4 v200, v106, 1.0 op_sel:[0,1,0]
	v_cvt_scalef32_pk_f16_fp4 v201, v110, 1.0 op_sel:[0,1,0]
	v_dot2c_f32_f16_e32 v186, v198, v148
	v_dot2c_f32_f16_e32 v187, v199, v148
	v_dot2c_f32_f16_e32 v188, v200, v148
	v_dot2c_f32_f16_e32 v189, v201, v148
	v_cvt_scalef32_pk_f16_fp4 v198, v98, 1.0 op_sel:[1,1,0]
	v_cvt_scalef32_pk_f16_fp4 v199, v102, 1.0 op_sel:[1,1,0]
	v_cvt_scalef32_pk_f16_fp4 v200, v106, 1.0 op_sel:[1,1,0]
	v_cvt_scalef32_pk_f16_fp4 v201, v110, 1.0 op_sel:[1,1,0]
	v_dot2c_f32_f16_e32 v186, v198, v149
	v_dot2c_f32_f16_e32 v187, v199, v149
	v_dot2c_f32_f16_e32 v188, v200, v149
	v_dot2c_f32_f16_e32 v189, v201, v149
	v_cvt_scalef32_pk_f16_fp4 v198, v99, 1.0
	v_cvt_scalef32_pk_f16_fp4 v199, v103, 1.0
	v_cvt_scalef32_pk_f16_fp4 v200, v107, 1.0
	v_cvt_scalef32_pk_f16_fp4 v201, v111, 1.0
	v_dot2c_f32_f16_e32 v186, v198, v150
	v_dot2c_f32_f16_e32 v187, v199, v150
	v_dot2c_f32_f16_e32 v188, v200, v150
	v_dot2c_f32_f16_e32 v189, v201, v150
	v_cvt_scalef32_pk_f16_fp4 v198, v99, 1.0 op_sel:[1,0,0]
	v_cvt_scalef32_pk_f16_fp4 v199, v103, 1.0 op_sel:[1,0,0]
	v_cvt_scalef32_pk_f16_fp4 v200, v107, 1.0 op_sel:[1,0,0]
	v_cvt_scalef32_pk_f16_fp4 v201, v111, 1.0 op_sel:[1,0,0]
	v_dot2c_f32_f16_e32 v186, v198, v151
	v_dot2c_f32_f16_e32 v187, v199, v151
	v_dot2c_f32_f16_e32 v188, v200, v151
	v_dot2c_f32_f16_e32 v189, v201, v151
	v_cvt_scalef32_pk_f16_fp4 v198, v99, 1.0 op_sel:[0,1,0]
	v_cvt_scalef32_pk_f16_fp4 v199, v103, 1.0 op_sel:[0,1,0]
	v_cvt_scalef32_pk_f16_fp4 v200, v107, 1.0 op_sel:[0,1,0]
	v_cvt_scalef32_pk_f16_fp4 v201, v111, 1.0 op_sel:[0,1,0]
	v_dot2c_f32_f16_e32 v186, v198, v152
	v_dot2c_f32_f16_e32 v187, v199, v152
	v_dot2c_f32_f16_e32 v188, v200, v152
	v_dot2c_f32_f16_e32 v189, v201, v152
	v_cvt_scalef32_pk_f16_fp4 v198, v99, 1.0 op_sel:[1,1,0]
	v_cvt_scalef32_pk_f16_fp4 v199, v103, 1.0 op_sel:[1,1,0]
	v_cvt_scalef32_pk_f16_fp4 v200, v107, 1.0 op_sel:[1,1,0]
	v_cvt_scalef32_pk_f16_fp4 v201, v111, 1.0 op_sel:[1,1,0]
	v_dot2c_f32_f16_e32 v186, v198, v153
	v_dot2c_f32_f16_e32 v187, v199, v153
	v_dot2c_f32_f16_e32 v188, v200, v153
	v_dot2c_f32_f16_e32 v189, v201, v153
	v_cvt_scalef32_pk_f16_fp4 v198, v100, 1.0
	v_cvt_scalef32_pk_f16_fp4 v199, v104, 1.0
	v_cvt_scalef32_pk_f16_fp4 v200, v108, 1.0
	v_cvt_scalef32_pk_f16_fp4 v201, v112, 1.0
	v_dot2c_f32_f16_e32 v186, v198, v154
	v_dot2c_f32_f16_e32 v187, v199, v154
	v_dot2c_f32_f16_e32 v188, v200, v154
	v_dot2c_f32_f16_e32 v189, v201, v154
	v_cvt_scalef32_pk_f16_fp4 v198, v100, 1.0 op_sel:[1,0,0]
	v_cvt_scalef32_pk_f16_fp4 v199, v104, 1.0 op_sel:[1,0,0]
	v_cvt_scalef32_pk_f16_fp4 v200, v108, 1.0 op_sel:[1,0,0]
	v_cvt_scalef32_pk_f16_fp4 v201, v112, 1.0 op_sel:[1,0,0]
	v_dot2c_f32_f16_e32 v186, v198, v155
	v_dot2c_f32_f16_e32 v187, v199, v155
	v_dot2c_f32_f16_e32 v188, v200, v155
	v_dot2c_f32_f16_e32 v189, v201, v155
	v_cvt_scalef32_pk_f16_fp4 v198, v100, 1.0 op_sel:[0,1,0]
	v_cvt_scalef32_pk_f16_fp4 v199, v104, 1.0 op_sel:[0,1,0]
	v_cvt_scalef32_pk_f16_fp4 v200, v108, 1.0 op_sel:[0,1,0]
	v_cvt_scalef32_pk_f16_fp4 v201, v112, 1.0 op_sel:[0,1,0]
	v_dot2c_f32_f16_e32 v186, v198, v156
	v_dot2c_f32_f16_e32 v187, v199, v156
	v_dot2c_f32_f16_e32 v188, v200, v156
	v_dot2c_f32_f16_e32 v189, v201, v156
	v_cvt_scalef32_pk_f16_fp4 v198, v100, 1.0 op_sel:[1,1,0]
	v_cvt_scalef32_pk_f16_fp4 v199, v104, 1.0 op_sel:[1,1,0]
	v_cvt_scalef32_pk_f16_fp4 v200, v108, 1.0 op_sel:[1,1,0]
	v_cvt_scalef32_pk_f16_fp4 v201, v112, 1.0 op_sel:[1,1,0]
	v_dot2c_f32_f16_e32 v186, v198, v157
	v_dot2c_f32_f16_e32 v187, v199, v157
	v_dot2c_f32_f16_e32 v188, v200, v157
	v_dot2c_f32_f16_e32 v189, v201, v157
	v_cvt_scalef32_pk_f16_fp4 v198, v101, 1.0
	v_cvt_scalef32_pk_f16_fp4 v199, v105, 1.0
	v_cvt_scalef32_pk_f16_fp4 v200, v109, 1.0
	v_cvt_scalef32_pk_f16_fp4 v201, v113, 1.0
	v_dot2c_f32_f16_e32 v186, v198, v158
	v_dot2c_f32_f16_e32 v187, v199, v158
	v_dot2c_f32_f16_e32 v188, v200, v158
	v_dot2c_f32_f16_e32 v189, v201, v158
	v_cvt_scalef32_pk_f16_fp4 v198, v101, 1.0 op_sel:[1,0,0]
	v_cvt_scalef32_pk_f16_fp4 v199, v105, 1.0 op_sel:[1,0,0]
	v_cvt_scalef32_pk_f16_fp4 v200, v109, 1.0 op_sel:[1,0,0]
	v_cvt_scalef32_pk_f16_fp4 v201, v113, 1.0 op_sel:[1,0,0]
	v_dot2c_f32_f16_e32 v186, v198, v159
	v_dot2c_f32_f16_e32 v187, v199, v159
	v_dot2c_f32_f16_e32 v188, v200, v159
	v_dot2c_f32_f16_e32 v189, v201, v159
	v_cvt_scalef32_pk_f16_fp4 v198, v101, 1.0 op_sel:[0,1,0]
	v_cvt_scalef32_pk_f16_fp4 v199, v105, 1.0 op_sel:[0,1,0]
	v_cvt_scalef32_pk_f16_fp4 v200, v109, 1.0 op_sel:[0,1,0]
	v_cvt_scalef32_pk_f16_fp4 v201, v113, 1.0 op_sel:[0,1,0]
	v_dot2c_f32_f16_e32 v186, v198, v160
	v_dot2c_f32_f16_e32 v187, v199, v160
	v_dot2c_f32_f16_e32 v188, v200, v160
	v_dot2c_f32_f16_e32 v189, v201, v160
	v_cvt_scalef32_pk_f16_fp4 v198, v101, 1.0 op_sel:[1,1,0]
	v_cvt_scalef32_pk_f16_fp4 v199, v105, 1.0 op_sel:[1,1,0]
	v_cvt_scalef32_pk_f16_fp4 v200, v109, 1.0 op_sel:[1,1,0]
	v_cvt_scalef32_pk_f16_fp4 v201, v113, 1.0 op_sel:[1,1,0]
	v_dot2c_f32_f16_e32 v186, v198, v161
	v_dot2c_f32_f16_e32 v187, v199, v161
	v_dot2c_f32_f16_e32 v188, v200, v161
	v_dot2c_f32_f16_e32 v189, v201, v161
	v_cvt_scalef32_pk_f16_fp4 v198, v114, 1.0
	v_cvt_scalef32_pk_f16_fp4 v199, v118, 1.0
	v_cvt_scalef32_pk_f16_fp4 v200, v122, 1.0
	v_cvt_scalef32_pk_f16_fp4 v201, v126, 1.0
	v_dot2_f32_f16 v190, v198, v146, 0
	v_dot2_f32_f16 v191, v199, v146, 0
	v_dot2_f32_f16 v192, v200, v146, 0
	v_dot2_f32_f16 v193, v201, v146, 0
	v_cvt_scalef32_pk_f16_fp4 v198, v114, 1.0 op_sel:[1,0,0]
	v_cvt_scalef32_pk_f16_fp4 v199, v118, 1.0 op_sel:[1,0,0]
	v_cvt_scalef32_pk_f16_fp4 v200, v122, 1.0 op_sel:[1,0,0]
	v_cvt_scalef32_pk_f16_fp4 v201, v126, 1.0 op_sel:[1,0,0]
	v_dot2c_f32_f16_e32 v190, v198, v147
	v_dot2c_f32_f16_e32 v191, v199, v147
	v_dot2c_f32_f16_e32 v192, v200, v147
	v_dot2c_f32_f16_e32 v193, v201, v147
	v_cvt_scalef32_pk_f16_fp4 v198, v114, 1.0 op_sel:[0,1,0]
	v_cvt_scalef32_pk_f16_fp4 v199, v118, 1.0 op_sel:[0,1,0]
	v_cvt_scalef32_pk_f16_fp4 v200, v122, 1.0 op_sel:[0,1,0]
	v_cvt_scalef32_pk_f16_fp4 v201, v126, 1.0 op_sel:[0,1,0]
	v_dot2c_f32_f16_e32 v190, v198, v148
	v_dot2c_f32_f16_e32 v191, v199, v148
	v_dot2c_f32_f16_e32 v192, v200, v148
	v_dot2c_f32_f16_e32 v193, v201, v148
	v_cvt_scalef32_pk_f16_fp4 v198, v114, 1.0 op_sel:[1,1,0]
	v_cvt_scalef32_pk_f16_fp4 v199, v118, 1.0 op_sel:[1,1,0]
	v_cvt_scalef32_pk_f16_fp4 v200, v122, 1.0 op_sel:[1,1,0]
	v_cvt_scalef32_pk_f16_fp4 v201, v126, 1.0 op_sel:[1,1,0]
	v_dot2c_f32_f16_e32 v190, v198, v149
	v_dot2c_f32_f16_e32 v191, v199, v149
	v_dot2c_f32_f16_e32 v192, v200, v149
	v_dot2c_f32_f16_e32 v193, v201, v149
	v_cvt_scalef32_pk_f16_fp4 v198, v115, 1.0
	v_cvt_scalef32_pk_f16_fp4 v199, v119, 1.0
	v_cvt_scalef32_pk_f16_fp4 v200, v123, 1.0
	v_cvt_scalef32_pk_f16_fp4 v201, v127, 1.0
	v_dot2c_f32_f16_e32 v190, v198, v150
	v_dot2c_f32_f16_e32 v191, v199, v150
	v_dot2c_f32_f16_e32 v192, v200, v150
	v_dot2c_f32_f16_e32 v193, v201, v150
	v_cvt_scalef32_pk_f16_fp4 v198, v115, 1.0 op_sel:[1,0,0]
	v_cvt_scalef32_pk_f16_fp4 v199, v119, 1.0 op_sel:[1,0,0]
	v_cvt_scalef32_pk_f16_fp4 v200, v123, 1.0 op_sel:[1,0,0]
	v_cvt_scalef32_pk_f16_fp4 v201, v127, 1.0 op_sel:[1,0,0]
	v_dot2c_f32_f16_e32 v190, v198, v151
	v_dot2c_f32_f16_e32 v191, v199, v151
	v_dot2c_f32_f16_e32 v192, v200, v151
	v_dot2c_f32_f16_e32 v193, v201, v151
	v_cvt_scalef32_pk_f16_fp4 v198, v115, 1.0 op_sel:[0,1,0]
	v_cvt_scalef32_pk_f16_fp4 v199, v119, 1.0 op_sel:[0,1,0]
	v_cvt_scalef32_pk_f16_fp4 v200, v123, 1.0 op_sel:[0,1,0]
	v_cvt_scalef32_pk_f16_fp4 v201, v127, 1.0 op_sel:[0,1,0]
	v_dot2c_f32_f16_e32 v190, v198, v152
	v_dot2c_f32_f16_e32 v191, v199, v152
	v_dot2c_f32_f16_e32 v192, v200, v152
	v_dot2c_f32_f16_e32 v193, v201, v152
	v_cvt_scalef32_pk_f16_fp4 v198, v115, 1.0 op_sel:[1,1,0]
	v_cvt_scalef32_pk_f16_fp4 v199, v119, 1.0 op_sel:[1,1,0]
	v_cvt_scalef32_pk_f16_fp4 v200, v123, 1.0 op_sel:[1,1,0]
	v_cvt_scalef32_pk_f16_fp4 v201, v127, 1.0 op_sel:[1,1,0]
	v_dot2c_f32_f16_e32 v190, v198, v153
	v_dot2c_f32_f16_e32 v191, v199, v153
	v_dot2c_f32_f16_e32 v192, v200, v153
	v_dot2c_f32_f16_e32 v193, v201, v153
	v_cvt_scalef32_pk_f16_fp4 v198, v116, 1.0
	v_cvt_scalef32_pk_f16_fp4 v199, v120, 1.0
	v_cvt_scalef32_pk_f16_fp4 v200, v124, 1.0
	v_cvt_scalef32_pk_f16_fp4 v201, v128, 1.0
	v_dot2c_f32_f16_e32 v190, v198, v154
	v_dot2c_f32_f16_e32 v191, v199, v154
	v_dot2c_f32_f16_e32 v192, v200, v154
	v_dot2c_f32_f16_e32 v193, v201, v154
	v_cvt_scalef32_pk_f16_fp4 v198, v116, 1.0 op_sel:[1,0,0]
	v_cvt_scalef32_pk_f16_fp4 v199, v120, 1.0 op_sel:[1,0,0]
	v_cvt_scalef32_pk_f16_fp4 v200, v124, 1.0 op_sel:[1,0,0]
	v_cvt_scalef32_pk_f16_fp4 v201, v128, 1.0 op_sel:[1,0,0]
	v_dot2c_f32_f16_e32 v190, v198, v155
	v_dot2c_f32_f16_e32 v191, v199, v155
	v_dot2c_f32_f16_e32 v192, v200, v155
	v_dot2c_f32_f16_e32 v193, v201, v155
	v_cvt_scalef32_pk_f16_fp4 v198, v116, 1.0 op_sel:[0,1,0]
	v_cvt_scalef32_pk_f16_fp4 v199, v120, 1.0 op_sel:[0,1,0]
	v_cvt_scalef32_pk_f16_fp4 v200, v124, 1.0 op_sel:[0,1,0]
	v_cvt_scalef32_pk_f16_fp4 v201, v128, 1.0 op_sel:[0,1,0]
	v_dot2c_f32_f16_e32 v190, v198, v156
	v_dot2c_f32_f16_e32 v191, v199, v156
	v_dot2c_f32_f16_e32 v192, v200, v156
	v_dot2c_f32_f16_e32 v193, v201, v156
	v_cvt_scalef32_pk_f16_fp4 v198, v116, 1.0 op_sel:[1,1,0]
	v_cvt_scalef32_pk_f16_fp4 v199, v120, 1.0 op_sel:[1,1,0]
	v_cvt_scalef32_pk_f16_fp4 v200, v124, 1.0 op_sel:[1,1,0]
	v_cvt_scalef32_pk_f16_fp4 v201, v128, 1.0 op_sel:[1,1,0]
	v_dot2c_f32_f16_e32 v190, v198, v157
	v_dot2c_f32_f16_e32 v191, v199, v157
	v_dot2c_f32_f16_e32 v192, v200, v157
	v_dot2c_f32_f16_e32 v193, v201, v157
	v_cvt_scalef32_pk_f16_fp4 v198, v117, 1.0
	v_cvt_scalef32_pk_f16_fp4 v199, v121, 1.0
	v_cvt_scalef32_pk_f16_fp4 v200, v125, 1.0
	v_cvt_scalef32_pk_f16_fp4 v201, v129, 1.0
	v_dot2c_f32_f16_e32 v190, v198, v158
	v_dot2c_f32_f16_e32 v191, v199, v158
	v_dot2c_f32_f16_e32 v192, v200, v158
	v_dot2c_f32_f16_e32 v193, v201, v158
	v_cvt_scalef32_pk_f16_fp4 v198, v117, 1.0 op_sel:[1,0,0]
	v_cvt_scalef32_pk_f16_fp4 v199, v121, 1.0 op_sel:[1,0,0]
	v_cvt_scalef32_pk_f16_fp4 v200, v125, 1.0 op_sel:[1,0,0]
	v_cvt_scalef32_pk_f16_fp4 v201, v129, 1.0 op_sel:[1,0,0]
	v_dot2c_f32_f16_e32 v190, v198, v159
	v_dot2c_f32_f16_e32 v191, v199, v159
	v_dot2c_f32_f16_e32 v192, v200, v159
	v_dot2c_f32_f16_e32 v193, v201, v159
	v_cvt_scalef32_pk_f16_fp4 v198, v117, 1.0 op_sel:[0,1,0]
	v_cvt_scalef32_pk_f16_fp4 v199, v121, 1.0 op_sel:[0,1,0]
	v_cvt_scalef32_pk_f16_fp4 v200, v125, 1.0 op_sel:[0,1,0]
	v_cvt_scalef32_pk_f16_fp4 v201, v129, 1.0 op_sel:[0,1,0]
	v_dot2c_f32_f16_e32 v190, v198, v160
	v_dot2c_f32_f16_e32 v191, v199, v160
	v_dot2c_f32_f16_e32 v192, v200, v160
	v_dot2c_f32_f16_e32 v193, v201, v160
	v_cvt_scalef32_pk_f16_fp4 v198, v117, 1.0 op_sel:[1,1,0]
	v_cvt_scalef32_pk_f16_fp4 v199, v121, 1.0 op_sel:[1,1,0]
	v_cvt_scalef32_pk_f16_fp4 v200, v125, 1.0 op_sel:[1,1,0]
	v_cvt_scalef32_pk_f16_fp4 v201, v129, 1.0 op_sel:[1,1,0]
	v_dot2c_f32_f16_e32 v190, v198, v161
	v_dot2c_f32_f16_e32 v191, v199, v161
	v_dot2c_f32_f16_e32 v192, v200, v161
	v_dot2c_f32_f16_e32 v193, v201, v161
	s_nop 3
	v_cndmask_b32_e64 v194, v178, v186, s[38:39]
	v_cndmask_b32_e64 v233, v186, v178, s[38:39]
	v_cndmask_b32_e64 v195, v179, v187, s[38:39]
	v_cndmask_b32_e64 v234, v187, v179, s[38:39]
	v_cndmask_b32_e64 v196, v180, v188, s[38:39]
	v_cndmask_b32_e64 v235, v188, v180, s[38:39]
	v_cndmask_b32_e64 v197, v181, v189, s[38:39]
	v_cndmask_b32_e64 v236, v189, v181, s[38:39]
	v_cndmask_b32_e64 v198, v182, v190, s[38:39]
	v_cndmask_b32_e64 v237, v190, v182, s[38:39]
	v_cndmask_b32_e64 v199, v183, v191, s[38:39]
	v_cndmask_b32_e64 v238, v191, v183, s[38:39]
	v_cndmask_b32_e64 v200, v184, v192, s[38:39]
	v_cndmask_b32_e64 v239, v192, v184, s[38:39]
	v_cndmask_b32_e64 v201, v185, v193, s[38:39]
	v_cndmask_b32_e64 v240, v193, v185, s[38:39]
	v_add_f32_dpp v241, v233, v194 row_half_mirror row_mask:0xf bank_mask:0xf bound_ctrl:1
	v_add_f32_dpp v242, v234, v195 row_half_mirror row_mask:0xf bank_mask:0xf bound_ctrl:1
	v_add_f32_dpp v243, v235, v196 row_half_mirror row_mask:0xf bank_mask:0xf bound_ctrl:1
	v_add_f32_dpp v244, v236, v197 row_half_mirror row_mask:0xf bank_mask:0xf bound_ctrl:1
	v_add_f32_dpp v245, v237, v198 row_half_mirror row_mask:0xf bank_mask:0xf bound_ctrl:1
	v_add_f32_dpp v246, v238, v199 row_half_mirror row_mask:0xf bank_mask:0xf bound_ctrl:1
	v_add_f32_dpp v247, v239, v200 row_half_mirror row_mask:0xf bank_mask:0xf bound_ctrl:1
	v_add_f32_dpp v248, v240, v201 row_half_mirror row_mask:0xf bank_mask:0xf bound_ctrl:1
	v_cndmask_b32_e64 v194, v245, v241, s[40:41]
	v_cndmask_b32_e64 v233, v241, v245, s[40:41]
	v_cndmask_b32_e64 v195, v246, v242, s[40:41]
	v_cndmask_b32_e64 v234, v242, v246, s[40:41]
	v_cndmask_b32_e64 v196, v247, v243, s[40:41]
	v_cndmask_b32_e64 v235, v243, v247, s[40:41]
	v_cndmask_b32_e64 v197, v248, v244, s[40:41]
	v_cndmask_b32_e64 v236, v244, v248, s[40:41]
	v_add_f32_dpp v178, v233, v194 quad_perm:[2,3,0,1] row_mask:0xf bank_mask:0xf bound_ctrl:1
	v_add_f32_dpp v179, v234, v195 quad_perm:[2,3,0,1] row_mask:0xf bank_mask:0xf bound_ctrl:1
	v_add_f32_dpp v180, v235, v196 quad_perm:[2,3,0,1] row_mask:0xf bank_mask:0xf bound_ctrl:1
	v_add_f32_dpp v181, v236, v197 quad_perm:[2,3,0,1] row_mask:0xf bank_mask:0xf bound_ctrl:1
	v_cndmask_b32_e64 v194, v180, v178, s[42:43]
	v_cndmask_b32_e64 v233, v178, v180, s[42:43]
	v_cndmask_b32_e64 v195, v181, v179, s[42:43]
	v_cndmask_b32_e64 v234, v179, v181, s[42:43]
	s_nop 1
	v_add_f32_dpp v196, v233, v194 quad_perm:[1,0,3,2] row_mask:0xf bank_mask:0xf bound_ctrl:1
	v_add_f32_dpp v197, v234, v195 quad_perm:[1,0,3,2] row_mask:0xf bank_mask:0xf bound_ctrl:1
	v_cvt_pk_bf16_f32 v198, v196, v197
	global_store_dword v227, v198, s[4:5] offset:256
	v_add_u32_e32 v227, 0x200, v227
	v_add_u32_e32 v226, 0x2000, v226
	s_add_i32 s34, s34, 2
	s_cmp_lt_u32 s34, 8
	s_cbranch_scc1 .Le1_loop
	s_branch .LBB0_724

.LBB0_888:
	s_or_b64 exec, exec, s[0:1]
	s_nop 0
	v_pk_add_f32 v[20:21], v[20:21], v[24:25]
	v_pk_add_f32 v[24:25], v[28:29], v[32:33]
	v_pk_add_f32 v[18:19], v[18:19], v[22:23]
	v_pk_add_f32 v[22:23], v[26:27], v[30:31]
	v_mov_b64_e32 v[82:83], v[12:13]
	v_mov_b64_e32 v[42:43], v[16:17]
	v_cndmask_b32_e64 v23, v23, v25, s[38:39]
	v_cndmask_b32_e64 v22, v22, v24, s[38:39]
	v_cndmask_b32_e64 v19, v19, v21, s[38:39]
	v_cndmask_b32_e64 v18, v18, v20, s[38:39]
	s_add_i32 s33, s33, 2
	v_lshl_add_u64 v[120:121], v[120:121], 0, s[82:83]
	s_and_b64 vcc, exec, s[42:43]
	v_mov_b64_e32 v[80:81], v[10:11]
	v_mov_b64_e32 v[40:41], v[14:15]
	s_waitcnt vmcnt(0)
	v_pk_fma_f32 v[18:19], v[238:239], v[18:19], v[234:235]
	v_pk_fma_f32 v[20:21], v[240:241], v[22:23], v[236:237]
	global_store_dwordx4 v[204:205], v[18:21], off
	s_cbranch_vccnz .LBB0_880

.LBB0_891:
	s_waitcnt vmcnt(18)
	v_mul_hi_i32 v244, v113, s69
	v_lshrrev_b32_e32 v245, 31, v244
	v_ashrrev_i32_e32 v244, 13, v244
	v_add_u32_e32 v245, v244, v245
	v_mul_i32_i24_e32 v248, 0xffffbf00, v245
	v_add_u32_e32 v244, v113, v248
	v_cmp_gt_i32_e32 vcc, s68, v244
	v_cmp_lt_i32_e64 s[0:1], s21, v244
	s_and_saveexec_b64 s[2:3], s[0:1]
	s_xor_b64 s[0:1], exec, s[2:3]
	v_lshl_add_u32 v244, v245, 14, v248
	v_add3_u32 v244, v113, v244, s88
	s_or_saveexec_b64 s[0:1], s[0:1]
	v_mov_b64_e32 v[246:247], s[18:19]
	s_xor_b64 exec, exec, s[0:1]
	v_lshlrev_b32_e32 v244, 8, v245
	v_add3_u32 v244, v248, v113, v244
	v_mov_b64_e32 v[246:247], s[72:73]
	s_or_b64 exec, exec, s[0:1]
	v_mul_i32_i24_e32 v245, 0x3000, v245
	v_cndmask_b32_e32 v248, v245, v223, vcc
	v_ashrrev_i32_e32 v249, 31, v248
	v_lshl_add_u64 v[248:249], v[248:249], 2, s[10:11]
	v_lshlrev_b32_e32 v210, 2, v118
	v_ashrrev_i32_e32 v245, 31, v244
	v_lshl_add_u64 v[250:251], v[248:249], 0, v[210:211]
	v_lshlrev_b64 v[244:245], 13, v[244:245]
	v_lshl_add_u64 v[244:245], v[246:247], 0, v[244:245]
	v_add_co_u32_e32 v250, vcc, s94, v250
	v_lshl_add_u64 v[204:205], v[244:245], 0, v[210:211]
	s_nop 0
	v_addc_co_u32_e32 v251, vcc, 0, v251, vcc
	global_load_dwordx4 v[196:199], v[204:205], off
	global_load_dwordx4 v[200:203], v[250:251], off
	v_mul_u32_u24_sdwa v38, v30, s93 dst_sel:DWORD dst_unused:UNUSED_PAD src0_sel:WORD_0 src1_sel:DWORD
	v_cvt_scalef32_pk_f16_fp4 v39, v108, 1.0
	v_cvt_scalef32_pk_f16_fp4 v48, v108, 1.0 op_sel:[1,0,0]
	v_cvt_scalef32_pk_f16_fp4 v49, v108, 1.0 op_sel:[0,1,0]
	v_cvt_scalef32_pk_f16_fp4 v78, v108, 1.0 op_sel:[1,1,0]
	v_cvt_scalef32_pk_f16_fp4 v79, v109, 1.0
	v_cvt_scalef32_pk_f16_fp4 v108, v109, 1.0 op_sel:[1,0,0]
	v_cvt_scalef32_pk_f16_fp4 v119, v109, 1.0 op_sel:[0,1,0]
	v_cvt_scalef32_pk_f16_fp4 v109, v109, 1.0 op_sel:[1,1,0]
	v_cvt_scalef32_pk_f16_fp4 v122, v110, 1.0
	v_cvt_scalef32_pk_f16_fp4 v123, v110, 1.0 op_sel:[1,0,0]
	v_cvt_scalef32_pk_f16_fp4 v124, v110, 1.0 op_sel:[0,1,0]
	v_cvt_scalef32_pk_f16_fp4 v110, v110, 1.0 op_sel:[1,1,0]
	v_cvt_scalef32_pk_f16_fp4 v125, v111, 1.0
	v_cvt_scalef32_pk_f16_fp4 v126, v111, 1.0 op_sel:[1,0,0]
	v_cvt_scalef32_pk_f16_fp4 v127, v111, 1.0 op_sel:[0,1,0]
	v_cvt_scalef32_pk_f16_fp4 v111, v111, 1.0 op_sel:[1,1,0]
	v_pk_fma_f16 v39, v39, v38, 0
	v_pk_fma_f16 v48, v48, v38, 0
	v_pk_fma_f16 v49, v49, v38, 0
	v_pk_fma_f16 v78, v78, v38, 0
	v_pk_fma_f16 v79, v79, v38, 0
	v_pk_fma_f16 v108, v108, v38, 0
	v_pk_fma_f16 v119, v119, v38, 0
	v_pk_fma_f16 v109, v109, v38, 0
	v_pk_fma_f16 v122, v122, v38, 0
	v_pk_fma_f16 v123, v123, v38, 0
	v_pk_fma_f16 v124, v124, v38, 0
	v_pk_fma_f16 v110, v110, v38, 0
	v_pk_fma_f16 v125, v125, v38, 0
	v_pk_fma_f16 v126, v126, v38, 0
	v_pk_fma_f16 v127, v127, v38, 0
	v_pk_fma_f16 v38, v111, v38, 0
	v_mul_u32_u24_sdwa v30, v30, s93 dst_sel:DWORD dst_unused:UNUSED_PAD src0_sel:WORD_1 src1_sel:DWORD
	v_cvt_scalef32_pk_f16_fp4 v111, v104, 1.0
	v_pk_fma_f16 v39, v111, v30, v39
	v_cvt_scalef32_pk_f16_fp4 v111, v104, 1.0 op_sel:[1,0,0]
	v_pk_fma_f16 v48, v111, v30, v48
	v_cvt_scalef32_pk_f16_fp4 v111, v104, 1.0 op_sel:[0,1,0]
	v_cvt_scalef32_pk_f16_fp4 v104, v104, 1.0 op_sel:[1,1,0]
	v_pk_fma_f16 v78, v104, v30, v78
	v_cvt_scalef32_pk_f16_fp4 v104, v105, 1.0
	v_pk_fma_f16 v79, v104, v30, v79
	v_cvt_scalef32_pk_f16_fp4 v104, v105, 1.0 op_sel:[1,0,0]
	v_pk_fma_f16 v104, v104, v30, v108
	v_cvt_scalef32_pk_f16_fp4 v108, v105, 1.0 op_sel:[0,1,0]
	v_cvt_scalef32_pk_f16_fp4 v105, v105, 1.0 op_sel:[1,1,0]
	v_pk_fma_f16 v49, v111, v30, v49
	v_pk_fma_f16 v108, v108, v30, v119
	v_pk_fma_f16 v105, v105, v30, v109
	v_cvt_scalef32_pk_f16_fp4 v109, v106, 1.0
	v_cvt_scalef32_pk_f16_fp4 v111, v106, 1.0 op_sel:[1,0,0]
	v_cvt_scalef32_pk_f16_fp4 v119, v106, 1.0 op_sel:[0,1,0]
	v_cvt_scalef32_pk_f16_fp4 v106, v106, 1.0 op_sel:[1,1,0]
	v_pk_fma_f16 v109, v109, v30, v122
	v_pk_fma_f16 v111, v111, v30, v123
	v_pk_fma_f16 v106, v106, v30, v110
	v_cvt_scalef32_pk_f16_fp4 v110, v107, 1.0
	v_cvt_scalef32_pk_f16_fp4 v122, v107, 1.0 op_sel:[1,0,0]
	v_cvt_scalef32_pk_f16_fp4 v123, v107, 1.0 op_sel:[0,1,0]
	v_cvt_scalef32_pk_f16_fp4 v107, v107, 1.0 op_sel:[1,1,0]
	v_pk_fma_f16 v119, v119, v30, v124
	v_pk_fma_f16 v110, v110, v30, v125
	v_pk_fma_f16 v122, v122, v30, v126
	v_pk_fma_f16 v123, v123, v30, v127
	v_pk_fma_f16 v30, v107, v30, v38
	v_mul_u32_u24_sdwa v38, v31, s93 dst_sel:DWORD dst_unused:UNUSED_PAD src0_sel:WORD_0 src1_sel:DWORD
	v_cvt_scalef32_pk_f16_fp4 v107, v100, 1.0
	v_pk_fma_f16 v39, v107, v38, v39
	v_cvt_scalef32_pk_f16_fp4 v107, v100, 1.0 op_sel:[1,0,0]
	v_pk_fma_f16 v48, v107, v38, v48
	v_cvt_scalef32_pk_f16_fp4 v107, v100, 1.0 op_sel:[0,1,0]
	v_cvt_scalef32_pk_f16_fp4 v100, v100, 1.0 op_sel:[1,1,0]
	v_pk_fma_f16 v78, v100, v38, v78
	v_cvt_scalef32_pk_f16_fp4 v100, v101, 1.0
	v_pk_fma_f16 v79, v100, v38, v79
	v_cvt_scalef32_pk_f16_fp4 v100, v101, 1.0 op_sel:[1,0,0]
	v_pk_fma_f16 v100, v100, v38, v104
	v_cvt_scalef32_pk_f16_fp4 v104, v101, 1.0 op_sel:[0,1,0]
	v_cvt_scalef32_pk_f16_fp4 v101, v101, 1.0 op_sel:[1,1,0]
	v_pk_fma_f16 v49, v107, v38, v49
	v_pk_fma_f16 v104, v104, v38, v108
	v_pk_fma_f16 v101, v101, v38, v105
	v_cvt_scalef32_pk_f16_fp4 v105, v102, 1.0
	v_cvt_scalef32_pk_f16_fp4 v107, v102, 1.0 op_sel:[1,0,0]
	v_cvt_scalef32_pk_f16_fp4 v108, v102, 1.0 op_sel:[0,1,0]
	v_cvt_scalef32_pk_f16_fp4 v102, v102, 1.0 op_sel:[1,1,0]
	v_pk_fma_f16 v102, v102, v38, v106
	v_cvt_scalef32_pk_f16_fp4 v106, v103, 1.0
	v_pk_fma_f16 v105, v105, v38, v109
	v_pk_fma_f16 v106, v106, v38, v110
	v_cvt_scalef32_pk_f16_fp4 v109, v103, 1.0 op_sel:[1,0,0]
	v_cvt_scalef32_pk_f16_fp4 v110, v103, 1.0 op_sel:[0,1,0]
	v_cvt_scalef32_pk_f16_fp4 v103, v103, 1.0 op_sel:[1,1,0]
	v_pk_fma_f16 v107, v107, v38, v111
	v_pk_fma_f16 v108, v108, v38, v119
	v_pk_fma_f16 v109, v109, v38, v122
	v_pk_fma_f16 v110, v110, v38, v123
	v_pk_fma_f16 v30, v103, v38, v30
	v_mul_u32_u24_sdwa v31, v31, s93 dst_sel:DWORD dst_unused:UNUSED_PAD src0_sel:WORD_1 src1_sel:DWORD
	v_cvt_scalef32_pk_f16_fp4 v38, v44, 1.0
	v_pk_fma_f16 v38, v38, v31, v39
	v_cvt_scalef32_pk_f16_fp4 v39, v44, 1.0 op_sel:[1,0,0]
	v_pk_fma_f16 v39, v39, v31, v48
	v_cvt_scalef32_pk_f16_fp4 v48, v44, 1.0 op_sel:[0,1,0]
	v_pk_fma_f16 v48, v48, v31, v49
	v_cvt_scalef32_pk_f16_fp4 v44, v44, 1.0 op_sel:[1,1,0]
	v_cvt_scalef32_pk_f16_fp4 v49, v45, 1.0
	v_pk_fma_f16 v44, v44, v31, v78
	v_pk_fma_f16 v49, v49, v31, v79
	v_cvt_scalef32_pk_f16_fp4 v78, v45, 1.0 op_sel:[1,0,0]
	v_cvt_scalef32_pk_f16_fp4 v79, v45, 1.0 op_sel:[0,1,0]
	v_cvt_scalef32_pk_f16_fp4 v45, v45, 1.0 op_sel:[1,1,0]
	v_pk_fma_f16 v78, v78, v31, v100
	v_pk_fma_f16 v45, v45, v31, v101
	v_cvt_scalef32_pk_f16_fp4 v100, v46, 1.0
	v_cvt_scalef32_pk_f16_fp4 v101, v46, 1.0 op_sel:[1,0,0]
	v_cvt_scalef32_pk_f16_fp4 v103, v46, 1.0 op_sel:[0,1,0]
	v_cvt_scalef32_pk_f16_fp4 v46, v46, 1.0 op_sel:[1,1,0]
	v_pk_fma_f16 v79, v79, v31, v104
	v_pk_fma_f16 v100, v100, v31, v105
	v_pk_fma_f16 v46, v46, v31, v102
	v_cvt_scalef32_pk_f16_fp4 v102, v47, 1.0
	v_cvt_scalef32_pk_f16_fp4 v104, v47, 1.0 op_sel:[1,0,0]
	v_cvt_scalef32_pk_f16_fp4 v105, v47, 1.0 op_sel:[0,1,0]
	v_cvt_scalef32_pk_f16_fp4 v47, v47, 1.0 op_sel:[1,1,0]
	v_pk_fma_f16 v101, v101, v31, v107
	v_pk_fma_f16 v103, v103, v31, v108
	v_pk_fma_f16 v102, v102, v31, v106
	v_pk_fma_f16 v104, v104, v31, v109
	v_pk_fma_f16 v105, v105, v31, v110
	v_pk_fma_f16 v30, v47, v31, v30
	v_mul_u32_u24_sdwa v31, v32, s93 dst_sel:DWORD dst_unused:UNUSED_PAD src0_sel:WORD_0 src1_sel:DWORD
	v_cvt_scalef32_pk_f16_fp4 v47, v34, 1.0
	v_pk_fma_f16 v38, v47, v31, v38
	v_cvt_scalef32_pk_f16_fp4 v47, v34, 1.0 op_sel:[1,0,0]
	v_pk_fma_f16 v39, v47, v31, v39
	v_cvt_scalef32_pk_f16_fp4 v47, v34, 1.0 op_sel:[0,1,0]
	v_cvt_scalef32_pk_f16_fp4 v34, v34, 1.0 op_sel:[1,1,0]
	v_pk_fma_f16 v34, v34, v31, v44
	v_cvt_scalef32_pk_f16_fp4 v44, v35, 1.0
	v_pk_fma_f16 v47, v47, v31, v48
	v_pk_fma_f16 v44, v44, v31, v49
	v_cvt_scalef32_pk_f16_fp4 v48, v35, 1.0 op_sel:[1,0,0]
	v_cvt_scalef32_pk_f16_fp4 v49, v35, 1.0 op_sel:[0,1,0]
	v_cvt_scalef32_pk_f16_fp4 v35, v35, 1.0 op_sel:[1,1,0]
	v_pk_fma_f16 v48, v48, v31, v78
	v_pk_fma_f16 v49, v49, v31, v79
	v_pk_fma_f16 v35, v35, v31, v45
	v_cvt_scalef32_pk_f16_fp4 v45, v36, 1.0
	v_cvt_scalef32_pk_f16_fp4 v78, v36, 1.0 op_sel:[1,0,0]
	v_cvt_scalef32_pk_f16_fp4 v79, v36, 1.0 op_sel:[0,1,0]
	v_cvt_scalef32_pk_f16_fp4 v36, v36, 1.0 op_sel:[1,1,0]
	v_pk_fma_f16 v45, v45, v31, v100
	v_pk_fma_f16 v78, v78, v31, v101
	v_pk_fma_f16 v36, v36, v31, v46
	v_cvt_scalef32_pk_f16_fp4 v46, v37, 1.0
	v_cvt_scalef32_pk_f16_fp4 v100, v37, 1.0 op_sel:[1,0,0]
	v_cvt_scalef32_pk_f16_fp4 v101, v37, 1.0 op_sel:[0,1,0]
	v_cvt_scalef32_pk_f16_fp4 v37, v37, 1.0 op_sel:[1,1,0]
	v_pk_fma_f16 v79, v79, v31, v103
	v_pk_fma_f16 v46, v46, v31, v102
	v_pk_fma_f16 v100, v100, v31, v104
	v_pk_fma_f16 v101, v101, v31, v105
	v_pk_fma_f16 v30, v37, v31, v30
	v_mul_u32_u24_sdwa v31, v32, s93 dst_sel:DWORD dst_unused:UNUSED_PAD src0_sel:WORD_1 src1_sel:DWORD
	v_cvt_scalef32_pk_f16_fp4 v32, v26, 1.0
	v_pk_fma_f16 v32, v32, v31, v38
	v_cvt_scalef32_pk_f16_fp4 v37, v26, 1.0 op_sel:[1,0,0]
	v_cvt_scalef32_pk_f16_fp4 v38, v26, 1.0 op_sel:[0,1,0]
	v_cvt_scalef32_pk_f16_fp4 v26, v26, 1.0 op_sel:[1,1,0]
	v_pk_fma_f16 v26, v26, v31, v34
	v_cvt_scalef32_pk_f16_fp4 v34, v27, 1.0
	v_pk_fma_f16 v37, v37, v31, v39
	v_pk_fma_f16 v34, v34, v31, v44
	v_cvt_scalef32_pk_f16_fp4 v39, v27, 1.0 op_sel:[1,0,0]
	v_cvt_scalef32_pk_f16_fp4 v44, v27, 1.0 op_sel:[0,1,0]
	v_cvt_scalef32_pk_f16_fp4 v27, v27, 1.0 op_sel:[1,1,0]
	v_pk_fma_f16 v27, v27, v31, v35
	v_cvt_scalef32_pk_f16_fp4 v35, v28, 1.0
	v_pk_fma_f16 v38, v38, v31, v47
	v_pk_fma_f16 v35, v35, v31, v45
	v_cvt_scalef32_pk_f16_fp4 v45, v28, 1.0 op_sel:[1,0,0]
	v_cvt_scalef32_pk_f16_fp4 v47, v28, 1.0 op_sel:[0,1,0]
	v_cvt_scalef32_pk_f16_fp4 v28, v28, 1.0 op_sel:[1,1,0]
	v_pk_fma_f16 v28, v28, v31, v36
	v_cvt_scalef32_pk_f16_fp4 v36, v29, 1.0
	v_pk_fma_f16 v39, v39, v31, v48
	v_pk_fma_f16 v36, v36, v31, v46
	v_cvt_scalef32_pk_f16_fp4 v46, v29, 1.0 op_sel:[1,0,0]
	v_cvt_scalef32_pk_f16_fp4 v48, v29, 1.0 op_sel:[0,1,0]
	v_cvt_scalef32_pk_f16_fp4 v29, v29, 1.0 op_sel:[1,1,0]
	v_pk_fma_f16 v44, v44, v31, v49
	v_pk_fma_f16 v45, v45, v31, v78
	v_pk_fma_f16 v47, v47, v31, v79
	v_pk_fma_f16 v46, v46, v31, v100
	v_pk_fma_f16 v48, v48, v31, v101
	v_pk_fma_f16 v29, v29, v31, v30
	v_mul_u32_u24_sdwa v30, v33, s93 dst_sel:DWORD dst_unused:UNUSED_PAD src0_sel:WORD_0 src1_sel:DWORD
	v_cvt_scalef32_pk_f16_fp4 v31, v22, 1.0
	v_pk_fma_f16 v31, v31, v30, v32
	v_cvt_scalef32_pk_f16_fp4 v32, v22, 1.0 op_sel:[1,0,0]
	v_pk_fma_f16 v32, v32, v30, v37
	v_cvt_scalef32_pk_f16_fp4 v37, v22, 1.0 op_sel:[0,1,0]
	v_cvt_scalef32_pk_f16_fp4 v22, v22, 1.0 op_sel:[1,1,0]
	v_pk_fma_f16 v22, v22, v30, v26
	v_cvt_scalef32_pk_f16_fp4 v26, v23, 1.0
	v_pk_fma_f16 v37, v37, v30, v38
	v_pk_fma_f16 v26, v26, v30, v34
	v_cvt_scalef32_pk_f16_fp4 v34, v23, 1.0 op_sel:[1,0,0]
	v_cvt_scalef32_pk_f16_fp4 v38, v23, 1.0 op_sel:[0,1,0]
	v_cvt_scalef32_pk_f16_fp4 v23, v23, 1.0 op_sel:[1,1,0]
	v_pk_fma_f16 v23, v23, v30, v27
	v_cvt_scalef32_pk_f16_fp4 v27, v24, 1.0
	v_pk_fma_f16 v34, v34, v30, v39
	v_pk_fma_f16 v27, v27, v30, v35
	v_cvt_scalef32_pk_f16_fp4 v35, v24, 1.0 op_sel:[1,0,0]
	v_cvt_scalef32_pk_f16_fp4 v39, v24, 1.0 op_sel:[0,1,0]
	v_cvt_scalef32_pk_f16_fp4 v24, v24, 1.0 op_sel:[1,1,0]
	v_pk_fma_f16 v24, v24, v30, v28
	v_cvt_scalef32_pk_f16_fp4 v28, v25, 1.0
	v_pk_fma_f16 v38, v38, v30, v44
	v_pk_fma_f16 v28, v28, v30, v36
	v_cvt_scalef32_pk_f16_fp4 v36, v25, 1.0 op_sel:[1,0,0]
	v_cvt_scalef32_pk_f16_fp4 v44, v25, 1.0 op_sel:[0,1,0]
	v_cvt_scalef32_pk_f16_fp4 v25, v25, 1.0 op_sel:[1,1,0]
	v_pk_fma_f16 v35, v35, v30, v45
	v_pk_fma_f16 v39, v39, v30, v47
	v_pk_fma_f16 v36, v36, v30, v46
	v_pk_fma_f16 v44, v44, v30, v48
	v_pk_fma_f16 v25, v25, v30, v29
	v_mul_u32_u24_sdwa v29, v33, s93 dst_sel:DWORD dst_unused:UNUSED_PAD src0_sel:WORD_1 src1_sel:DWORD
	v_cvt_scalef32_pk_f16_fp4 v30, v18, 1.0
	v_pk_fma_f16 v78, v30, v29, v31
	v_cvt_scalef32_pk_f16_fp4 v30, v18, 1.0 op_sel:[1,0,0]
	v_pk_fma_f16 v79, v30, v29, v32
	v_cvt_scalef32_pk_f16_fp4 v30, v18, 1.0 op_sel:[0,1,0]
	v_cvt_scalef32_pk_f16_fp4 v18, v18, 1.0 op_sel:[1,1,0]
	v_pk_fma_f16 v101, v18, v29, v22
	v_cvt_scalef32_pk_f16_fp4 v18, v19, 1.0
	v_pk_fma_f16 v102, v18, v29, v26
	v_cvt_scalef32_pk_f16_fp4 v18, v19, 1.0 op_sel:[1,0,0]
	v_pk_fma_f16 v103, v18, v29, v34
	v_cvt_scalef32_pk_f16_fp4 v18, v19, 1.0 op_sel:[0,1,0]
	v_mul_u32_u24_sdwa v123, v62, s93 dst_sel:DWORD dst_unused:UNUSED_PAD src0_sel:WORD_0 src1_sel:DWORD
	v_cvt_scalef32_pk_f16_fp4 v124, v96, 1.0
	v_pk_fma_f16 v104, v18, v29, v38
	v_cvt_scalef32_pk_f16_fp4 v18, v19, 1.0 op_sel:[1,1,0]
	v_pk_fma_f16 v78, v124, v123, v78
	v_cvt_scalef32_pk_f16_fp4 v124, v96, 1.0 op_sel:[1,0,0]
	v_pk_fma_f16 v105, v18, v29, v23
	v_cvt_scalef32_pk_f16_fp4 v18, v20, 1.0
	v_pk_fma_f16 v79, v124, v123, v79
	v_cvt_scalef32_pk_f16_fp4 v124, v96, 1.0 op_sel:[0,1,0]
	v_cvt_scalef32_pk_f16_fp4 v96, v96, 1.0 op_sel:[1,1,0]
	v_pk_fma_f16 v106, v18, v29, v27
	v_cvt_scalef32_pk_f16_fp4 v18, v20, 1.0 op_sel:[1,0,0]
	v_pk_fma_f16 v96, v96, v123, v101
	v_cvt_scalef32_pk_f16_fp4 v101, v97, 1.0
	v_pk_fma_f16 v107, v18, v29, v35
	v_cvt_scalef32_pk_f16_fp4 v18, v20, 1.0 op_sel:[0,1,0]
	v_pk_fma_f16 v101, v101, v123, v102
	v_cvt_scalef32_pk_f16_fp4 v102, v97, 1.0 op_sel:[1,0,0]
	v_pk_fma_f16 v108, v18, v29, v39
	v_cvt_scalef32_pk_f16_fp4 v18, v20, 1.0 op_sel:[1,1,0]
	v_pk_fma_f16 v102, v102, v123, v103
	v_cvt_scalef32_pk_f16_fp4 v103, v97, 1.0 op_sel:[0,1,0]
	v_cvt_scalef32_pk_f16_fp4 v97, v97, 1.0 op_sel:[1,1,0]
	v_pk_fma_f16 v109, v18, v29, v24
	v_cvt_scalef32_pk_f16_fp4 v18, v21, 1.0
	v_pk_fma_f16 v97, v97, v123, v105
	v_cvt_scalef32_pk_f16_fp4 v105, v98, 1.0 op_sel:[1,0,0]
	v_pk_fma_f16 v110, v18, v29, v28
	v_pk_fma_f16 v105, v105, v123, v107
	v_cvt_scalef32_pk_f16_fp4 v107, v99, 1.0
	v_pk_fma_f16 v107, v107, v123, v110
	v_mul_u32_u24_sdwa v62, v62, s93 dst_sel:DWORD dst_unused:UNUSED_PAD src0_sel:WORD_1 src1_sel:DWORD
	v_cvt_scalef32_pk_f16_fp4 v110, v92, 1.0
	v_pk_fma_f16 v78, v110, v62, v78
	v_cvt_scalef32_pk_f16_fp4 v110, v92, 1.0 op_sel:[1,0,0]
	v_pk_fma_f16 v79, v110, v62, v79
	v_cvt_scalef32_pk_f16_fp4 v110, v92, 1.0 op_sel:[0,1,0]
	v_cvt_scalef32_pk_f16_fp4 v92, v92, 1.0 op_sel:[1,1,0]
	v_pk_fma_f16 v92, v92, v62, v96
	v_cvt_scalef32_pk_f16_fp4 v96, v93, 1.0
	v_cvt_scalef32_pk_f16_fp4 v18, v21, 1.0 op_sel:[1,0,0]
	v_pk_fma_f16 v96, v96, v62, v101
	v_cvt_scalef32_pk_f16_fp4 v101, v93, 1.0 op_sel:[1,0,0]
	v_pk_fma_f16 v111, v18, v29, v36
	v_cvt_scalef32_pk_f16_fp4 v18, v21, 1.0 op_sel:[0,1,0]
	v_pk_fma_f16 v103, v103, v123, v104
	v_cvt_scalef32_pk_f16_fp4 v104, v98, 1.0
	v_pk_fma_f16 v101, v101, v62, v102
	v_cvt_scalef32_pk_f16_fp4 v102, v93, 1.0 op_sel:[0,1,0]
	v_cvt_scalef32_pk_f16_fp4 v93, v93, 1.0 op_sel:[1,1,0]
	v_pk_fma_f16 v119, v18, v29, v44
	v_cvt_scalef32_pk_f16_fp4 v18, v21, 1.0 op_sel:[1,1,0]
	v_pk_fma_f16 v104, v104, v123, v106
	v_cvt_scalef32_pk_f16_fp4 v106, v98, 1.0 op_sel:[0,1,0]
	v_cvt_scalef32_pk_f16_fp4 v98, v98, 1.0 op_sel:[1,1,0]
	v_pk_fma_f16 v93, v93, v62, v97
	v_cvt_scalef32_pk_f16_fp4 v97, v94, 1.0
	v_pk_fma_f16 v100, v30, v29, v37
	v_pk_fma_f16 v122, v18, v29, v25
	v_pk_fma_f16 v106, v106, v123, v108
	v_pk_fma_f16 v98, v98, v123, v109
	v_cvt_scalef32_pk_f16_fp4 v108, v99, 1.0 op_sel:[1,0,0]
	v_cvt_scalef32_pk_f16_fp4 v109, v99, 1.0 op_sel:[0,1,0]
	v_cvt_scalef32_pk_f16_fp4 v99, v99, 1.0 op_sel:[1,1,0]
	v_pk_fma_f16 v102, v102, v62, v103
	v_pk_fma_f16 v97, v97, v62, v104
	v_cvt_scalef32_pk_f16_fp4 v103, v94, 1.0 op_sel:[1,0,0]
	v_cvt_scalef32_pk_f16_fp4 v104, v94, 1.0 op_sel:[0,1,0]
	v_cvt_scalef32_pk_f16_fp4 v94, v94, 1.0 op_sel:[1,1,0]
	v_pk_fma_f16 v100, v124, v123, v100
	v_pk_fma_f16 v108, v108, v123, v111
	v_pk_fma_f16 v109, v109, v123, v119
	v_pk_fma_f16 v99, v99, v123, v122
	v_pk_fma_f16 v103, v103, v62, v105
	v_pk_fma_f16 v104, v104, v62, v106
	v_pk_fma_f16 v94, v94, v62, v98
	v_cvt_scalef32_pk_f16_fp4 v98, v95, 1.0
	v_cvt_scalef32_pk_f16_fp4 v105, v95, 1.0 op_sel:[1,0,0]
	v_cvt_scalef32_pk_f16_fp4 v106, v95, 1.0 op_sel:[0,1,0]
	v_cvt_scalef32_pk_f16_fp4 v95, v95, 1.0 op_sel:[1,1,0]
	v_pk_fma_f16 v100, v110, v62, v100
	v_pk_fma_f16 v98, v98, v62, v107
	v_pk_fma_f16 v105, v105, v62, v108
	v_pk_fma_f16 v106, v106, v62, v109
	v_pk_fma_f16 v62, v95, v62, v99
	v_mul_u32_u24_sdwa v95, v63, s93 dst_sel:DWORD dst_unused:UNUSED_PAD src0_sel:WORD_0 src1_sel:DWORD
	v_cvt_scalef32_pk_f16_fp4 v99, v84, 1.0
	v_pk_fma_f16 v78, v99, v95, v78
	v_cvt_scalef32_pk_f16_fp4 v99, v84, 1.0 op_sel:[1,0,0]
	v_pk_fma_f16 v79, v99, v95, v79
	v_cvt_scalef32_pk_f16_fp4 v99, v84, 1.0 op_sel:[0,1,0]
	v_cvt_scalef32_pk_f16_fp4 v84, v84, 1.0 op_sel:[1,1,0]
	v_pk_fma_f16 v84, v84, v95, v92
	v_cvt_scalef32_pk_f16_fp4 v92, v85, 1.0
	v_pk_fma_f16 v99, v99, v95, v100
	v_pk_fma_f16 v92, v92, v95, v96
	v_cvt_scalef32_pk_f16_fp4 v96, v85, 1.0 op_sel:[1,0,0]
	v_cvt_scalef32_pk_f16_fp4 v100, v85, 1.0 op_sel:[0,1,0]
	v_cvt_scalef32_pk_f16_fp4 v85, v85, 1.0 op_sel:[1,1,0]
	v_pk_fma_f16 v85, v85, v95, v93
	v_cvt_scalef32_pk_f16_fp4 v93, v86, 1.0
	v_pk_fma_f16 v96, v96, v95, v101
	v_pk_fma_f16 v93, v93, v95, v97
	v_cvt_scalef32_pk_f16_fp4 v97, v86, 1.0 op_sel:[1,0,0]
	v_cvt_scalef32_pk_f16_fp4 v101, v86, 1.0 op_sel:[0,1,0]
	v_cvt_scalef32_pk_f16_fp4 v86, v86, 1.0 op_sel:[1,1,0]
	v_pk_fma_f16 v86, v86, v95, v94
	v_cvt_scalef32_pk_f16_fp4 v94, v87, 1.0
	v_pk_fma_f16 v100, v100, v95, v102
	v_pk_fma_f16 v94, v94, v95, v98
	v_cvt_scalef32_pk_f16_fp4 v98, v87, 1.0 op_sel:[1,0,0]
	v_cvt_scalef32_pk_f16_fp4 v102, v87, 1.0 op_sel:[0,1,0]
	v_cvt_scalef32_pk_f16_fp4 v87, v87, 1.0 op_sel:[1,1,0]
	v_pk_fma_f16 v62, v87, v95, v62
	v_mul_u32_u24_sdwa v63, v63, s93 dst_sel:DWORD dst_unused:UNUSED_PAD src0_sel:WORD_1 src1_sel:DWORD
	v_cvt_scalef32_pk_f16_fp4 v87, v74, 1.0
	v_pk_fma_f16 v78, v87, v63, v78
	v_cvt_scalef32_pk_f16_fp4 v87, v74, 1.0 op_sel:[1,0,0]
	v_pk_fma_f16 v79, v87, v63, v79
	v_cvt_scalef32_pk_f16_fp4 v87, v74, 1.0 op_sel:[0,1,0]
	v_cvt_scalef32_pk_f16_fp4 v74, v74, 1.0 op_sel:[1,1,0]
	v_pk_fma_f16 v74, v74, v63, v84
	v_cvt_scalef32_pk_f16_fp4 v84, v75, 1.0
	v_pk_fma_f16 v97, v97, v95, v103
	v_pk_fma_f16 v101, v101, v95, v104
	v_pk_fma_f16 v98, v98, v95, v105
	v_pk_fma_f16 v102, v102, v95, v106
	v_pk_fma_f16 v84, v84, v63, v92
	v_cvt_scalef32_pk_f16_fp4 v92, v75, 1.0 op_sel:[1,0,0]
	v_cvt_scalef32_pk_f16_fp4 v95, v75, 1.0 op_sel:[0,1,0]
	v_cvt_scalef32_pk_f16_fp4 v75, v75, 1.0 op_sel:[1,1,0]
	v_pk_fma_f16 v75, v75, v63, v85
	v_cvt_scalef32_pk_f16_fp4 v85, v76, 1.0
	v_pk_fma_f16 v92, v92, v63, v96
	v_pk_fma_f16 v85, v85, v63, v93
	v_cvt_scalef32_pk_f16_fp4 v93, v76, 1.0 op_sel:[1,0,0]
	v_cvt_scalef32_pk_f16_fp4 v96, v76, 1.0 op_sel:[0,1,0]
	v_cvt_scalef32_pk_f16_fp4 v76, v76, 1.0 op_sel:[1,1,0]
	v_pk_fma_f16 v76, v76, v63, v86
	v_cvt_scalef32_pk_f16_fp4 v86, v77, 1.0
	v_pk_fma_f16 v93, v93, v63, v97
	v_pk_fma_f16 v86, v86, v63, v94
	v_cvt_scalef32_pk_f16_fp4 v94, v77, 1.0 op_sel:[1,0,0]
	v_cvt_scalef32_pk_f16_fp4 v97, v77, 1.0 op_sel:[0,1,0]
	v_cvt_scalef32_pk_f16_fp4 v77, v77, 1.0 op_sel:[1,1,0]
	v_pk_fma_f16 v87, v87, v63, v99
	v_pk_fma_f16 v95, v95, v63, v100
	v_pk_fma_f16 v96, v96, v63, v101
	v_pk_fma_f16 v94, v94, v63, v98
	v_pk_fma_f16 v97, v97, v63, v102
	v_pk_fma_f16 v62, v77, v63, v62
	v_mul_u32_u24_sdwa v63, v64, s93 dst_sel:DWORD dst_unused:UNUSED_PAD src0_sel:WORD_0 src1_sel:DWORD
	v_cvt_scalef32_pk_f16_fp4 v77, v70, 1.0
	v_pk_fma_f16 v77, v77, v63, v78
	v_cvt_scalef32_pk_f16_fp4 v78, v70, 1.0 op_sel:[1,0,0]
	v_pk_fma_f16 v78, v78, v63, v79
	v_cvt_scalef32_pk_f16_fp4 v79, v70, 1.0 op_sel:[0,1,0]
	v_cvt_scalef32_pk_f16_fp4 v70, v70, 1.0 op_sel:[1,1,0]
	v_pk_fma_f16 v70, v70, v63, v74
	v_cvt_scalef32_pk_f16_fp4 v74, v71, 1.0
	v_pk_fma_f16 v79, v79, v63, v87
	v_pk_fma_f16 v74, v74, v63, v84
	v_cvt_scalef32_pk_f16_fp4 v84, v71, 1.0 op_sel:[1,0,0]
	v_cvt_scalef32_pk_f16_fp4 v87, v71, 1.0 op_sel:[0,1,0]
	v_cvt_scalef32_pk_f16_fp4 v71, v71, 1.0 op_sel:[1,1,0]
	v_pk_fma_f16 v71, v71, v63, v75
	v_cvt_scalef32_pk_f16_fp4 v75, v72, 1.0
	v_pk_fma_f16 v84, v84, v63, v92
	v_pk_fma_f16 v75, v75, v63, v85
	v_cvt_scalef32_pk_f16_fp4 v85, v72, 1.0 op_sel:[1,0,0]
	v_cvt_scalef32_pk_f16_fp4 v92, v72, 1.0 op_sel:[0,1,0]
	v_cvt_scalef32_pk_f16_fp4 v72, v72, 1.0 op_sel:[1,1,0]
	v_pk_fma_f16 v72, v72, v63, v76
	v_cvt_scalef32_pk_f16_fp4 v76, v73, 1.0
	v_pk_fma_f16 v85, v85, v63, v93
	v_pk_fma_f16 v76, v76, v63, v86
	v_cvt_scalef32_pk_f16_fp4 v86, v73, 1.0 op_sel:[1,0,0]
	v_cvt_scalef32_pk_f16_fp4 v93, v73, 1.0 op_sel:[0,1,0]
	v_cvt_scalef32_pk_f16_fp4 v73, v73, 1.0 op_sel:[1,1,0]
	v_pk_fma_f16 v87, v87, v63, v95
	v_pk_fma_f16 v92, v92, v63, v96
	v_pk_fma_f16 v86, v86, v63, v94
	v_pk_fma_f16 v93, v93, v63, v97
	v_pk_fma_f16 v62, v73, v63, v62
	v_mul_u32_u24_sdwa v63, v64, s93 dst_sel:DWORD dst_unused:UNUSED_PAD src0_sel:WORD_1 src1_sel:DWORD
	v_cvt_scalef32_pk_f16_fp4 v64, v66, 1.0
	v_pk_fma_f16 v64, v64, v63, v77
	v_cvt_scalef32_pk_f16_fp4 v73, v66, 1.0 op_sel:[1,0,0]
	v_cvt_scalef32_pk_f16_fp4 v77, v66, 1.0 op_sel:[0,1,0]
	v_cvt_scalef32_pk_f16_fp4 v66, v66, 1.0 op_sel:[1,1,0]
	v_pk_fma_f16 v66, v66, v63, v70
	v_cvt_scalef32_pk_f16_fp4 v70, v67, 1.0
	v_pk_fma_f16 v73, v73, v63, v78
	v_pk_fma_f16 v70, v70, v63, v74
	v_cvt_scalef32_pk_f16_fp4 v74, v67, 1.0 op_sel:[1,0,0]
	v_cvt_scalef32_pk_f16_fp4 v78, v67, 1.0 op_sel:[0,1,0]
	v_cvt_scalef32_pk_f16_fp4 v67, v67, 1.0 op_sel:[1,1,0]
	v_pk_fma_f16 v67, v67, v63, v71
	v_cvt_scalef32_pk_f16_fp4 v71, v68, 1.0
	v_pk_fma_f16 v77, v77, v63, v79
	v_pk_fma_f16 v71, v71, v63, v75
	v_cvt_scalef32_pk_f16_fp4 v75, v68, 1.0 op_sel:[1,0,0]
	v_cvt_scalef32_pk_f16_fp4 v79, v68, 1.0 op_sel:[0,1,0]
	v_cvt_scalef32_pk_f16_fp4 v68, v68, 1.0 op_sel:[1,1,0]
	v_pk_fma_f16 v68, v68, v63, v72
	v_cvt_scalef32_pk_f16_fp4 v72, v69, 1.0
	v_pk_fma_f16 v74, v74, v63, v84
	v_pk_fma_f16 v72, v72, v63, v76
	v_cvt_scalef32_pk_f16_fp4 v76, v69, 1.0 op_sel:[1,0,0]
	v_cvt_scalef32_pk_f16_fp4 v84, v69, 1.0 op_sel:[0,1,0]
	v_cvt_scalef32_pk_f16_fp4 v69, v69, 1.0 op_sel:[1,1,0]
	v_pk_fma_f16 v78, v78, v63, v87
	v_pk_fma_f16 v75, v75, v63, v85
	v_pk_fma_f16 v79, v79, v63, v92
	v_pk_fma_f16 v76, v76, v63, v86
	v_pk_fma_f16 v84, v84, v63, v93
	v_pk_fma_f16 v62, v69, v63, v62
	v_mul_u32_u24_sdwa v63, v65, s93 dst_sel:DWORD dst_unused:UNUSED_PAD src0_sel:WORD_0 src1_sel:DWORD
	v_cvt_scalef32_pk_f16_fp4 v69, v58, 1.0
	v_pk_fma_f16 v64, v69, v63, v64
	v_cvt_scalef32_pk_f16_fp4 v69, v58, 1.0 op_sel:[1,0,0]
	v_pk_fma_f16 v69, v69, v63, v73
	v_cvt_scalef32_pk_f16_fp4 v73, v58, 1.0 op_sel:[0,1,0]
	v_cvt_scalef32_pk_f16_fp4 v58, v58, 1.0 op_sel:[1,1,0]
	v_pk_fma_f16 v58, v58, v63, v66
	v_cvt_scalef32_pk_f16_fp4 v66, v59, 1.0
	v_pk_fma_f16 v66, v66, v63, v70
	v_cvt_scalef32_pk_f16_fp4 v70, v59, 1.0 op_sel:[1,0,0]
	v_pk_fma_f16 v70, v70, v63, v74
	v_cvt_scalef32_pk_f16_fp4 v74, v59, 1.0 op_sel:[0,1,0]
	v_cvt_scalef32_pk_f16_fp4 v59, v59, 1.0 op_sel:[1,1,0]
	v_pk_fma_f16 v59, v59, v63, v67
	v_cvt_scalef32_pk_f16_fp4 v67, v60, 1.0
	v_pk_fma_f16 v67, v67, v63, v71
	v_cvt_scalef32_pk_f16_fp4 v71, v60, 1.0 op_sel:[1,0,0]
	v_pk_fma_f16 v71, v71, v63, v75
	v_cvt_scalef32_pk_f16_fp4 v75, v60, 1.0 op_sel:[0,1,0]
	v_cvt_scalef32_pk_f16_fp4 v60, v60, 1.0 op_sel:[1,1,0]
	v_pk_fma_f16 v60, v60, v63, v68
	v_cvt_scalef32_pk_f16_fp4 v68, v61, 1.0
	v_pk_fma_f16 v68, v68, v63, v72
	v_cvt_scalef32_pk_f16_fp4 v72, v61, 1.0 op_sel:[1,0,0]
	v_pk_fma_f16 v72, v72, v63, v76
	v_cvt_scalef32_pk_f16_fp4 v76, v61, 1.0 op_sel:[0,1,0]
	v_cvt_scalef32_pk_f16_fp4 v61, v61, 1.0 op_sel:[1,1,0]
	v_pk_fma_f16 v93, v61, v63, v62
	v_mul_u32_u24_sdwa v94, v65, s93 dst_sel:DWORD dst_unused:UNUSED_PAD src0_sel:WORD_1 src1_sel:DWORD
	v_cvt_scalef32_pk_f16_fp4 v61, v88, 1.0
	v_pk_fma_f16 v95, v61, v94, v64
	v_cvt_scalef32_pk_f16_fp4 v61, v88, 1.0 op_sel:[1,0,0]
	v_pk_fma_f16 v73, v73, v63, v77
	v_pk_fma_f16 v96, v61, v94, v69
	v_cvt_scalef32_pk_f16_fp4 v61, v88, 1.0 op_sel:[0,1,0]
	v_pk_fma_f16 v97, v61, v94, v73
	v_cvt_scalef32_pk_f16_fp4 v61, v88, 1.0 op_sel:[1,1,0]
	v_pk_fma_f16 v100, v61, v94, v58
	v_cvt_scalef32_pk_f16_fp4 v58, v89, 1.0
	v_pk_fma_f16 v101, v58, v94, v66
	v_cvt_scalef32_pk_f16_fp4 v58, v89, 1.0 op_sel:[1,0,0]
	v_pk_fma_f16 v74, v74, v63, v78
	v_pk_fma_f16 v104, v58, v94, v70
	v_cvt_scalef32_pk_f16_fp4 v58, v89, 1.0 op_sel:[0,1,0]
	v_pk_fma_f16 v105, v58, v94, v74
	v_cvt_scalef32_pk_f16_fp4 v58, v89, 1.0 op_sel:[1,1,0]
	v_pk_fma_f16 v106, v58, v94, v59
	v_cvt_scalef32_pk_f16_fp4 v58, v90, 1.0
	v_pk_fma_f16 v98, v58, v94, v67
	v_cvt_scalef32_pk_f16_fp4 v58, v90, 1.0 op_sel:[1,0,0]
	v_pk_fma_f16 v75, v75, v63, v79
	v_pk_fma_f16 v99, v58, v94, v71
	v_cvt_scalef32_pk_f16_fp4 v58, v90, 1.0 op_sel:[0,1,0]
	v_pk_fma_f16 v102, v58, v94, v75
	v_cvt_scalef32_pk_f16_fp4 v58, v90, 1.0 op_sel:[1,1,0]
	v_pk_fma_f16 v103, v58, v94, v60
	v_cvt_scalef32_pk_f16_fp4 v58, v91, 1.0
	v_pk_fma_f16 v107, v58, v94, v68
	v_cvt_scalef32_pk_f16_fp4 v58, v91, 1.0 op_sel:[1,0,0]
	v_pk_fma_f16 v108, v58, v94, v72
	v_pk_fma_f16 v92, v76, v63, v84
	v_cvt_scalef32_pk_f16_fp4 v90, v91, 1.0 op_sel:[0,1,0]
	v_pk_fma_f16 v109, v90, v94, v92
	v_cvt_scalef32_pk_f16_fp4 v90, v91, 1.0 op_sel:[1,1,0]
	v_permlane32_swap_b32_e32 v96, v99
	v_pk_fma_f16 v110, v90, v94, v93
	v_permlane32_swap_b32_e32 v95, v98
	v_pk_add_f16 v92, v96, v99
	v_permlane32_swap_b32_e32 v97, v102
	v_pk_add_f16 v91, v95, v98
	v_cvt_f32_f16_e32 v98, v92
	v_cvt_f32_f16_sdwa v99, v92 dst_sel:DWORD dst_unused:UNUSED_PAD src0_sel:WORD_1
	v_pk_add_f16 v92, v97, v102
	v_permlane32_swap_b32_e32 v100, v103
	v_permlane32_swap_b32_e32 v101, v107
	v_permlane32_swap_b32_e32 v104, v108
	v_permlane32_swap_b32_e32 v105, v109
	v_permlane32_swap_b32_e32 v106, v110
	v_cvt_f32_f16_e32 v94, v92
	v_cvt_f32_f16_sdwa v95, v92 dst_sel:DWORD dst_unused:UNUSED_PAD src0_sel:WORD_1
	v_pk_add_f16 v92, v100, v103
	v_pk_add_f16 v93, v101, v107
	v_pk_add_f16 v96, v104, v108
	v_pk_add_f16 v97, v105, v109
	v_pk_add_f16 v105, v106, v110
	v_cvt_f32_f16_e32 v90, v91
	v_cvt_f32_f16_sdwa v91, v91 dst_sel:DWORD dst_unused:UNUSED_PAD src0_sel:WORD_1
	v_cvt_f32_f16_e32 v102, v92
	v_cvt_f32_f16_sdwa v103, v92 dst_sel:DWORD dst_unused:UNUSED_PAD src0_sel:WORD_1
	v_cvt_f32_f16_e32 v92, v93
	v_cvt_f32_f16_sdwa v93, v93 dst_sel:DWORD dst_unused:UNUSED_PAD src0_sel:WORD_1
	v_cvt_f32_f16_e32 v100, v96
	v_cvt_f32_f16_sdwa v101, v96 dst_sel:DWORD dst_unused:UNUSED_PAD src0_sel:WORD_1
	v_cvt_f32_f16_e32 v96, v97
	v_cvt_f32_f16_sdwa v97, v97 dst_sel:DWORD dst_unused:UNUSED_PAD src0_sel:WORD_1
	v_cvt_f32_f16_e32 v104, v105
	v_cvt_f32_f16_sdwa v105, v105 dst_sel:DWORD dst_unused:UNUSED_PAD src0_sel:WORD_1
	v_mul_hi_i32 v106, v113, s69
	v_lshrrev_b32_e32 v107, 31, v106
	v_ashrrev_i32_e32 v106, 13, v106
	v_add_u32_e32 v107, v106, v107
	v_permlane16_swap_b32_e32 v90, v92
	v_permlane16_swap_b32_e32 v91, v93
	v_permlane16_swap_b32_e32 v98, v100
	v_permlane16_swap_b32_e32 v99, v101
	v_permlane16_swap_b32_e32 v94, v96
	v_permlane16_swap_b32_e32 v95, v97
	v_permlane16_swap_b32_e32 v102, v104
	v_permlane16_swap_b32_e32 v103, v105
	v_mul_i32_i24_e32 v110, 0xffffbf00, v107
	v_pk_add_f32 v[92:93], v[90:91], v[92:93]
	v_pk_add_f32 v[90:91], v[94:95], v[96:97]
	v_pk_add_f32 v[100:101], v[98:99], v[100:101]
	v_pk_add_f32 v[98:99], v[102:103], v[104:105]
	v_add3_u32 v106, v112, v110, s33
	v_mov_b32_dpp v96, v92 row_ror:8 row_mask:0xf bank_mask:0xf bound_ctrl:1
	v_mov_b32_dpp v94, v90 row_ror:8 row_mask:0xf bank_mask:0xf bound_ctrl:1
	v_mov_b32_dpp v97, v93 row_ror:8 row_mask:0xf bank_mask:0xf bound_ctrl:1
	v_mov_b32_dpp v95, v91 row_ror:8 row_mask:0xf bank_mask:0xf bound_ctrl:1
	v_mov_b32_dpp v104, v100 row_ror:8 row_mask:0xf bank_mask:0xf bound_ctrl:1
	v_mov_b32_dpp v102, v98 row_ror:8 row_mask:0xf bank_mask:0xf bound_ctrl:1
	v_mov_b32_dpp v105, v101 row_ror:8 row_mask:0xf bank_mask:0xf bound_ctrl:1
	v_mov_b32_dpp v103, v99 row_ror:8 row_mask:0xf bank_mask:0xf bound_ctrl:1
	v_cmp_lt_i32_e64 s[0:1], s21, v106
	s_and_saveexec_b64 s[2:3], s[0:1]
	s_xor_b64 s[0:1], exec, s[2:3]
	s_or_saveexec_b64 s[0:1], s[0:1]
	s_xor_b64 exec, exec, s[0:1]
	s_or_b64 exec, exec, s[0:1]
	s_nop 0
	v_pk_add_f32 v[92:93], v[92:93], v[96:97]
	v_pk_add_f32 v[96:97], v[100:101], v[104:105]
	v_pk_add_f32 v[90:91], v[90:91], v[94:95]
	v_pk_add_f32 v[94:95], v[98:99], v[102:103]
	v_cndmask_b32_e64 v91, v91, v93, s[38:39]
	v_cndmask_b32_e64 v95, v95, v97, s[38:39]
	v_cndmask_b32_e64 v94, v94, v96, s[38:39]
	v_cndmask_b32_e64 v90, v90, v92, s[38:39]
	s_waitcnt vmcnt(2)
	v_mul_u32_u24_sdwa v98, v50, s93 dst_sel:DWORD dst_unused:UNUSED_PAD src0_sel:WORD_0 src1_sel:DWORD
	v_mul_u32_u24_sdwa v97, v50, s93 dst_sel:DWORD dst_unused:UNUSED_PAD src0_sel:WORD_1 src1_sel:DWORD
	v_mul_u32_u24_sdwa v96, v51, s93 dst_sel:DWORD dst_unused:UNUSED_PAD src0_sel:WORD_1 src1_sel:DWORD
	v_mul_u32_u24_sdwa v51, v51, s93 dst_sel:DWORD dst_unused:UNUSED_PAD src0_sel:WORD_0 src1_sel:DWORD
	s_waitcnt vmcnt(2)
	v_cvt_scalef32_pk_f16_fp4 v119, v143, 1.0 op_sel:[1,1,0]
	s_waitcnt vmcnt(2)
	v_cvt_scalef32_pk_f16_fp4 v111, v147, 1.0 op_sel:[1,1,0]
	s_waitcnt vmcnt(2)
	v_cvt_scalef32_pk_f16_fp4 v105, v167, 1.0 op_sel:[1,1,0]
	s_waitcnt vmcnt(2)
	v_cvt_scalef32_pk_f16_fp4 v104, v171, 1.0 op_sel:[1,1,0]
	s_waitcnt vmcnt(2)
	v_cvt_scalef32_pk_f16_fp4 v103, v175, 1.0 op_sel:[1,1,0]
	s_waitcnt vmcnt(2)
	v_cvt_scalef32_pk_f16_fp4 v102, v179, 1.0 op_sel:[1,1,0]
	s_waitcnt vmcnt(2)
	v_cvt_scalef32_pk_f16_fp4 v101, v183, 1.0 op_sel:[1,1,0]
	s_waitcnt vmcnt(2)
	v_cvt_scalef32_pk_f16_fp4 v100, v187, 1.0 op_sel:[1,1,0]
	s_waitcnt vmcnt(2)
	v_cvt_scalef32_pk_f16_fp4 v99, v191, 1.0 op_sel:[1,1,0]
	v_add_u32_e32 v110, 1, v113
	s_waitcnt vmcnt(0)
	v_pk_fma_f32 v[92:93], v[202:203], v[94:95], v[198:199]
	v_cvt_scalef32_pk_f16_fp4 v124, v131, 1.0 op_sel:[1,1,0]
	v_pk_fma_f32 v[90:91], v[200:201], v[90:91], v[196:197]
	v_cvt_scalef32_pk_f16_fp4 v123, v135, 1.0 op_sel:[1,1,0]
	v_pk_fma_f16 v50, v124, v98, 0
	v_cvt_scalef32_pk_f16_fp4 v124, v131, 1.0 op_sel:[0,1,0]
	v_cvt_scalef32_pk_f16_fp4 v122, v139, 1.0 op_sel:[1,1,0]
	v_pk_fma_f16 v50, v123, v97, v50
	v_cvt_scalef32_pk_f16_fp4 v123, v135, 1.0 op_sel:[0,1,0]
	v_pk_fma_f16 v124, v124, v98, 0
	v_cvt_scalef32_pk_f16_fp4 v125, v131, 1.0 op_sel:[1,0,0]
	v_pk_fma_f16 v50, v122, v51, v50
	v_cvt_scalef32_pk_f16_fp4 v122, v139, 1.0 op_sel:[0,1,0]
	v_pk_fma_f16 v123, v123, v97, v124
	v_cvt_scalef32_pk_f16_fp4 v124, v135, 1.0 op_sel:[1,0,0]
	v_pk_fma_f16 v125, v125, v98, 0
	v_cvt_scalef32_pk_f16_fp4 v21, v131, 1.0
	v_mul_u32_u24_sdwa v95, v52, s93 dst_sel:DWORD dst_unused:UNUSED_PAD src0_sel:WORD_1 src1_sel:DWORD
	v_mul_u32_u24_sdwa v52, v52, s93 dst_sel:DWORD dst_unused:UNUSED_PAD src0_sel:WORD_0 src1_sel:DWORD
	v_pk_fma_f16 v50, v119, v96, v50
	v_cvt_scalef32_pk_f16_fp4 v119, v143, 1.0 op_sel:[0,1,0]
	v_pk_fma_f16 v122, v122, v51, v123
	v_cvt_scalef32_pk_f16_fp4 v123, v139, 1.0 op_sel:[1,0,0]
	v_pk_fma_f16 v124, v124, v97, v125
	v_cvt_scalef32_pk_f16_fp4 v25, v135, 1.0
	v_pk_fma_f16 v21, v21, v98, 0
	v_cvt_scalef32_pk_f16_fp4 v109, v151, 1.0 op_sel:[1,1,0]
	v_pk_fma_f16 v50, v111, v52, v50
	v_cvt_scalef32_pk_f16_fp4 v111, v147, 1.0 op_sel:[0,1,0]
	v_pk_fma_f16 v119, v119, v96, v122
	v_cvt_scalef32_pk_f16_fp4 v122, v143, 1.0 op_sel:[1,0,0]
	v_pk_fma_f16 v123, v123, v51, v124
	v_cvt_scalef32_pk_f16_fp4 v29, v139, 1.0
	v_pk_fma_f16 v21, v25, v97, v21
	v_mul_u32_u24_sdwa v94, v53, s93 dst_sel:DWORD dst_unused:UNUSED_PAD src0_sel:WORD_1 src1_sel:DWORD
	v_cvt_scalef32_pk_f16_fp4 v108, v155, 1.0 op_sel:[1,1,0]
	v_mul_u32_u24_sdwa v53, v53, s93 dst_sel:DWORD dst_unused:UNUSED_PAD src0_sel:WORD_0 src1_sel:DWORD
	v_pk_fma_f16 v50, v109, v95, v50
	v_cvt_scalef32_pk_f16_fp4 v109, v151, 1.0 op_sel:[0,1,0]
	v_pk_fma_f16 v111, v111, v52, v119
	v_cvt_scalef32_pk_f16_fp4 v119, v147, 1.0 op_sel:[1,0,0]
	v_pk_fma_f16 v122, v122, v96, v123
	v_cvt_scalef32_pk_f16_fp4 v33, v143, 1.0
	v_pk_fma_f16 v21, v29, v51, v21
	v_cvt_scalef32_pk_f16_fp4 v107, v159, 1.0 op_sel:[1,1,0]
	v_pk_fma_f16 v50, v108, v53, v50
	v_cvt_scalef32_pk_f16_fp4 v108, v155, 1.0 op_sel:[0,1,0]
	v_pk_fma_f16 v109, v109, v95, v111
	v_cvt_scalef32_pk_f16_fp4 v111, v151, 1.0 op_sel:[1,0,0]
	v_pk_fma_f16 v119, v119, v52, v122
	v_cvt_scalef32_pk_f16_fp4 v37, v147, 1.0
	v_pk_fma_f16 v21, v33, v96, v21
	global_store_dwordx4 v[204:205], v[90:93], off
	v_add_u32_e32 v218, 1, v113
	v_mul_hi_i32 v244, v218, s69
	v_lshrrev_b32_e32 v245, 31, v244
	v_ashrrev_i32_e32 v244, 13, v244
	v_add_u32_e32 v245, v244, v245
	v_mul_i32_i24_e32 v248, 0xffffbf00, v245
	v_add_u32_e32 v244, v218, v248
	v_cmp_gt_i32_e32 vcc, s68, v244
	v_cmp_lt_i32_e64 s[0:1], s21, v244
	s_and_saveexec_b64 s[2:3], s[0:1]
	s_xor_b64 s[0:1], exec, s[2:3]
	v_lshl_add_u32 v244, v245, 14, v248
	v_add3_u32 v244, v218, v244, s88
	s_or_saveexec_b64 s[0:1], s[0:1]
	v_mov_b64_e32 v[246:247], s[18:19]
	s_xor_b64 exec, exec, s[0:1]
	v_lshlrev_b32_e32 v244, 8, v245
	v_add3_u32 v244, v248, v218, v244
	v_mov_b64_e32 v[246:247], s[72:73]
	s_or_b64 exec, exec, s[0:1]
	v_mul_i32_i24_e32 v245, 0x3000, v245
	v_cndmask_b32_e32 v248, v245, v223, vcc
	v_ashrrev_i32_e32 v249, 31, v248
	v_lshl_add_u64 v[248:249], v[248:249], 2, s[10:11]
	v_lshlrev_b32_e32 v210, 2, v118
	v_ashrrev_i32_e32 v245, 31, v244
	v_lshl_add_u64 v[250:251], v[248:249], 0, v[210:211]
	v_lshlrev_b64 v[244:245], 13, v[244:245]
	v_lshl_add_u64 v[244:245], v[246:247], 0, v[244:245]
	v_add_co_u32_e32 v250, vcc, s94, v250
	v_lshl_add_u64 v[204:205], v[244:245], 0, v[210:211]
	s_nop 0
	v_addc_co_u32_e32 v251, vcc, 0, v251, vcc
	global_load_dwordx4 v[234:237], v[204:205], off
	global_load_dwordx4 v[238:241], v[250:251], off
	v_cvt_scalef32_pk_f16_fp4 v106, v163, 1.0 op_sel:[1,1,0]
	v_pk_fma_f16 v50, v107, v94, v50
	v_mul_u32_u24_sdwa v93, v54, s93 dst_sel:DWORD dst_unused:UNUSED_PAD src0_sel:WORD_1 src1_sel:DWORD
	v_mul_u32_u24_sdwa v54, v54, s93 dst_sel:DWORD dst_unused:UNUSED_PAD src0_sel:WORD_0 src1_sel:DWORD
	v_cvt_scalef32_pk_f16_fp4 v107, v159, 1.0 op_sel:[0,1,0]
	v_pk_fma_f16 v108, v108, v53, v109
	v_cvt_scalef32_pk_f16_fp4 v109, v155, 1.0 op_sel:[1,0,0]
	v_pk_fma_f16 v111, v111, v95, v119
	v_cvt_scalef32_pk_f16_fp4 v41, v151, 1.0
	v_pk_fma_f16 v21, v37, v52, v21
	v_pk_fma_f16 v50, v106, v54, v50
	v_cvt_scalef32_pk_f16_fp4 v106, v163, 1.0 op_sel:[0,1,0]
	v_pk_fma_f16 v107, v107, v94, v108
	v_cvt_scalef32_pk_f16_fp4 v108, v159, 1.0 op_sel:[1,0,0]
	v_pk_fma_f16 v109, v109, v53, v111
	v_cvt_scalef32_pk_f16_fp4 v45, v155, 1.0
	v_pk_fma_f16 v21, v41, v95, v21
	v_mul_u32_u24_sdwa v92, v55, s93 dst_sel:DWORD dst_unused:UNUSED_PAD src0_sel:WORD_1 src1_sel:DWORD
	v_mul_u32_u24_sdwa v55, v55, s93 dst_sel:DWORD dst_unused:UNUSED_PAD src0_sel:WORD_0 src1_sel:DWORD
	v_pk_fma_f16 v50, v105, v93, v50
	v_cvt_scalef32_pk_f16_fp4 v105, v167, 1.0 op_sel:[0,1,0]
	v_pk_fma_f16 v106, v106, v54, v107
	v_cvt_scalef32_pk_f16_fp4 v107, v163, 1.0 op_sel:[1,0,0]
	v_pk_fma_f16 v108, v108, v94, v109
	v_cvt_scalef32_pk_f16_fp4 v49, v159, 1.0
	v_pk_fma_f16 v21, v45, v53, v21
	v_pk_fma_f16 v50, v104, v55, v50
	v_cvt_scalef32_pk_f16_fp4 v104, v171, 1.0 op_sel:[0,1,0]
	v_pk_fma_f16 v105, v105, v93, v106
	v_cvt_scalef32_pk_f16_fp4 v106, v167, 1.0 op_sel:[1,0,0]
	v_pk_fma_f16 v107, v107, v54, v108
	v_cvt_scalef32_pk_f16_fp4 v61, v163, 1.0
	v_pk_fma_f16 v21, v49, v94, v21
	v_mul_u32_u24_sdwa v91, v56, s93 dst_sel:DWORD dst_unused:UNUSED_PAD src0_sel:WORD_1 src1_sel:DWORD
	v_mul_u32_u24_sdwa v56, v56, s93 dst_sel:DWORD dst_unused:UNUSED_PAD src0_sel:WORD_0 src1_sel:DWORD
	v_pk_fma_f16 v50, v103, v92, v50
	v_cvt_scalef32_pk_f16_fp4 v103, v175, 1.0 op_sel:[0,1,0]
	v_pk_fma_f16 v104, v104, v55, v105
	v_cvt_scalef32_pk_f16_fp4 v105, v171, 1.0 op_sel:[1,0,0]
	v_pk_fma_f16 v106, v106, v93, v107
	v_cvt_scalef32_pk_f16_fp4 v65, v167, 1.0
	v_pk_fma_f16 v21, v61, v54, v21
	v_pk_fma_f16 v50, v102, v56, v50
	v_cvt_scalef32_pk_f16_fp4 v102, v179, 1.0 op_sel:[0,1,0]
	v_pk_fma_f16 v103, v103, v92, v104
	v_cvt_scalef32_pk_f16_fp4 v104, v175, 1.0 op_sel:[1,0,0]
	v_pk_fma_f16 v105, v105, v55, v106
	v_cvt_scalef32_pk_f16_fp4 v69, v171, 1.0
	v_pk_fma_f16 v21, v65, v93, v21
	v_mul_u32_u24_sdwa v90, v57, s93 dst_sel:DWORD dst_unused:UNUSED_PAD src0_sel:WORD_1 src1_sel:DWORD
	v_mul_u32_u24_sdwa v57, v57, s93 dst_sel:DWORD dst_unused:UNUSED_PAD src0_sel:WORD_0 src1_sel:DWORD
	v_pk_fma_f16 v50, v101, v91, v50
	v_cvt_scalef32_pk_f16_fp4 v101, v183, 1.0 op_sel:[0,1,0]
	v_pk_fma_f16 v102, v102, v56, v103
	v_cvt_scalef32_pk_f16_fp4 v103, v179, 1.0 op_sel:[1,0,0]
	v_pk_fma_f16 v104, v104, v92, v105
	v_cvt_scalef32_pk_f16_fp4 v73, v175, 1.0
	v_pk_fma_f16 v21, v69, v55, v21
	v_pk_fma_f16 v50, v100, v57, v50
	v_cvt_scalef32_pk_f16_fp4 v100, v187, 1.0 op_sel:[0,1,0]
	v_pk_fma_f16 v101, v101, v91, v102
	v_cvt_scalef32_pk_f16_fp4 v102, v183, 1.0 op_sel:[1,0,0]
	v_pk_fma_f16 v103, v103, v56, v104
	v_cvt_scalef32_pk_f16_fp4 v77, v179, 1.0
	v_pk_fma_f16 v21, v73, v92, v21
	v_pk_fma_f16 v50, v99, v90, v50
	v_cvt_scalef32_pk_f16_fp4 v99, v191, 1.0 op_sel:[0,1,0]
	v_pk_fma_f16 v100, v100, v57, v101
	v_cvt_scalef32_pk_f16_fp4 v101, v187, 1.0 op_sel:[1,0,0]
	v_pk_fma_f16 v102, v102, v91, v103
	v_cvt_scalef32_pk_f16_fp4 v81, v183, 1.0
	v_pk_fma_f16 v21, v77, v56, v21
	v_pk_fma_f16 v99, v99, v90, v100
	v_cvt_scalef32_pk_f16_fp4 v100, v191, 1.0 op_sel:[1,0,0]
	v_pk_fma_f16 v101, v101, v57, v102
	v_cvt_scalef32_pk_f16_fp4 v85, v187, 1.0
	v_pk_fma_f16 v21, v81, v91, v21
	v_pk_fma_f16 v100, v100, v90, v101
	v_cvt_scalef32_pk_f16_fp4 v89, v191, 1.0
	v_pk_fma_f16 v21, v85, v57, v21
	v_cvt_scalef32_pk_f16_fp4 v101, v130, 1.0 op_sel:[1,1,0]
	v_pk_fma_f16 v21, v89, v90, v21
	v_cvt_scalef32_pk_f16_fp4 v89, v134, 1.0 op_sel:[1,1,0]
	v_pk_fma_f16 v101, v101, v98, 0
	v_cvt_scalef32_pk_f16_fp4 v102, v130, 1.0 op_sel:[0,1,0]
	v_cvt_scalef32_pk_f16_fp4 v85, v138, 1.0 op_sel:[1,1,0]
	v_pk_fma_f16 v89, v89, v97, v101
	v_cvt_scalef32_pk_f16_fp4 v101, v134, 1.0 op_sel:[0,1,0]
	v_pk_fma_f16 v102, v102, v98, 0
	v_cvt_scalef32_pk_f16_fp4 v103, v130, 1.0 op_sel:[1,0,0]
	v_cvt_scalef32_pk_f16_fp4 v81, v142, 1.0 op_sel:[1,1,0]
	v_pk_fma_f16 v85, v85, v51, v89
	v_cvt_scalef32_pk_f16_fp4 v89, v138, 1.0 op_sel:[0,1,0]
	v_pk_fma_f16 v101, v101, v97, v102
	v_cvt_scalef32_pk_f16_fp4 v102, v134, 1.0 op_sel:[1,0,0]
	v_pk_fma_f16 v103, v103, v98, 0
	v_cvt_scalef32_pk_f16_fp4 v20, v130, 1.0
	v_cvt_scalef32_pk_f16_fp4 v77, v146, 1.0 op_sel:[1,1,0]
	v_pk_fma_f16 v81, v81, v96, v85
	v_cvt_scalef32_pk_f16_fp4 v85, v142, 1.0 op_sel:[0,1,0]
	v_pk_fma_f16 v89, v89, v51, v101
	v_cvt_scalef32_pk_f16_fp4 v101, v138, 1.0 op_sel:[1,0,0]
	v_pk_fma_f16 v102, v102, v97, v103
	v_cvt_scalef32_pk_f16_fp4 v24, v134, 1.0
	v_pk_fma_f16 v20, v20, v98, 0
	v_cvt_scalef32_pk_f16_fp4 v73, v150, 1.0 op_sel:[1,1,0]
	v_pk_fma_f16 v77, v77, v52, v81
	v_cvt_scalef32_pk_f16_fp4 v81, v146, 1.0 op_sel:[0,1,0]
	v_pk_fma_f16 v85, v85, v96, v89
	v_cvt_scalef32_pk_f16_fp4 v89, v142, 1.0 op_sel:[1,0,0]
	v_pk_fma_f16 v101, v101, v51, v102
	v_cvt_scalef32_pk_f16_fp4 v28, v138, 1.0
	v_pk_fma_f16 v20, v24, v97, v20
	v_cvt_scalef32_pk_f16_fp4 v69, v154, 1.0 op_sel:[1,1,0]
	v_pk_fma_f16 v73, v73, v95, v77
	v_cvt_scalef32_pk_f16_fp4 v77, v150, 1.0 op_sel:[0,1,0]
	v_pk_fma_f16 v81, v81, v52, v85
	v_cvt_scalef32_pk_f16_fp4 v85, v146, 1.0 op_sel:[1,0,0]
	v_pk_fma_f16 v89, v89, v96, v101
	v_cvt_scalef32_pk_f16_fp4 v32, v142, 1.0
	v_pk_fma_f16 v20, v28, v51, v20
	v_cvt_scalef32_pk_f16_fp4 v65, v158, 1.0 op_sel:[1,1,0]
	v_pk_fma_f16 v69, v69, v53, v73
	v_cvt_scalef32_pk_f16_fp4 v73, v154, 1.0 op_sel:[0,1,0]
	v_pk_fma_f16 v77, v77, v95, v81
	v_cvt_scalef32_pk_f16_fp4 v81, v150, 1.0 op_sel:[1,0,0]
	v_pk_fma_f16 v85, v85, v52, v89
	v_cvt_scalef32_pk_f16_fp4 v36, v146, 1.0
	v_pk_fma_f16 v20, v32, v96, v20
	v_cvt_scalef32_pk_f16_fp4 v61, v162, 1.0 op_sel:[1,1,0]
	v_pk_fma_f16 v65, v65, v94, v69
	v_cvt_scalef32_pk_f16_fp4 v69, v158, 1.0 op_sel:[0,1,0]
	v_pk_fma_f16 v73, v73, v53, v77
	v_cvt_scalef32_pk_f16_fp4 v77, v154, 1.0 op_sel:[1,0,0]
	v_pk_fma_f16 v81, v81, v95, v85
	v_cvt_scalef32_pk_f16_fp4 v40, v150, 1.0
	v_pk_fma_f16 v20, v36, v52, v20
	v_cvt_scalef32_pk_f16_fp4 v49, v166, 1.0 op_sel:[1,1,0]
	v_pk_fma_f16 v61, v61, v54, v65
	v_cvt_scalef32_pk_f16_fp4 v65, v162, 1.0 op_sel:[0,1,0]
	v_pk_fma_f16 v69, v69, v94, v73
	v_cvt_scalef32_pk_f16_fp4 v73, v158, 1.0 op_sel:[1,0,0]
	v_pk_fma_f16 v77, v77, v53, v81
	v_cvt_scalef32_pk_f16_fp4 v44, v154, 1.0
	v_pk_fma_f16 v20, v40, v95, v20
	v_cvt_scalef32_pk_f16_fp4 v45, v170, 1.0 op_sel:[1,1,0]
	v_pk_fma_f16 v49, v49, v93, v61
	v_cvt_scalef32_pk_f16_fp4 v61, v166, 1.0 op_sel:[0,1,0]
	v_pk_fma_f16 v65, v65, v54, v69
	v_cvt_scalef32_pk_f16_fp4 v69, v162, 1.0 op_sel:[1,0,0]
	v_pk_fma_f16 v73, v73, v94, v77
	v_cvt_scalef32_pk_f16_fp4 v48, v158, 1.0
	v_pk_fma_f16 v20, v44, v53, v20
	v_pk_fma_f16 v45, v45, v55, v49
	v_cvt_scalef32_pk_f16_fp4 v49, v170, 1.0 op_sel:[0,1,0]
	v_pk_fma_f16 v61, v61, v93, v65
	v_cvt_scalef32_pk_f16_fp4 v65, v166, 1.0 op_sel:[1,0,0]
	v_pk_fma_f16 v69, v69, v54, v73
	v_cvt_scalef32_pk_f16_fp4 v60, v162, 1.0
	v_pk_fma_f16 v20, v48, v94, v20
	v_cvt_scalef32_pk_f16_fp4 v41, v174, 1.0 op_sel:[1,1,0]
	v_pk_fma_f16 v49, v49, v55, v61
	v_cvt_scalef32_pk_f16_fp4 v61, v170, 1.0 op_sel:[1,0,0]
	v_pk_fma_f16 v65, v65, v93, v69
	v_cvt_scalef32_pk_f16_fp4 v64, v166, 1.0
	v_pk_fma_f16 v20, v60, v54, v20
	v_pk_fma_f16 v41, v41, v92, v45
	v_cvt_scalef32_pk_f16_fp4 v45, v174, 1.0 op_sel:[0,1,0]
	v_pk_fma_f16 v61, v61, v55, v65
	v_cvt_scalef32_pk_f16_fp4 v65, v170, 1.0
	v_pk_fma_f16 v20, v64, v93, v20
	v_cvt_scalef32_pk_f16_fp4 v68, v129, 1.0 op_sel:[1,1,0]
	v_cvt_scalef32_pk_f16_fp4 v37, v178, 1.0 op_sel:[1,1,0]
	v_pk_fma_f16 v45, v45, v92, v49
	v_cvt_scalef32_pk_f16_fp4 v49, v174, 1.0 op_sel:[1,0,0]
	v_pk_fma_f16 v20, v65, v55, v20
	v_cvt_scalef32_pk_f16_fp4 v65, v133, 1.0 op_sel:[1,1,0]
	v_pk_fma_f16 v68, v68, v98, 0
	v_cvt_scalef32_pk_f16_fp4 v69, v129, 1.0 op_sel:[0,1,0]
	v_pk_fma_f16 v37, v37, v56, v41
	v_cvt_scalef32_pk_f16_fp4 v41, v178, 1.0 op_sel:[0,1,0]
	v_pk_fma_f16 v49, v49, v92, v61
	v_cvt_scalef32_pk_f16_fp4 v61, v174, 1.0
	v_cvt_scalef32_pk_f16_fp4 v64, v137, 1.0 op_sel:[1,1,0]
	v_pk_fma_f16 v65, v65, v97, v68
	v_cvt_scalef32_pk_f16_fp4 v68, v133, 1.0 op_sel:[0,1,0]
	v_pk_fma_f16 v69, v69, v98, 0
	v_cvt_scalef32_pk_f16_fp4 v72, v129, 1.0 op_sel:[1,0,0]
	v_cvt_scalef32_pk_f16_fp4 v33, v182, 1.0 op_sel:[1,1,0]
	v_pk_fma_f16 v41, v41, v56, v45
	v_cvt_scalef32_pk_f16_fp4 v45, v178, 1.0 op_sel:[1,0,0]
	v_pk_fma_f16 v20, v61, v92, v20
	v_cvt_scalef32_pk_f16_fp4 v61, v141, 1.0 op_sel:[1,1,0]
	v_pk_fma_f16 v64, v64, v51, v65
	v_cvt_scalef32_pk_f16_fp4 v65, v137, 1.0 op_sel:[0,1,0]
	v_pk_fma_f16 v68, v68, v97, v69
	v_cvt_scalef32_pk_f16_fp4 v69, v133, 1.0 op_sel:[1,0,0]
	v_pk_fma_f16 v72, v72, v98, 0
	v_cvt_scalef32_pk_f16_fp4 v19, v129, 1.0
	v_pk_fma_f16 v33, v33, v91, v37
	v_cvt_scalef32_pk_f16_fp4 v37, v182, 1.0 op_sel:[0,1,0]
	v_pk_fma_f16 v45, v45, v56, v49
	v_cvt_scalef32_pk_f16_fp4 v49, v178, 1.0
	v_cvt_scalef32_pk_f16_fp4 v60, v145, 1.0 op_sel:[1,1,0]
	v_pk_fma_f16 v61, v61, v96, v64
	v_cvt_scalef32_pk_f16_fp4 v64, v141, 1.0 op_sel:[0,1,0]
	v_pk_fma_f16 v65, v65, v51, v68
	v_cvt_scalef32_pk_f16_fp4 v68, v137, 1.0 op_sel:[1,0,0]
	v_pk_fma_f16 v69, v69, v97, v72
	v_cvt_scalef32_pk_f16_fp4 v23, v133, 1.0
	v_pk_fma_f16 v19, v19, v98, 0
	v_cvt_scalef32_pk_f16_fp4 v29, v186, 1.0 op_sel:[1,1,0]
	v_pk_fma_f16 v37, v37, v91, v41
	v_cvt_scalef32_pk_f16_fp4 v41, v182, 1.0 op_sel:[1,0,0]
	v_pk_fma_f16 v20, v49, v56, v20
	v_cvt_scalef32_pk_f16_fp4 v49, v149, 1.0 op_sel:[1,1,0]
	v_pk_fma_f16 v60, v60, v52, v61
	v_cvt_scalef32_pk_f16_fp4 v61, v145, 1.0 op_sel:[0,1,0]
	v_pk_fma_f16 v64, v64, v96, v65
	v_cvt_scalef32_pk_f16_fp4 v65, v141, 1.0 op_sel:[1,0,0]
	v_pk_fma_f16 v68, v68, v51, v69
	v_cvt_scalef32_pk_f16_fp4 v27, v137, 1.0
	v_pk_fma_f16 v19, v23, v97, v19
	v_pk_fma_f16 v29, v29, v57, v33
	v_cvt_scalef32_pk_f16_fp4 v33, v186, 1.0 op_sel:[0,1,0]
	v_pk_fma_f16 v41, v41, v91, v45
	v_cvt_scalef32_pk_f16_fp4 v45, v182, 1.0
	v_cvt_scalef32_pk_f16_fp4 v48, v153, 1.0 op_sel:[1,1,0]
	v_pk_fma_f16 v49, v49, v95, v60
	v_cvt_scalef32_pk_f16_fp4 v60, v149, 1.0 op_sel:[0,1,0]
	v_pk_fma_f16 v61, v61, v52, v64
	v_cvt_scalef32_pk_f16_fp4 v64, v145, 1.0 op_sel:[1,0,0]
	v_pk_fma_f16 v65, v65, v96, v68
	v_cvt_scalef32_pk_f16_fp4 v31, v141, 1.0
	v_pk_fma_f16 v19, v27, v51, v19
	v_pk_fma_f16 v33, v33, v57, v37
	v_cvt_scalef32_pk_f16_fp4 v37, v186, 1.0 op_sel:[1,0,0]
	v_pk_fma_f16 v20, v45, v91, v20
	v_cvt_scalef32_pk_f16_fp4 v45, v157, 1.0 op_sel:[1,1,0]
	v_pk_fma_f16 v48, v48, v53, v49
	v_cvt_scalef32_pk_f16_fp4 v49, v153, 1.0 op_sel:[0,1,0]
	v_pk_fma_f16 v60, v60, v95, v61
	v_cvt_scalef32_pk_f16_fp4 v61, v149, 1.0 op_sel:[1,0,0]
	v_pk_fma_f16 v64, v64, v52, v65
	v_cvt_scalef32_pk_f16_fp4 v35, v145, 1.0
	v_pk_fma_f16 v19, v31, v96, v19
	v_cvt_scalef32_pk_f16_fp4 v25, v190, 1.0 op_sel:[1,1,0]
	v_pk_fma_f16 v37, v37, v57, v41
	v_cvt_scalef32_pk_f16_fp4 v41, v186, 1.0
	v_cvt_scalef32_pk_f16_fp4 v44, v161, 1.0 op_sel:[1,1,0]
	v_pk_fma_f16 v45, v45, v94, v48
	v_cvt_scalef32_pk_f16_fp4 v48, v157, 1.0 op_sel:[0,1,0]
	v_pk_fma_f16 v49, v49, v53, v60
	v_cvt_scalef32_pk_f16_fp4 v60, v153, 1.0 op_sel:[1,0,0]
	v_pk_fma_f16 v61, v61, v95, v64
	v_cvt_scalef32_pk_f16_fp4 v39, v149, 1.0
	v_pk_fma_f16 v19, v35, v52, v19
	v_pk_fma_f16 v25, v25, v90, v29
	v_cvt_scalef32_pk_f16_fp4 v29, v190, 1.0 op_sel:[0,1,0]
	v_pk_fma_f16 v20, v41, v57, v20
	v_cvt_scalef32_pk_f16_fp4 v41, v165, 1.0 op_sel:[1,1,0]
	v_pk_fma_f16 v44, v44, v54, v45
	v_cvt_scalef32_pk_f16_fp4 v45, v161, 1.0 op_sel:[0,1,0]
	v_pk_fma_f16 v48, v48, v94, v49
	v_cvt_scalef32_pk_f16_fp4 v49, v157, 1.0 op_sel:[1,0,0]
	v_pk_fma_f16 v60, v60, v53, v61
	v_cvt_scalef32_pk_f16_fp4 v43, v153, 1.0
	v_pk_fma_f16 v19, v39, v95, v19
	v_pk_fma_f16 v29, v29, v90, v33
	v_cvt_scalef32_pk_f16_fp4 v33, v190, 1.0 op_sel:[1,0,0]
	v_pk_fma_f16 v41, v41, v93, v44
	v_cvt_scalef32_pk_f16_fp4 v44, v165, 1.0 op_sel:[0,1,0]
	v_pk_fma_f16 v45, v45, v54, v48
	v_cvt_scalef32_pk_f16_fp4 v48, v161, 1.0 op_sel:[1,0,0]
	v_pk_fma_f16 v49, v49, v94, v60
	v_cvt_scalef32_pk_f16_fp4 v47, v157, 1.0
	v_pk_fma_f16 v19, v43, v53, v19
	v_pk_fma_f16 v33, v33, v90, v37
	v_cvt_scalef32_pk_f16_fp4 v37, v190, 1.0
	v_cvt_scalef32_pk_f16_fp4 v40, v169, 1.0 op_sel:[1,1,0]
	v_pk_fma_f16 v44, v44, v93, v45
	v_cvt_scalef32_pk_f16_fp4 v45, v165, 1.0 op_sel:[1,0,0]
	v_pk_fma_f16 v48, v48, v54, v49
	v_cvt_scalef32_pk_f16_fp4 v49, v161, 1.0
	v_pk_fma_f16 v19, v47, v94, v19
	v_cvt_scalef32_pk_f16_fp4 v59, v128, 1.0 op_sel:[1,1,0]
	v_pk_fma_f16 v20, v37, v90, v20
	v_cvt_scalef32_pk_f16_fp4 v37, v173, 1.0 op_sel:[1,1,0]
	v_pk_fma_f16 v40, v40, v55, v41
	v_cvt_scalef32_pk_f16_fp4 v41, v169, 1.0 op_sel:[0,1,0]
	v_pk_fma_f16 v45, v45, v93, v48
	v_cvt_scalef32_pk_f16_fp4 v48, v165, 1.0
	v_pk_fma_f16 v19, v49, v54, v19
	v_cvt_scalef32_pk_f16_fp4 v49, v132, 1.0 op_sel:[1,1,0]
	v_pk_fma_f16 v59, v59, v98, 0
	v_pk_fma_f16 v37, v37, v92, v40
	v_cvt_scalef32_pk_f16_fp4 v40, v173, 1.0 op_sel:[0,1,0]
	v_pk_fma_f16 v41, v41, v55, v44
	v_cvt_scalef32_pk_f16_fp4 v44, v169, 1.0 op_sel:[1,0,0]
	v_pk_fma_f16 v19, v48, v93, v19
	v_cvt_scalef32_pk_f16_fp4 v48, v136, 1.0 op_sel:[1,1,0]
	v_pk_fma_f16 v49, v49, v97, v59
	v_cvt_scalef32_pk_f16_fp4 v60, v128, 1.0 op_sel:[0,1,0]
	v_cvt_scalef32_pk_f16_fp4 v36, v177, 1.0 op_sel:[1,1,0]
	v_pk_fma_f16 v40, v40, v92, v41
	v_cvt_scalef32_pk_f16_fp4 v41, v173, 1.0 op_sel:[1,0,0]
	v_pk_fma_f16 v44, v44, v55, v45
	v_cvt_scalef32_pk_f16_fp4 v45, v169, 1.0
	v_cvt_scalef32_pk_f16_fp4 v47, v140, 1.0 op_sel:[1,1,0]
	v_pk_fma_f16 v48, v48, v51, v49
	v_cvt_scalef32_pk_f16_fp4 v59, v132, 1.0 op_sel:[0,1,0]
	v_pk_fma_f16 v60, v60, v98, 0
	v_cvt_scalef32_pk_f16_fp4 v61, v128, 1.0 op_sel:[1,0,0]
	v_cvt_scalef32_pk_f16_fp4 v32, v181, 1.0 op_sel:[1,1,0]
	v_pk_fma_f16 v36, v36, v56, v37
	v_cvt_scalef32_pk_f16_fp4 v37, v177, 1.0 op_sel:[0,1,0]
	v_pk_fma_f16 v41, v41, v92, v44
	v_cvt_scalef32_pk_f16_fp4 v44, v173, 1.0
	v_pk_fma_f16 v19, v45, v55, v19
	v_cvt_scalef32_pk_f16_fp4 v45, v144, 1.0 op_sel:[1,1,0]
	v_pk_fma_f16 v47, v47, v96, v48
	v_cvt_scalef32_pk_f16_fp4 v49, v136, 1.0 op_sel:[0,1,0]
	v_pk_fma_f16 v59, v59, v97, v60
	v_cvt_scalef32_pk_f16_fp4 v60, v132, 1.0 op_sel:[1,0,0]
	v_pk_fma_f16 v61, v61, v98, 0
	v_cvt_scalef32_pk_f16_fp4 v18, v128, 1.0
	v_cvt_scalef32_pk_f16_fp4 v28, v185, 1.0 op_sel:[1,1,0]
	v_pk_fma_f16 v32, v32, v91, v36
	v_cvt_scalef32_pk_f16_fp4 v36, v181, 1.0 op_sel:[0,1,0]
	v_pk_fma_f16 v37, v37, v56, v40
	v_cvt_scalef32_pk_f16_fp4 v40, v177, 1.0 op_sel:[1,0,0]
	v_pk_fma_f16 v19, v44, v92, v19
	v_cvt_scalef32_pk_f16_fp4 v44, v148, 1.0 op_sel:[1,1,0]
	v_pk_fma_f16 v45, v45, v52, v47
	v_cvt_scalef32_pk_f16_fp4 v48, v140, 1.0 op_sel:[0,1,0]
	v_pk_fma_f16 v49, v49, v51, v59
	v_cvt_scalef32_pk_f16_fp4 v59, v136, 1.0 op_sel:[1,0,0]
	v_pk_fma_f16 v60, v60, v97, v61
	v_cvt_scalef32_pk_f16_fp4 v22, v132, 1.0
	v_pk_fma_f16 v18, v18, v98, 0
	v_cvt_scalef32_pk_f16_fp4 v24, v189, 1.0 op_sel:[1,1,0]
	v_pk_fma_f16 v28, v28, v57, v32
	v_pk_fma_f16 v36, v36, v91, v37
	v_cvt_scalef32_pk_f16_fp4 v37, v181, 1.0 op_sel:[1,0,0]
	v_pk_fma_f16 v40, v40, v56, v41
	v_cvt_scalef32_pk_f16_fp4 v41, v177, 1.0
	v_cvt_scalef32_pk_f16_fp4 v43, v152, 1.0 op_sel:[1,1,0]
	v_pk_fma_f16 v44, v44, v95, v45
	v_cvt_scalef32_pk_f16_fp4 v47, v144, 1.0 op_sel:[0,1,0]
	v_pk_fma_f16 v48, v48, v96, v49
	v_cvt_scalef32_pk_f16_fp4 v49, v140, 1.0 op_sel:[1,0,0]
	v_pk_fma_f16 v59, v59, v51, v60
	v_cvt_scalef32_pk_f16_fp4 v26, v136, 1.0
	v_pk_fma_f16 v18, v22, v97, v18
	v_pk_fma_f16 v32, v24, v90, v28
	v_cvt_scalef32_pk_f16_fp4 v28, v185, 1.0 op_sel:[0,1,0]
	v_pk_fma_f16 v37, v37, v91, v40
	v_cvt_scalef32_pk_f16_fp4 v40, v181, 1.0
	v_pk_fma_f16 v19, v41, v56, v19
	v_cvt_scalef32_pk_f16_fp4 v41, v156, 1.0 op_sel:[1,1,0]
	v_pk_fma_f16 v43, v43, v53, v44
	v_cvt_scalef32_pk_f16_fp4 v45, v148, 1.0 op_sel:[0,1,0]
	v_pk_fma_f16 v47, v47, v52, v48
	v_cvt_scalef32_pk_f16_fp4 v48, v144, 1.0 op_sel:[1,0,0]
	v_pk_fma_f16 v49, v49, v96, v59
	v_cvt_scalef32_pk_f16_fp4 v30, v140, 1.0
	v_pk_fma_f16 v18, v26, v51, v18
	v_cvt_scalef32_pk_f16_fp4 v24, v189, 1.0 op_sel:[0,1,0]
	v_pk_fma_f16 v28, v28, v57, v36
	v_cvt_scalef32_pk_f16_fp4 v36, v185, 1.0 op_sel:[1,0,0]
	v_pk_fma_f16 v19, v40, v91, v19
	v_cvt_scalef32_pk_f16_fp4 v40, v160, 1.0 op_sel:[1,1,0]
	v_pk_fma_f16 v41, v41, v94, v43
	v_cvt_scalef32_pk_f16_fp4 v44, v152, 1.0 op_sel:[0,1,0]
	v_pk_fma_f16 v45, v45, v95, v47
	v_cvt_scalef32_pk_f16_fp4 v47, v148, 1.0 op_sel:[1,0,0]
	v_pk_fma_f16 v48, v48, v52, v49
	v_cvt_scalef32_pk_f16_fp4 v34, v144, 1.0
	v_pk_fma_f16 v18, v30, v96, v18
	v_pk_fma_f16 v24, v24, v90, v28
	v_cvt_scalef32_pk_f16_fp4 v28, v189, 1.0 op_sel:[1,0,0]
	v_pk_fma_f16 v36, v36, v57, v37
	v_cvt_scalef32_pk_f16_fp4 v37, v185, 1.0
	v_cvt_scalef32_pk_f16_fp4 v39, v164, 1.0 op_sel:[1,1,0]
	v_pk_fma_f16 v40, v40, v54, v41
	v_cvt_scalef32_pk_f16_fp4 v43, v156, 1.0 op_sel:[0,1,0]
	v_pk_fma_f16 v44, v44, v53, v45
	v_cvt_scalef32_pk_f16_fp4 v45, v152, 1.0 op_sel:[1,0,0]
	v_pk_fma_f16 v47, v47, v95, v48
	v_cvt_scalef32_pk_f16_fp4 v38, v148, 1.0
	v_pk_fma_f16 v18, v34, v52, v18
	v_pk_fma_f16 v28, v28, v90, v36
	v_cvt_scalef32_pk_f16_fp4 v36, v189, 1.0
	v_pk_fma_f16 v19, v37, v57, v19
	v_cvt_scalef32_pk_f16_fp4 v37, v168, 1.0 op_sel:[1,1,0]
	v_pk_fma_f16 v39, v39, v93, v40
	v_cvt_scalef32_pk_f16_fp4 v41, v160, 1.0 op_sel:[0,1,0]
	v_pk_fma_f16 v43, v43, v94, v44
	v_cvt_scalef32_pk_f16_fp4 v44, v156, 1.0 op_sel:[1,0,0]
	v_pk_fma_f16 v45, v45, v53, v47
	v_cvt_scalef32_pk_f16_fp4 v42, v152, 1.0
	v_pk_fma_f16 v18, v38, v95, v18
	v_pk_fma_f16 v35, v36, v90, v19
	v_cvt_scalef32_pk_f16_fp4 v36, v172, 1.0 op_sel:[1,1,0]
	v_pk_fma_f16 v37, v37, v55, v39
	v_cvt_scalef32_pk_f16_fp4 v40, v164, 1.0 op_sel:[0,1,0]
	v_pk_fma_f16 v41, v41, v54, v43
	v_cvt_scalef32_pk_f16_fp4 v43, v160, 1.0 op_sel:[1,0,0]
	v_pk_fma_f16 v44, v44, v94, v45
	v_cvt_scalef32_pk_f16_fp4 v45, v156, 1.0
	v_pk_fma_f16 v18, v42, v53, v18
	v_cvt_scalef32_pk_f16_fp4 v31, v176, 1.0 op_sel:[1,1,0]
	v_pk_fma_f16 v36, v36, v92, v37
	v_cvt_scalef32_pk_f16_fp4 v39, v168, 1.0 op_sel:[0,1,0]
	v_pk_fma_f16 v40, v40, v93, v41
	v_cvt_scalef32_pk_f16_fp4 v41, v164, 1.0 op_sel:[1,0,0]
	v_pk_fma_f16 v43, v43, v54, v44
	v_cvt_scalef32_pk_f16_fp4 v44, v160, 1.0
	v_pk_fma_f16 v18, v45, v94, v18
	v_cvt_scalef32_pk_f16_fp4 v27, v180, 1.0 op_sel:[1,1,0]
	v_pk_fma_f16 v31, v31, v56, v36
	v_cvt_scalef32_pk_f16_fp4 v37, v172, 1.0 op_sel:[0,1,0]
	v_pk_fma_f16 v39, v39, v55, v40
	v_cvt_scalef32_pk_f16_fp4 v40, v168, 1.0 op_sel:[1,0,0]
	v_pk_fma_f16 v41, v41, v93, v43
	v_cvt_scalef32_pk_f16_fp4 v43, v164, 1.0
	v_pk_fma_f16 v18, v44, v54, v18
	v_cvt_scalef32_pk_f16_fp4 v23, v184, 1.0 op_sel:[1,1,0]
	v_pk_fma_f16 v27, v27, v91, v31
	v_cvt_scalef32_pk_f16_fp4 v36, v176, 1.0 op_sel:[0,1,0]
	v_pk_fma_f16 v37, v37, v92, v39
	v_cvt_scalef32_pk_f16_fp4 v39, v172, 1.0 op_sel:[1,0,0]
	v_pk_fma_f16 v40, v40, v55, v41
	v_cvt_scalef32_pk_f16_fp4 v41, v168, 1.0
	v_pk_fma_f16 v18, v43, v93, v18
	v_cvt_scalef32_pk_f16_fp4 v19, v188, 1.0 op_sel:[1,1,0]
	v_pk_fma_f16 v23, v23, v57, v27
	v_cvt_scalef32_pk_f16_fp4 v27, v180, 1.0 op_sel:[0,1,0]
	v_pk_fma_f16 v36, v36, v56, v37
	v_cvt_scalef32_pk_f16_fp4 v37, v176, 1.0 op_sel:[1,0,0]
	v_pk_fma_f16 v39, v39, v92, v40
	v_cvt_scalef32_pk_f16_fp4 v40, v172, 1.0
	v_pk_fma_f16 v18, v41, v55, v18
	v_pk_fma_f16 v31, v19, v90, v23
	v_cvt_scalef32_pk_f16_fp4 v23, v184, 1.0 op_sel:[0,1,0]
	v_pk_fma_f16 v27, v27, v91, v36
	v_cvt_scalef32_pk_f16_fp4 v36, v180, 1.0 op_sel:[1,0,0]
	v_pk_fma_f16 v37, v37, v56, v39
	v_cvt_scalef32_pk_f16_fp4 v39, v176, 1.0
	v_pk_fma_f16 v18, v40, v92, v18
	v_cvt_scalef32_pk_f16_fp4 v19, v188, 1.0 op_sel:[0,1,0]
	v_pk_fma_f16 v23, v23, v57, v27
	v_cvt_scalef32_pk_f16_fp4 v27, v184, 1.0 op_sel:[1,0,0]
	v_pk_fma_f16 v36, v36, v91, v37
	v_cvt_scalef32_pk_f16_fp4 v37, v180, 1.0
	v_pk_fma_f16 v18, v39, v56, v18
	v_pk_fma_f16 v23, v19, v90, v23
	v_cvt_scalef32_pk_f16_fp4 v19, v188, 1.0 op_sel:[1,0,0]
	v_pk_fma_f16 v27, v27, v57, v36
	v_cvt_scalef32_pk_f16_fp4 v36, v184, 1.0
	v_pk_fma_f16 v18, v37, v91, v18
	v_pk_fma_f16 v27, v19, v90, v27
	v_cvt_scalef32_pk_f16_fp4 v19, v188, 1.0
	v_pk_fma_f16 v18, v36, v57, v18
	v_permlane32_swap_b32_e32 v27, v33
	v_pk_fma_f16 v18, v19, v90, v18
	v_permlane32_swap_b32_e32 v23, v29
	s_nop 0
	v_permlane32_swap_b32_e32 v18, v20
	v_pk_add_f16 v19, v18, v20
	v_pk_add_f16 v20, v27, v33
	v_permlane32_swap_b32_e32 v31, v25
	v_cvt_f32_f16_e32 v26, v20
	v_cvt_f32_f16_sdwa v27, v20 dst_sel:DWORD dst_unused:UNUSED_PAD src0_sel:WORD_1
	v_pk_add_f16 v20, v23, v29
	v_permlane32_swap_b32_e32 v28, v100
	v_cvt_f32_f16_e32 v22, v20
	v_cvt_f32_f16_sdwa v23, v20 dst_sel:DWORD dst_unused:UNUSED_PAD src0_sel:WORD_1
	v_pk_add_f16 v20, v31, v25
	v_permlane32_swap_b32_e32 v35, v21
	v_pk_add_f16 v25, v28, v100
	v_permlane32_swap_b32_e32 v24, v99
	v_permlane32_swap_b32_e32 v32, v50
	v_pk_add_f16 v21, v35, v21
	v_cvt_f32_f16_e32 v28, v25
	v_cvt_f32_f16_sdwa v29, v25 dst_sel:DWORD dst_unused:UNUSED_PAD src0_sel:WORD_1
	v_pk_add_f16 v25, v24, v99
	v_pk_add_f16 v33, v32, v50
	v_cvt_f32_f16_e32 v18, v19
	v_cvt_f32_f16_sdwa v19, v19 dst_sel:DWORD dst_unused:UNUSED_PAD src0_sel:WORD_1
	v_cvt_f32_f16_e32 v30, v20
	v_cvt_f32_f16_sdwa v31, v20 dst_sel:DWORD dst_unused:UNUSED_PAD src0_sel:WORD_1
	v_cvt_f32_f16_e32 v20, v21
	v_cvt_f32_f16_sdwa v21, v21 dst_sel:DWORD dst_unused:UNUSED_PAD src0_sel:WORD_1
	v_cvt_f32_f16_e32 v24, v25
	v_cvt_f32_f16_sdwa v25, v25 dst_sel:DWORD dst_unused:UNUSED_PAD src0_sel:WORD_1
	v_cvt_f32_f16_e32 v32, v33
	v_cvt_f32_f16_sdwa v33, v33 dst_sel:DWORD dst_unused:UNUSED_PAD src0_sel:WORD_1
	v_mul_hi_i32 v34, v110, s69
	v_lshrrev_b32_e32 v35, 31, v34
	v_ashrrev_i32_e32 v34, 13, v34
	v_add_u32_e32 v35, v34, v35
	v_permlane16_swap_b32_e32 v18, v20
	v_permlane16_swap_b32_e32 v19, v21
	v_permlane16_swap_b32_e32 v26, v28
	v_permlane16_swap_b32_e32 v27, v29
	v_permlane16_swap_b32_e32 v22, v24
	v_permlane16_swap_b32_e32 v23, v25
	v_permlane16_swap_b32_e32 v30, v32
	v_permlane16_swap_b32_e32 v31, v33
	v_mad_i32_i24 v34, v35, s20, v112
	v_pk_add_f32 v[20:21], v[18:19], v[20:21]
	v_pk_add_f32 v[18:19], v[22:23], v[24:25]
	v_pk_add_f32 v[28:29], v[26:27], v[28:29]
	v_pk_add_f32 v[26:27], v[30:31], v[32:33]
	v_add3_u32 v34, v34, s33, 1
	v_mov_b32_dpp v24, v20 row_ror:8 row_mask:0xf bank_mask:0xf bound_ctrl:1
	v_mov_b32_dpp v22, v18 row_ror:8 row_mask:0xf bank_mask:0xf bound_ctrl:1
	v_mov_b32_dpp v25, v21 row_ror:8 row_mask:0xf bank_mask:0xf bound_ctrl:1
	v_mov_b32_dpp v23, v19 row_ror:8 row_mask:0xf bank_mask:0xf bound_ctrl:1
	v_mov_b32_dpp v32, v28 row_ror:8 row_mask:0xf bank_mask:0xf bound_ctrl:1
	v_mov_b32_dpp v30, v26 row_ror:8 row_mask:0xf bank_mask:0xf bound_ctrl:1
	v_mov_b32_dpp v33, v29 row_ror:8 row_mask:0xf bank_mask:0xf bound_ctrl:1
	v_mov_b32_dpp v31, v27 row_ror:8 row_mask:0xf bank_mask:0xf bound_ctrl:1
	v_cmp_lt_i32_e64 s[0:1], s21, v34
	s_and_saveexec_b64 s[2:3], s[0:1]
	s_xor_b64 s[0:1], exec, s[2:3]
	s_movk_i32 s2, 0xff01
	s_or_saveexec_b64 s[0:1], s[0:1]
	s_xor_b64 exec, exec, s[0:1]
	s_cbranch_execz .LBB0_888
	s_branch .LBB0_888
